# GLU epilogue loads kept in flight; final phase: slot indices fetched one iteration ahead
# speedup vs baseline: 1.0111x; 1.0088x over previous
; __device__ __forceinline__ float sigmoidf_(float x) { return 1.f / (1.f + __expf(-x)); }
; __device__ __forceinline__ unsigned cvt_pk_bf16(float lo, float hi) { const f32x2c v = {lo, hi}; const bf16x2c b = __builtin_convertvector(v, bf16x2c); return __builtin_bit_cast(unsigned, b); }
;     __device__ __forceinline__ void operator()(const f32x4 (&acc)[2][2][4][2], const Unit& u, int wr, int wc, int fr, int fq) const {
;     ...
;             for (int m = 0; m < 4; ++m) { const size_t row = (size_t)(row0 + ai * HALF + m * 16);
; #pragma unroll
;                 for (int bj = 0; bj < 2; ++bj) { const int col = col0 + bj * HALF;
;                     const u32x4 zz = *(const u32x4*)(Z + row * 512 + col);
;                     const f32x4 b0 = *(const f32x4*)(bias + col), b1 = *(const f32x4*)(bias + col + 4);
;                     const f32x4 v0 = acc[ai][bj][m][0] + b0, v1 = acc[ai][bj][m][1] + b1;
;                     float o[8]; const unsigned zw[4] = {zz.x, zz.y, zz.z, zz.w};
; #pragma unroll
;                     for (int q = 0; q < 4; ++q) { const float zl = __builtin_bit_cast(float, zw[q] << 16), zh = __builtin_bit_cast(float, zw[q] & 0xffff0000u);
;                         const float al = (q < 2) ? v0[2 * q] : v1[2 * q - 4], ah = (q < 2) ? v0[2 * q + 1] : v1[2 * q - 3];
;                         o[2 * q] = zl * sigmoidf_(al); o[2 * q + 1] = zh * sigmoidf_(ah); }
;                     u32x4 w; w.x = cvt_pk_bf16(o[0], o[1]); w.y = cvt_pk_bf16(o[2], o[3]); w.z = cvt_pk_bf16(o[4], o[5]); w.w = cvt_pk_bf16(o[6], o[7]);
;                     *(u32x4*)(YM + row * D + 512 + col) = w; } }
.LBB0_2021:
	v_lshl_add_u32 v144, s14, 8, v150
	v_lshl_or_b32 v140, s15, 8, v152
	v_ashrrev_i32_e32 v145, 31, v144
	v_lshlrev_b64 v[142:143], 10, v[144:145]
	v_ashrrev_i32_e32 v141, 31, v140
	v_readlane_b32 s0, v243, 26
	v_lshl_add_u64 v[148:149], s[36:37], 0, v[142:143]
	v_lshlrev_b64 v[142:143], 1, v[140:141]
	v_readlane_b32 s1, v243, 27
	v_lshl_add_u64 v[148:149], v[148:149], 0, v[142:143]
	v_lshl_add_u64 v[140:141], v[140:141], 2, s[0:1]
	v_mov_b32_e32 v166, v148
	v_mov_b32_e32 v167, v149
	global_load_dwordx4 v[170:173], v[140:141], off
	global_load_dwordx4 v[174:177], v[140:141], off offset:16
	global_load_dwordx4 v[178:181], v[140:141], off offset:512
	global_load_dwordx4 v[182:185], v[140:141], off offset:528
	global_load_dwordx4 v[186:189], v[166:167], off
	global_load_dwordx4 v[190:193], v[166:167], off offset:256
	s_mov_b64 s[98:99], 0x4000
	v_lshl_add_u64 v[168:169], v[166:167], 0, s[98:99]
	global_load_dwordx4 v[198:201], v[168:169], off
	global_load_dwordx4 v[202:205], v[168:169], off offset:256
	s_mov_b64 s[98:99], 0x8000
	v_lshl_add_u64 v[168:169], v[166:167], 0, s[98:99]
	global_load_dwordx4 v[206:209], v[168:169], off
	global_load_dwordx4 v[210:213], v[168:169], off offset:256
	v_readlane_b32 s14, v243, 40
	v_readlane_b32 s15, v243, 41
	v_lshlrev_b64 v[146:147], 11, v[144:145]
	v_readlane_b32 s2, v243, 28
	v_readlane_b32 s3, v243, 29
	v_readlane_b32 s4, v243, 30
	v_readlane_b32 s5, v243, 31
	v_readlane_b32 s6, v243, 32
	v_readlane_b32 s7, v243, 33
	v_readlane_b32 s8, v243, 34
	v_readlane_b32 s9, v243, 35
	v_readlane_b32 s10, v243, 36
	v_readlane_b32 s11, v243, 37
	v_readlane_b32 s12, v243, 38
	v_readlane_b32 s13, v243, 39
	s_waitcnt vmcnt(5)
	v_mov_b32_e32 v154, v186
	v_mov_b32_e32 v155, v187
	v_mov_b32_e32 v156, v188
	v_mov_b32_e32 v157, v189
	v_mov_b32_e32 v158, v174
	v_mov_b32_e32 v159, v175
	v_mov_b32_e32 v160, v176
	v_mov_b32_e32 v161, v177
	v_mov_b32_e32 v162, v170
	v_mov_b32_e32 v163, v171
	v_mov_b32_e32 v164, v172
	v_mov_b32_e32 v165, v173
	s_mov_b64 s[98:99], 0xc000
	v_lshl_add_u64 v[168:169], v[166:167], 0, s[98:99]
	global_load_dwordx4 v[186:189], v[168:169], off
	v_pk_add_f32 v[120:121], v[120:121], v[158:159]
	v_pk_add_f32 v[124:125], v[124:125], v[162:163]
	v_lshlrev_b32_e32 v158, 16, v154
	v_mul_f32_e32 v124, 0xbfb8aa3b, v124
	v_mul_f32_e32 v125, 0xbfb8aa3b, v125
	v_exp_f32_e32 v124, v124
	v_exp_f32_e32 v125, v125
	v_and_b32_e32 v159, 0xffff0000, v154
	v_pk_add_f32 v[122:123], v[122:123], v[160:161]
	v_pk_add_f32 v[126:127], v[126:127], v[164:165]
	v_pk_add_f32 v[124:125], v[124:125], 1.0 op_sel_hi:[1,0]
	v_mul_f32_e32 v126, 0xbfb8aa3b, v126
	v_div_scale_f32 v145, s[14:15], v125, v125, 1.0
	v_rcp_f32_e32 v154, v145
	v_mul_f32_e32 v127, 0xbfb8aa3b, v127
	v_exp_f32_e32 v126, v126
	v_exp_f32_e32 v127, v127
	v_fma_f32 v160, -v145, v154, 1.0
	v_fmac_f32_e32 v154, v160, v154
	v_div_scale_f32 v160, vcc, 1.0, v125, 1.0
	v_mul_f32_e32 v161, v160, v154
	v_fma_f32 v162, -v145, v161, v160
	v_fmac_f32_e32 v161, v162, v154
	v_fma_f32 v145, -v145, v161, v160
	v_div_fmas_f32 v145, v145, v154, v161
	v_div_fixup_f32 v125, v145, v125, 1.0
	v_div_scale_f32 v145, s[14:15], v124, v124, 1.0
	v_rcp_f32_e32 v154, v145
	v_pk_add_f32 v[126:127], v[126:127], 1.0 op_sel_hi:[1,0]
	v_mul_f32_e32 v120, 0xbfb8aa3b, v120
	v_mul_f32_e32 v121, 0xbfb8aa3b, v121
	v_fma_f32 v160, -v145, v154, 1.0
	v_fmac_f32_e32 v154, v160, v154
	v_div_scale_f32 v160, vcc, 1.0, v124, 1.0
	v_mul_f32_e32 v161, v160, v154
	v_fma_f32 v162, -v145, v161, v160
	v_fmac_f32_e32 v161, v162, v154
	v_fma_f32 v145, -v145, v161, v160
	v_div_fmas_f32 v145, v145, v154, v161
	v_div_fixup_f32 v124, v145, v124, 1.0
	v_div_scale_f32 v145, s[14:15], v127, v127, 1.0
	v_pk_mul_f32 v[124:125], v[124:125], v[158:159]
	v_rcp_f32_e32 v158, v145
	v_exp_f32_e32 v120, v120
	v_exp_f32_e32 v121, v121
	v_lshlrev_b32_e32 v154, 16, v155
	v_fma_f32 v159, -v145, v158, 1.0
	v_fmac_f32_e32 v158, v159, v158
	v_div_scale_f32 v159, vcc, 1.0, v127, 1.0
	v_mul_f32_e32 v160, v159, v158
	v_fma_f32 v161, -v145, v160, v159
	v_fmac_f32_e32 v160, v161, v158
	v_fma_f32 v145, -v145, v160, v159
	v_div_fmas_f32 v145, v145, v158, v160
	v_div_fixup_f32 v127, v145, v127, 1.0
	v_div_scale_f32 v145, s[14:15], v126, v126, 1.0
	v_rcp_f32_e32 v158, v145
	v_pk_add_f32 v[120:121], v[120:121], 1.0 op_sel_hi:[1,0]
	v_and_b32_e32 v155, 0xffff0000, v155
	v_fma_f32 v159, -v145, v158, 1.0
	v_fmac_f32_e32 v158, v159, v158
	v_div_scale_f32 v159, vcc, 1.0, v126, 1.0
	v_mul_f32_e32 v160, v159, v158
	v_fma_f32 v161, -v145, v160, v159
	v_fmac_f32_e32 v160, v161, v158
	v_fma_f32 v145, -v145, v160, v159
	v_div_fmas_f32 v145, v145, v158, v160
	v_div_fixup_f32 v126, v145, v126, 1.0
	v_div_scale_f32 v145, s[14:15], v121, v121, 1.0
	v_pk_mul_f32 v[126:127], v[126:127], v[154:155]
	v_lshlrev_b32_e32 v154, 16, v156
	v_and_b32_e32 v155, 0xffff0000, v156
	v_rcp_f32_e32 v156, v145
	s_nop 0
	v_fma_f32 v158, -v145, v156, 1.0
	v_fmac_f32_e32 v156, v158, v156
	v_div_scale_f32 v158, vcc, 1.0, v121, 1.0
	v_mul_f32_e32 v159, v158, v156
	v_fma_f32 v160, -v145, v159, v158
	v_fmac_f32_e32 v159, v160, v156
	v_fma_f32 v145, -v145, v159, v158
	v_div_fmas_f32 v145, v145, v156, v159
	v_div_fixup_f32 v121, v145, v121, 1.0
	v_div_scale_f32 v145, s[14:15], v120, v120, 1.0
	v_rcp_f32_e32 v156, v145
	s_nop 0
	v_fma_f32 v158, -v145, v156, 1.0
	v_fmac_f32_e32 v156, v158, v156
	v_div_scale_f32 v158, vcc, 1.0, v120, 1.0
	v_mul_f32_e32 v159, v158, v156
	v_fma_f32 v160, -v145, v159, v158
	v_fmac_f32_e32 v159, v160, v156
	v_fma_f32 v145, -v145, v159, v158
	v_div_fmas_f32 v145, v145, v156, v159
	v_div_fixup_f32 v120, v145, v120, 1.0
	v_pk_mul_f32 v[154:155], v[120:121], v[154:155]
; __device__ __forceinline__ float sigmoidf_(float x) { return 1.f / (1.f + __expf(-x)); }
; __device__ __forceinline__ unsigned cvt_pk_bf16(float lo, float hi) { const f32x2c v = {lo, hi}; const bf16x2c b = __builtin_convertvector(v, bf16x2c); return __builtin_bit_cast(unsigned, b); }
;     __device__ __forceinline__ void operator()(const f32x4 (&acc)[2][2][4][2], const Unit& u, int wr, int wc, int fr, int fq) const {
;     ...
;             for (int m = 0; m < 4; ++m) { const size_t row = (size_t)(row0 + ai * HALF + m * 16);
; #pragma unroll
;                 for (int bj = 0; bj < 2; ++bj) { const int col = col0 + bj * HALF;
;                     const u32x4 zz = *(const u32x4*)(Z + row * 512 + col);
;                     const f32x4 b0 = *(const f32x4*)(bias + col), b1 = *(const f32x4*)(bias + col + 4);
;                     const f32x4 v0 = acc[ai][bj][m][0] + b0, v1 = acc[ai][bj][m][1] + b1;
;                     float o[8]; const unsigned zw[4] = {zz.x, zz.y, zz.z, zz.w};
; #pragma unroll
;                     for (int q = 0; q < 4; ++q) { const float zl = __builtin_bit_cast(float, zw[q] << 16), zh = __builtin_bit_cast(float, zw[q] & 0xffff0000u);
;                         const float al = (q < 2) ? v0[2 * q] : v1[2 * q - 4], ah = (q < 2) ? v0[2 * q + 1] : v1[2 * q - 3];
;                         o[2 * q] = zl * sigmoidf_(al); o[2 * q + 1] = zh * sigmoidf_(ah); }
;                     u32x4 w; w.x = cvt_pk_bf16(o[0], o[1]); w.y = cvt_pk_bf16(o[2], o[3]); w.z = cvt_pk_bf16(o[4], o[5]); w.w = cvt_pk_bf16(o[6], o[7]);
;                     *(u32x4*)(YM + row * D + 512 + col) = w; } }
	v_mul_f32_e32 v120, 0xbfb8aa3b, v122
	v_mul_f32_e32 v121, 0xbfb8aa3b, v123
	v_exp_f32_e32 v120, v120
	v_exp_f32_e32 v121, v121
	v_lshlrev_b32_e32 v122, 16, v157
	v_and_b32_e32 v123, 0xffff0000, v157
	v_pk_add_f32 v[120:121], v[120:121], 1.0 op_sel_hi:[1,0]
	s_nop 0
	v_div_scale_f32 v145, s[14:15], v121, v121, 1.0
	v_rcp_f32_e32 v156, v145
	s_nop 0
	v_fma_f32 v157, -v145, v156, 1.0
	v_fmac_f32_e32 v156, v157, v156
	v_div_scale_f32 v157, vcc, 1.0, v121, 1.0
	v_mul_f32_e32 v158, v157, v156
	v_fma_f32 v159, -v145, v158, v157
	v_fmac_f32_e32 v158, v159, v156
	v_fma_f32 v145, -v145, v158, v157
	v_div_fmas_f32 v145, v145, v156, v158
	v_div_fixup_f32 v121, v145, v121, 1.0
	v_div_scale_f32 v145, s[14:15], v120, v120, 1.0
	v_rcp_f32_e32 v156, v145
	s_nop 0
	v_fma_f32 v157, -v145, v156, 1.0
	v_fmac_f32_e32 v156, v157, v156
	v_div_scale_f32 v157, vcc, 1.0, v120, 1.0
	v_mul_f32_e32 v158, v157, v156
	v_fma_f32 v159, -v145, v158, v157
	v_fmac_f32_e32 v158, v159, v156
	v_fma_f32 v145, -v145, v158, v157
	v_div_fmas_f32 v145, v145, v156, v158
	v_div_fixup_f32 v120, v145, v120, 1.0
	v_pk_mul_f32 v[156:157], v[120:121], v[122:123]
	v_cvt_pk_bf16_f32 v120, v124, v125
	v_lshl_add_u64 v[124:125], s[26:27], 0, v[146:147]
	v_cvt_pk_bf16_f32 v121, v126, v127
	v_cvt_pk_bf16_f32 v122, v154, v155
	v_cvt_pk_bf16_f32 v123, v156, v157
	v_lshl_add_u64 v[146:147], v[124:125], 0, v[142:143]
	global_store_dwordx4 v[146:147], v[120:123], off offset:1024
	s_nop 1
	s_nop 0
	s_waitcnt vmcnt(6)
	v_mov_b32_e32 v120, v190
	v_mov_b32_e32 v121, v191
	v_mov_b32_e32 v122, v192
	v_mov_b32_e32 v123, v193
	v_mov_b32_e32 v124, v182
	v_mov_b32_e32 v125, v183
	v_mov_b32_e32 v126, v184
	v_mov_b32_e32 v127, v185
	v_mov_b32_e32 v154, v178
	v_mov_b32_e32 v155, v179
	v_mov_b32_e32 v156, v180
	v_mov_b32_e32 v157, v181
	global_load_dwordx4 v[190:193], v[168:169], off offset:256
	v_pk_add_f32 v[114:115], v[114:115], v[126:127]
	v_pk_add_f32 v[148:149], v[116:117], v[154:155]
	v_pk_add_f32 v[116:117], v[112:113], v[124:125]
	v_mul_f32_e32 v112, 0xbfb8aa3b, v148
	v_mul_f32_e32 v113, 0xbfb8aa3b, v149
	v_exp_f32_e32 v112, v112
	v_exp_f32_e32 v113, v113
	v_lshlrev_b32_e32 v124, 16, v120
	v_and_b32_e32 v125, 0xffff0000, v120
	v_pk_add_f32 v[118:119], v[118:119], v[156:157]
	v_pk_add_f32 v[112:113], v[112:113], 1.0 op_sel_hi:[1,0]
	v_mul_f32_e32 v118, 0xbfb8aa3b, v118
	v_div_scale_f32 v120, s[14:15], v113, v113, 1.0
	v_rcp_f32_e32 v126, v120
	v_mul_f32_e32 v119, 0xbfb8aa3b, v119
	v_exp_f32_e32 v118, v118
	v_exp_f32_e32 v119, v119
	v_fma_f32 v127, -v120, v126, 1.0
	v_fmac_f32_e32 v126, v127, v126
	v_div_scale_f32 v127, vcc, 1.0, v113, 1.0
	v_mul_f32_e32 v145, v127, v126
	v_fma_f32 v148, -v120, v145, v127
	v_fmac_f32_e32 v145, v148, v126
	v_fma_f32 v120, -v120, v145, v127
	v_div_fmas_f32 v120, v120, v126, v145
	v_div_fixup_f32 v113, v120, v113, 1.0
	v_div_scale_f32 v120, s[14:15], v112, v112, 1.0
	v_rcp_f32_e32 v126, v120
	v_pk_add_f32 v[118:119], v[118:119], 1.0 op_sel_hi:[1,0]
	v_mul_f32_e32 v116, 0xbfb8aa3b, v116
	v_mul_f32_e32 v117, 0xbfb8aa3b, v117
	v_fma_f32 v127, -v120, v126, 1.0
	v_fmac_f32_e32 v126, v127, v126
	v_div_scale_f32 v127, vcc, 1.0, v112, 1.0
	v_mul_f32_e32 v145, v127, v126
	v_fma_f32 v148, -v120, v145, v127
	v_fmac_f32_e32 v145, v148, v126
	v_fma_f32 v120, -v120, v145, v127
	v_div_fmas_f32 v120, v120, v126, v145
	v_div_fixup_f32 v112, v120, v112, 1.0
	v_pk_mul_f32 v[112:113], v[112:113], v[124:125]
	v_div_scale_f32 v124, s[14:15], v119, v119, 1.0
	v_rcp_f32_e32 v125, v124
	v_exp_f32_e32 v116, v116
	v_exp_f32_e32 v117, v117
	v_lshlrev_b32_e32 v120, 16, v121
	v_fma_f32 v126, -v124, v125, 1.0
	v_fmac_f32_e32 v125, v126, v125
	v_div_scale_f32 v126, vcc, 1.0, v119, 1.0
	v_mul_f32_e32 v127, v126, v125
	v_fma_f32 v145, -v124, v127, v126
	v_fmac_f32_e32 v127, v145, v125
	v_fma_f32 v124, -v124, v127, v126
	v_div_fmas_f32 v124, v124, v125, v127
	v_div_fixup_f32 v119, v124, v119, 1.0
	v_div_scale_f32 v124, s[14:15], v118, v118, 1.0
	v_rcp_f32_e32 v125, v124
	v_and_b32_e32 v121, 0xffff0000, v121
	v_pk_add_f32 v[116:117], v[116:117], 1.0 op_sel_hi:[1,0]
	v_mul_f32_e32 v114, 0xbfb8aa3b, v114
	v_fma_f32 v126, -v124, v125, 1.0
	v_fmac_f32_e32 v125, v126, v125
	v_div_scale_f32 v126, vcc, 1.0, v118, 1.0
	v_mul_f32_e32 v127, v126, v125
	v_fma_f32 v145, -v124, v127, v126
	v_fmac_f32_e32 v127, v145, v125
	v_fma_f32 v124, -v124, v127, v126
	v_div_fmas_f32 v124, v124, v125, v127
	v_div_fixup_f32 v118, v124, v118, 1.0
	v_pk_mul_f32 v[118:119], v[118:119], v[120:121]
	v_lshlrev_b32_e32 v120, 16, v122
	v_and_b32_e32 v121, 0xffff0000, v122
	v_div_scale_f32 v122, s[14:15], v117, v117, 1.0
	v_rcp_f32_e32 v124, v122
	v_mul_f32_e32 v115, 0xbfb8aa3b, v115
	v_exp_f32_e32 v114, v114
	v_exp_f32_e32 v115, v115
	v_fma_f32 v125, -v122, v124, 1.0
	v_fmac_f32_e32 v124, v125, v124
	v_div_scale_f32 v125, vcc, 1.0, v117, 1.0
	v_mul_f32_e32 v126, v125, v124
	v_fma_f32 v127, -v122, v126, v125
	v_fmac_f32_e32 v126, v127, v124
	v_fma_f32 v122, -v122, v126, v125
	v_div_fmas_f32 v122, v122, v124, v126
	v_div_fixup_f32 v117, v122, v117, 1.0
	v_div_scale_f32 v122, s[14:15], v116, v116, 1.0
	v_rcp_f32_e32 v124, v122
	v_pk_add_f32 v[114:115], v[114:115], 1.0 op_sel_hi:[1,0]
	v_cvt_pk_bf16_f32 v112, v112, v113
	v_cvt_pk_bf16_f32 v113, v118, v119
	v_fma_f32 v125, -v122, v124, 1.0
	v_fmac_f32_e32 v124, v125, v124
	v_div_scale_f32 v125, vcc, 1.0, v116, 1.0
	v_mul_f32_e32 v126, v125, v124
	v_fma_f32 v127, -v122, v126, v125
	v_fmac_f32_e32 v126, v127, v124
	v_fma_f32 v122, -v122, v126, v125
	v_div_fmas_f32 v122, v122, v124, v126
	v_div_fixup_f32 v116, v122, v116, 1.0
	v_div_scale_f32 v122, s[14:15], v115, v115, 1.0
	v_pk_mul_f32 v[116:117], v[116:117], v[120:121]
	v_lshlrev_b32_e32 v120, 16, v123
	v_and_b32_e32 v121, 0xffff0000, v123
	v_rcp_f32_e32 v123, v122
	s_nop 0
	v_fma_f32 v124, -v122, v123, 1.0
	v_fmac_f32_e32 v123, v124, v123
	v_div_scale_f32 v124, vcc, 1.0, v115, 1.0
	v_mul_f32_e32 v125, v124, v123
	v_fma_f32 v126, -v122, v125, v124
	v_fmac_f32_e32 v125, v126, v123
	v_fma_f32 v122, -v122, v125, v124
	v_div_fmas_f32 v122, v122, v123, v125
	v_div_fixup_f32 v115, v122, v115, 1.0
	v_div_scale_f32 v122, s[14:15], v114, v114, 1.0
	v_rcp_f32_e32 v123, v122
	s_nop 0
	v_fma_f32 v124, -v122, v123, 1.0
	v_fmac_f32_e32 v123, v124, v123
	v_div_scale_f32 v124, vcc, 1.0, v114, 1.0
	v_mul_f32_e32 v125, v124, v123
	v_fma_f32 v126, -v122, v125, v124
	v_fmac_f32_e32 v125, v126, v123
	v_fma_f32 v122, -v122, v125, v124
	v_div_fmas_f32 v122, v122, v123, v125
	v_div_fixup_f32 v114, v122, v114, 1.0
	v_pk_mul_f32 v[120:121], v[114:115], v[120:121]
	v_cvt_pk_bf16_f32 v114, v116, v117
	v_cvt_pk_bf16_f32 v115, v120, v121
	global_store_dwordx4 v[146:147], v[112:115], off offset:1280
	s_nop 1
	v_or_b32_e32 v112, 16, v144
	v_ashrrev_i32_e32 v113, 31, v112
	v_lshlrev_b64 v[114:115], 10, v[112:113]
	v_lshl_add_u64 v[114:115], s[36:37], 0, v[114:115]
	v_lshl_add_u64 v[114:115], v[114:115], 0, v[142:143]
	s_nop 1
	v_lshlrev_b64 v[112:113], 11, v[112:113]
	s_waitcnt vmcnt(7)
; __device__ __forceinline__ float sigmoidf_(float x) { return 1.f / (1.f + __expf(-x)); }
; __device__ __forceinline__ unsigned cvt_pk_bf16(float lo, float hi) { const f32x2c v = {lo, hi}; const bf16x2c b = __builtin_convertvector(v, bf16x2c); return __builtin_bit_cast(unsigned, b); }
;     __device__ __forceinline__ void operator()(const f32x4 (&acc)[2][2][4][2], const Unit& u, int wr, int wc, int fr, int fq) const {
;     ...
;             for (int m = 0; m < 4; ++m) { const size_t row = (size_t)(row0 + ai * HALF + m * 16);
; #pragma unroll
;                 for (int bj = 0; bj < 2; ++bj) { const int col = col0 + bj * HALF;
;                     const u32x4 zz = *(const u32x4*)(Z + row * 512 + col);
;                     const f32x4 b0 = *(const f32x4*)(bias + col), b1 = *(const f32x4*)(bias + col + 4);
;                     const f32x4 v0 = acc[ai][bj][m][0] + b0, v1 = acc[ai][bj][m][1] + b1;
;                     float o[8]; const unsigned zw[4] = {zz.x, zz.y, zz.z, zz.w};
; #pragma unroll
;                     for (int q = 0; q < 4; ++q) { const float zl = __builtin_bit_cast(float, zw[q] << 16), zh = __builtin_bit_cast(float, zw[q] & 0xffff0000u);
;                         const float al = (q < 2) ? v0[2 * q] : v1[2 * q - 4], ah = (q < 2) ? v0[2 * q + 1] : v1[2 * q - 3];
;                         o[2 * q] = zl * sigmoidf_(al); o[2 * q + 1] = zh * sigmoidf_(ah); }
;                     u32x4 w; w.x = cvt_pk_bf16(o[0], o[1]); w.y = cvt_pk_bf16(o[2], o[3]); w.z = cvt_pk_bf16(o[4], o[5]); w.w = cvt_pk_bf16(o[6], o[7]);
;                     *(u32x4*)(YM + row * D + 512 + col) = w; } }
	v_mov_b32_e32 v116, v198
	v_mov_b32_e32 v117, v199
	v_mov_b32_e32 v118, v200
	v_mov_b32_e32 v119, v201
	v_mov_b32_e32 v120, v174
	v_mov_b32_e32 v121, v175
	v_mov_b32_e32 v122, v176
	v_mov_b32_e32 v123, v177
	v_mov_b32_e32 v124, v170
	v_mov_b32_e32 v125, v171
	v_mov_b32_e32 v126, v172
	v_mov_b32_e32 v127, v173
	s_mov_b64 s[98:99], 0x20000
	v_lshl_add_u64 v[168:169], v[166:167], 0, s[98:99]
	global_load_dwordx4 v[198:201], v[168:169], off
	v_pk_add_f32 v[104:105], v[104:105], v[120:121]
	v_pk_add_f32 v[108:109], v[108:109], v[124:125]
	v_lshlrev_b32_e32 v120, 16, v116
	v_mul_f32_e32 v108, 0xbfb8aa3b, v108
	v_mul_f32_e32 v109, 0xbfb8aa3b, v109
	v_exp_f32_e32 v108, v108
	v_exp_f32_e32 v109, v109
	v_and_b32_e32 v121, 0xffff0000, v116
	v_pk_add_f32 v[106:107], v[106:107], v[122:123]
	v_pk_add_f32 v[110:111], v[110:111], v[126:127]
	v_pk_add_f32 v[108:109], v[108:109], 1.0 op_sel_hi:[1,0]
	v_mul_f32_e32 v110, 0xbfb8aa3b, v110
	v_div_scale_f32 v116, s[14:15], v109, v109, 1.0
	v_rcp_f32_e32 v122, v116
	v_mul_f32_e32 v111, 0xbfb8aa3b, v111
	v_exp_f32_e32 v110, v110
	v_exp_f32_e32 v111, v111
	v_fma_f32 v123, -v116, v122, 1.0
	v_fmac_f32_e32 v122, v123, v122
	v_div_scale_f32 v123, vcc, 1.0, v109, 1.0
	v_mul_f32_e32 v124, v123, v122
	v_fma_f32 v125, -v116, v124, v123
	v_fmac_f32_e32 v124, v125, v122
	v_fma_f32 v116, -v116, v124, v123
	v_div_fmas_f32 v116, v116, v122, v124
	v_div_fixup_f32 v109, v116, v109, 1.0
	v_div_scale_f32 v116, s[14:15], v108, v108, 1.0
	v_rcp_f32_e32 v122, v116
	v_pk_add_f32 v[110:111], v[110:111], 1.0 op_sel_hi:[1,0]
	v_mul_f32_e32 v104, 0xbfb8aa3b, v104
	v_mul_f32_e32 v105, 0xbfb8aa3b, v105
	v_fma_f32 v123, -v116, v122, 1.0
	v_fmac_f32_e32 v122, v123, v122
	v_div_scale_f32 v123, vcc, 1.0, v108, 1.0
	v_mul_f32_e32 v124, v123, v122
	v_fma_f32 v125, -v116, v124, v123
	v_fmac_f32_e32 v124, v125, v122
	v_fma_f32 v116, -v116, v124, v123
	v_div_fmas_f32 v116, v116, v122, v124
	v_div_fixup_f32 v108, v116, v108, 1.0
	v_pk_mul_f32 v[108:109], v[108:109], v[120:121]
	v_div_scale_f32 v120, s[14:15], v111, v111, 1.0
	v_rcp_f32_e32 v121, v120
	v_exp_f32_e32 v104, v104
	v_exp_f32_e32 v105, v105
	v_lshlrev_b32_e32 v116, 16, v117
	v_fma_f32 v122, -v120, v121, 1.0
	v_fmac_f32_e32 v121, v122, v121
	v_div_scale_f32 v122, vcc, 1.0, v111, 1.0
	v_mul_f32_e32 v123, v122, v121
	v_fma_f32 v124, -v120, v123, v122
	v_fmac_f32_e32 v123, v124, v121
	v_fma_f32 v120, -v120, v123, v122
	v_div_fmas_f32 v120, v120, v121, v123
	v_div_fixup_f32 v111, v120, v111, 1.0
	v_div_scale_f32 v120, s[14:15], v110, v110, 1.0
	v_rcp_f32_e32 v121, v120
	v_and_b32_e32 v117, 0xffff0000, v117
	v_pk_add_f32 v[104:105], v[104:105], 1.0 op_sel_hi:[1,0]
	v_fma_f32 v122, -v120, v121, 1.0
	v_fmac_f32_e32 v121, v122, v121
	v_div_scale_f32 v122, vcc, 1.0, v110, 1.0
	v_mul_f32_e32 v123, v122, v121
	v_fma_f32 v124, -v120, v123, v122
	v_fmac_f32_e32 v123, v124, v121
	v_fma_f32 v120, -v120, v123, v122
	v_div_fmas_f32 v120, v120, v121, v123
	v_div_fixup_f32 v110, v120, v110, 1.0
	v_pk_mul_f32 v[110:111], v[110:111], v[116:117]
	v_lshlrev_b32_e32 v116, 16, v118
	v_and_b32_e32 v117, 0xffff0000, v118
	v_div_scale_f32 v118, s[14:15], v105, v105, 1.0
	v_rcp_f32_e32 v120, v118
	s_nop 0
	v_fma_f32 v121, -v118, v120, 1.0
	v_fmac_f32_e32 v120, v121, v120
	v_div_scale_f32 v121, vcc, 1.0, v105, 1.0
	v_mul_f32_e32 v122, v121, v120
	v_fma_f32 v123, -v118, v122, v121
	v_fmac_f32_e32 v122, v123, v120
	v_fma_f32 v118, -v118, v122, v121
	v_div_fmas_f32 v118, v118, v120, v122
	v_div_fixup_f32 v105, v118, v105, 1.0
	v_div_scale_f32 v118, s[14:15], v104, v104, 1.0
	v_rcp_f32_e32 v120, v118
	s_nop 0
	v_fma_f32 v121, -v118, v120, 1.0
	v_fmac_f32_e32 v120, v121, v120
	v_div_scale_f32 v121, vcc, 1.0, v104, 1.0
	v_mul_f32_e32 v122, v121, v120
	v_fma_f32 v123, -v118, v122, v121
	v_fmac_f32_e32 v122, v123, v120
	v_fma_f32 v118, -v118, v122, v121
	v_div_fmas_f32 v118, v118, v120, v122
	v_div_fixup_f32 v104, v118, v104, 1.0
	v_pk_mul_f32 v[116:117], v[104:105], v[116:117]
	v_mul_f32_e32 v104, 0xbfb8aa3b, v106
	v_mul_f32_e32 v105, 0xbfb8aa3b, v107
	v_exp_f32_e32 v104, v104
	v_exp_f32_e32 v105, v105
	v_lshlrev_b32_e32 v106, 16, v119
	v_and_b32_e32 v107, 0xffff0000, v119
	v_pk_add_f32 v[104:105], v[104:105], 1.0 op_sel_hi:[1,0]
	s_nop 0
	v_div_scale_f32 v118, s[14:15], v105, v105, 1.0
	v_rcp_f32_e32 v119, v118
	s_nop 0
	v_fma_f32 v120, -v118, v119, 1.0
	v_fmac_f32_e32 v119, v120, v119
	v_div_scale_f32 v120, vcc, 1.0, v105, 1.0
	v_mul_f32_e32 v121, v120, v119
	v_fma_f32 v122, -v118, v121, v120
	v_fmac_f32_e32 v121, v122, v119
	v_fma_f32 v118, -v118, v121, v120
	v_div_fmas_f32 v118, v118, v119, v121
	v_div_fixup_f32 v105, v118, v105, 1.0
	v_div_scale_f32 v118, s[14:15], v104, v104, 1.0
	v_rcp_f32_e32 v119, v118
	s_nop 0
	v_fma_f32 v120, -v118, v119, 1.0
	v_fmac_f32_e32 v119, v120, v119
	v_div_scale_f32 v120, vcc, 1.0, v104, 1.0
	v_mul_f32_e32 v121, v120, v119
	v_fma_f32 v122, -v118, v121, v120
	v_fmac_f32_e32 v121, v122, v119
	v_fma_f32 v118, -v118, v121, v120
	v_div_fmas_f32 v118, v118, v119, v121
	v_div_fixup_f32 v104, v118, v104, 1.0
	v_pk_mul_f32 v[118:119], v[104:105], v[106:107]
	v_cvt_pk_bf16_f32 v104, v108, v109
	v_lshl_add_u64 v[108:109], s[26:27], 0, v[112:113]
	v_cvt_pk_bf16_f32 v105, v110, v111
	v_cvt_pk_bf16_f32 v106, v116, v117
	v_cvt_pk_bf16_f32 v107, v118, v119
	v_lshl_add_u64 v[112:113], v[108:109], 0, v[142:143]
	global_store_dwordx4 v[112:113], v[104:107], off offset:1024
	s_nop 1
	s_nop 0
	s_waitcnt vmcnt(8)
; __device__ __forceinline__ float sigmoidf_(float x) { return 1.f / (1.f + __expf(-x)); }
; __device__ __forceinline__ unsigned cvt_pk_bf16(float lo, float hi) { const f32x2c v = {lo, hi}; const bf16x2c b = __builtin_convertvector(v, bf16x2c); return __builtin_bit_cast(unsigned, b); }
;     __device__ __forceinline__ void operator()(const f32x4 (&acc)[2][2][4][2], const Unit& u, int wr, int wc, int fr, int fq) const {
;     ...
;             for (int m = 0; m < 4; ++m) { const size_t row = (size_t)(row0 + ai * HALF + m * 16);
; #pragma unroll
;                 for (int bj = 0; bj < 2; ++bj) { const int col = col0 + bj * HALF;
;                     const u32x4 zz = *(const u32x4*)(Z + row * 512 + col);
;                     const f32x4 b0 = *(const f32x4*)(bias + col), b1 = *(const f32x4*)(bias + col + 4);
;                     const f32x4 v0 = acc[ai][bj][m][0] + b0, v1 = acc[ai][bj][m][1] + b1;
;                     float o[8]; const unsigned zw[4] = {zz.x, zz.y, zz.z, zz.w};
; #pragma unroll
;                     for (int q = 0; q < 4; ++q) { const float zl = __builtin_bit_cast(float, zw[q] << 16), zh = __builtin_bit_cast(float, zw[q] & 0xffff0000u);
;                         const float al = (q < 2) ? v0[2 * q] : v1[2 * q - 4], ah = (q < 2) ? v0[2 * q + 1] : v1[2 * q - 3];
;                         o[2 * q] = zl * sigmoidf_(al); o[2 * q + 1] = zh * sigmoidf_(ah); }
;                     u32x4 w; w.x = cvt_pk_bf16(o[0], o[1]); w.y = cvt_pk_bf16(o[2], o[3]); w.z = cvt_pk_bf16(o[4], o[5]); w.w = cvt_pk_bf16(o[6], o[7]);
;                     *(u32x4*)(YM + row * D + 512 + col) = w; } }
	v_mov_b32_e32 v104, v202
	v_mov_b32_e32 v105, v203
	v_mov_b32_e32 v106, v204
	v_mov_b32_e32 v107, v205
	v_mov_b32_e32 v108, v182
	v_mov_b32_e32 v109, v183
	v_mov_b32_e32 v110, v184
	v_mov_b32_e32 v111, v185
	v_mov_b32_e32 v114, v178
	v_mov_b32_e32 v115, v179
	v_mov_b32_e32 v116, v180
	v_mov_b32_e32 v117, v181
	global_load_dwordx4 v[202:205], v[168:169], off offset:256
	v_pk_add_f32 v[108:109], v[96:97], v[108:109]
	v_pk_add_f32 v[100:101], v[100:101], v[114:115]
	v_pk_add_f32 v[98:99], v[98:99], v[110:111]
	v_mul_f32_e32 v96, 0xbfb8aa3b, v100
	v_mul_f32_e32 v97, 0xbfb8aa3b, v101
	v_exp_f32_e32 v96, v96
	v_exp_f32_e32 v97, v97
	v_lshlrev_b32_e32 v100, 16, v104
	v_and_b32_e32 v101, 0xffff0000, v104
	v_pk_add_f32 v[102:103], v[102:103], v[116:117]
	v_pk_add_f32 v[96:97], v[96:97], 1.0 op_sel_hi:[1,0]
	v_mul_f32_e32 v98, 0xbfb8aa3b, v98
	v_div_scale_f32 v104, s[14:15], v97, v97, 1.0
	v_rcp_f32_e32 v110, v104
	v_mul_f32_e32 v99, 0xbfb8aa3b, v99
	v_exp_f32_e32 v98, v98
	v_exp_f32_e32 v99, v99
	v_fma_f32 v111, -v104, v110, 1.0
	v_fmac_f32_e32 v110, v111, v110
	v_div_scale_f32 v111, vcc, 1.0, v97, 1.0
	v_mul_f32_e32 v114, v111, v110
	v_fma_f32 v115, -v104, v114, v111
	v_fmac_f32_e32 v114, v115, v110
	v_fma_f32 v104, -v104, v114, v111
	v_div_fmas_f32 v104, v104, v110, v114
	v_div_fixup_f32 v97, v104, v97, 1.0
	v_div_scale_f32 v104, s[14:15], v96, v96, 1.0
	v_rcp_f32_e32 v110, v104
	v_pk_add_f32 v[98:99], v[98:99], 1.0 op_sel_hi:[1,0]
	v_fma_f32 v111, -v104, v110, 1.0
	v_fmac_f32_e32 v110, v111, v110
	v_div_scale_f32 v111, vcc, 1.0, v96, 1.0
	v_mul_f32_e32 v114, v111, v110
	v_fma_f32 v115, -v104, v114, v111
	v_fmac_f32_e32 v114, v115, v110
	v_fma_f32 v104, -v104, v114, v111
	v_div_fmas_f32 v104, v104, v110, v114
	v_div_fixup_f32 v96, v104, v96, 1.0
	v_pk_mul_f32 v[96:97], v[96:97], v[100:101]
	v_mul_f32_e32 v100, 0xbfb8aa3b, v102
	v_mul_f32_e32 v101, 0xbfb8aa3b, v103
	v_exp_f32_e32 v100, v100
	v_exp_f32_e32 v101, v101
	v_lshlrev_b32_e32 v102, 16, v105
	v_and_b32_e32 v103, 0xffff0000, v105
	v_cvt_pk_bf16_f32 v96, v96, v97
	v_pk_add_f32 v[100:101], v[100:101], 1.0 op_sel_hi:[1,0]
	s_nop 0
	v_div_scale_f32 v104, s[14:15], v101, v101, 1.0
	v_rcp_f32_e32 v105, v104
	s_nop 0
	v_fma_f32 v110, -v104, v105, 1.0
	v_fmac_f32_e32 v105, v110, v105
	v_div_scale_f32 v110, vcc, 1.0, v101, 1.0
	v_mul_f32_e32 v111, v110, v105
	v_fma_f32 v114, -v104, v111, v110
	v_fmac_f32_e32 v111, v114, v105
	v_fma_f32 v104, -v104, v111, v110
	v_div_fmas_f32 v104, v104, v105, v111
	v_div_fixup_f32 v101, v104, v101, 1.0
	v_div_scale_f32 v104, s[14:15], v100, v100, 1.0
	v_rcp_f32_e32 v105, v104
	s_nop 0
	v_fma_f32 v110, -v104, v105, 1.0
	v_fmac_f32_e32 v105, v110, v105
	v_div_scale_f32 v110, vcc, 1.0, v100, 1.0
	v_mul_f32_e32 v111, v110, v105
	v_fma_f32 v114, -v104, v111, v110
	v_fmac_f32_e32 v111, v114, v105
	v_fma_f32 v104, -v104, v111, v110
	v_div_fmas_f32 v104, v104, v105, v111
	v_div_fixup_f32 v100, v104, v100, 1.0
	v_pk_mul_f32 v[100:101], v[100:101], v[102:103]
	v_mul_f32_e32 v102, 0xbfb8aa3b, v108
	v_mul_f32_e32 v103, 0xbfb8aa3b, v109
	v_exp_f32_e32 v102, v102
	v_exp_f32_e32 v103, v103
	v_lshlrev_b32_e32 v104, 16, v106
	v_and_b32_e32 v105, 0xffff0000, v106
	v_cvt_pk_bf16_f32 v97, v100, v101
	v_pk_add_f32 v[102:103], v[102:103], 1.0 op_sel_hi:[1,0]
	s_nop 0
	v_div_scale_f32 v106, s[14:15], v103, v103, 1.0
	v_rcp_f32_e32 v108, v106
	s_nop 0
	v_fma_f32 v109, -v106, v108, 1.0
	v_fmac_f32_e32 v108, v109, v108
	v_div_scale_f32 v109, vcc, 1.0, v103, 1.0
	v_mul_f32_e32 v110, v109, v108
	v_fma_f32 v111, -v106, v110, v109
	v_fmac_f32_e32 v110, v111, v108
	v_fma_f32 v106, -v106, v110, v109
	v_div_fmas_f32 v106, v106, v108, v110
	v_div_fixup_f32 v103, v106, v103, 1.0
	v_div_scale_f32 v106, s[14:15], v102, v102, 1.0
	v_rcp_f32_e32 v108, v106
	s_nop 0
	v_fma_f32 v109, -v106, v108, 1.0
	v_fmac_f32_e32 v108, v109, v108
	v_div_scale_f32 v109, vcc, 1.0, v102, 1.0
	v_mul_f32_e32 v110, v109, v108
	v_fma_f32 v111, -v106, v110, v109
	v_fmac_f32_e32 v110, v111, v108
	v_fma_f32 v106, -v106, v110, v109
	v_div_fmas_f32 v106, v106, v108, v110
	v_div_fixup_f32 v102, v106, v102, 1.0
	v_div_scale_f32 v106, s[14:15], v99, v99, 1.0
	v_pk_mul_f32 v[102:103], v[102:103], v[104:105]
	v_lshlrev_b32_e32 v104, 16, v107
	v_and_b32_e32 v105, 0xffff0000, v107
	v_rcp_f32_e32 v107, v106
	s_nop 0
	v_fma_f32 v108, -v106, v107, 1.0
	v_fmac_f32_e32 v107, v108, v107
	v_div_scale_f32 v108, vcc, 1.0, v99, 1.0
	v_mul_f32_e32 v109, v108, v107
	v_fma_f32 v110, -v106, v109, v108
	v_fmac_f32_e32 v109, v110, v107
	v_fma_f32 v106, -v106, v109, v108
	v_div_fmas_f32 v106, v106, v107, v109
	v_div_fixup_f32 v99, v106, v99, 1.0
	v_div_scale_f32 v106, s[14:15], v98, v98, 1.0
	v_rcp_f32_e32 v107, v106
	s_nop 0
	v_fma_f32 v108, -v106, v107, 1.0
	v_fmac_f32_e32 v107, v108, v107
	v_div_scale_f32 v108, vcc, 1.0, v98, 1.0
	v_mul_f32_e32 v109, v108, v107
	v_fma_f32 v110, -v106, v109, v108
	v_fmac_f32_e32 v109, v110, v107
	v_fma_f32 v106, -v106, v109, v108
	v_div_fmas_f32 v106, v106, v107, v109
	v_div_fixup_f32 v98, v106, v98, 1.0
	v_pk_mul_f32 v[104:105], v[98:99], v[104:105]
	v_cvt_pk_bf16_f32 v98, v102, v103
	v_cvt_pk_bf16_f32 v99, v104, v105
	global_store_dwordx4 v[112:113], v[96:99], off offset:1280
	s_nop 1
	v_or_b32_e32 v96, 32, v144
	v_ashrrev_i32_e32 v97, 31, v96
	v_lshlrev_b64 v[98:99], 10, v[96:97]
	v_lshl_add_u64 v[98:99], s[36:37], 0, v[98:99]
	v_lshl_add_u64 v[98:99], v[98:99], 0, v[142:143]
	s_nop 1
	v_lshlrev_b64 v[96:97], 11, v[96:97]
	s_waitcnt vmcnt(9)
; __device__ __forceinline__ float sigmoidf_(float x) { return 1.f / (1.f + __expf(-x)); }
; __device__ __forceinline__ unsigned cvt_pk_bf16(float lo, float hi) { const f32x2c v = {lo, hi}; const bf16x2c b = __builtin_convertvector(v, bf16x2c); return __builtin_bit_cast(unsigned, b); }
;     __device__ __forceinline__ void operator()(const f32x4 (&acc)[2][2][4][2], const Unit& u, int wr, int wc, int fr, int fq) const {
;     ...
;             for (int m = 0; m < 4; ++m) { const size_t row = (size_t)(row0 + ai * HALF + m * 16);
; #pragma unroll
;                 for (int bj = 0; bj < 2; ++bj) { const int col = col0 + bj * HALF;
;                     const u32x4 zz = *(const u32x4*)(Z + row * 512 + col);
;                     const f32x4 b0 = *(const f32x4*)(bias + col), b1 = *(const f32x4*)(bias + col + 4);
;                     const f32x4 v0 = acc[ai][bj][m][0] + b0, v1 = acc[ai][bj][m][1] + b1;
;                     float o[8]; const unsigned zw[4] = {zz.x, zz.y, zz.z, zz.w};
; #pragma unroll
;                     for (int q = 0; q < 4; ++q) { const float zl = __builtin_bit_cast(float, zw[q] << 16), zh = __builtin_bit_cast(float, zw[q] & 0xffff0000u);
;                         const float al = (q < 2) ? v0[2 * q] : v1[2 * q - 4], ah = (q < 2) ? v0[2 * q + 1] : v1[2 * q - 3];
;                         o[2 * q] = zl * sigmoidf_(al); o[2 * q + 1] = zh * sigmoidf_(ah); }
;                     u32x4 w; w.x = cvt_pk_bf16(o[0], o[1]); w.y = cvt_pk_bf16(o[2], o[3]); w.z = cvt_pk_bf16(o[4], o[5]); w.w = cvt_pk_bf16(o[6], o[7]);
;                     *(u32x4*)(YM + row * D + 512 + col) = w; } }
	v_mov_b32_e32 v100, v206
	v_mov_b32_e32 v101, v207
	v_mov_b32_e32 v102, v208
	v_mov_b32_e32 v103, v209
	v_mov_b32_e32 v104, v174
	v_mov_b32_e32 v105, v175
	v_mov_b32_e32 v106, v176
	v_mov_b32_e32 v107, v177
	v_mov_b32_e32 v108, v170
	v_mov_b32_e32 v109, v171
	v_mov_b32_e32 v110, v172
	v_mov_b32_e32 v111, v173
	s_mov_b64 s[98:99], 0x24000
	v_lshl_add_u64 v[168:169], v[166:167], 0, s[98:99]
	global_load_dwordx4 v[206:209], v[168:169], off
	v_pk_add_f32 v[88:89], v[88:89], v[104:105]
	v_pk_add_f32 v[92:93], v[92:93], v[108:109]
	v_lshlrev_b32_e32 v104, 16, v100
	v_mul_f32_e32 v92, 0xbfb8aa3b, v92
	v_mul_f32_e32 v93, 0xbfb8aa3b, v93
	v_exp_f32_e32 v92, v92
	v_exp_f32_e32 v93, v93
	v_and_b32_e32 v105, 0xffff0000, v100
	v_pk_add_f32 v[90:91], v[90:91], v[106:107]
	v_pk_add_f32 v[94:95], v[94:95], v[110:111]
	v_pk_add_f32 v[92:93], v[92:93], 1.0 op_sel_hi:[1,0]
	v_mul_f32_e32 v94, 0xbfb8aa3b, v94
	v_div_scale_f32 v100, s[14:15], v93, v93, 1.0
	v_rcp_f32_e32 v106, v100
	v_mul_f32_e32 v95, 0xbfb8aa3b, v95
	v_exp_f32_e32 v94, v94
	v_exp_f32_e32 v95, v95
	v_fma_f32 v107, -v100, v106, 1.0
	v_fmac_f32_e32 v106, v107, v106
	v_div_scale_f32 v107, vcc, 1.0, v93, 1.0
	v_mul_f32_e32 v108, v107, v106
	v_fma_f32 v109, -v100, v108, v107
	v_fmac_f32_e32 v108, v109, v106
	v_fma_f32 v100, -v100, v108, v107
	v_div_fmas_f32 v100, v100, v106, v108
	v_div_fixup_f32 v93, v100, v93, 1.0
	v_div_scale_f32 v100, s[14:15], v92, v92, 1.0
	v_rcp_f32_e32 v106, v100
	v_pk_add_f32 v[94:95], v[94:95], 1.0 op_sel_hi:[1,0]
	v_mul_f32_e32 v88, 0xbfb8aa3b, v88
	v_mul_f32_e32 v89, 0xbfb8aa3b, v89
	v_fma_f32 v107, -v100, v106, 1.0
	v_fmac_f32_e32 v106, v107, v106
	v_div_scale_f32 v107, vcc, 1.0, v92, 1.0
	v_mul_f32_e32 v108, v107, v106
	v_fma_f32 v109, -v100, v108, v107
	v_fmac_f32_e32 v108, v109, v106
	v_fma_f32 v100, -v100, v108, v107
	v_div_fmas_f32 v100, v100, v106, v108
	v_div_fixup_f32 v92, v100, v92, 1.0
	v_pk_mul_f32 v[92:93], v[92:93], v[104:105]
	v_div_scale_f32 v104, s[14:15], v95, v95, 1.0
	v_rcp_f32_e32 v105, v104
	v_exp_f32_e32 v88, v88
	v_exp_f32_e32 v89, v89
	v_lshlrev_b32_e32 v100, 16, v101
	v_fma_f32 v106, -v104, v105, 1.0
	v_fmac_f32_e32 v105, v106, v105
	v_div_scale_f32 v106, vcc, 1.0, v95, 1.0
	v_mul_f32_e32 v107, v106, v105
	v_fma_f32 v108, -v104, v107, v106
	v_fmac_f32_e32 v107, v108, v105
	v_fma_f32 v104, -v104, v107, v106
	v_div_fmas_f32 v104, v104, v105, v107
	v_div_fixup_f32 v95, v104, v95, 1.0
	v_div_scale_f32 v104, s[14:15], v94, v94, 1.0
	v_rcp_f32_e32 v105, v104
	v_and_b32_e32 v101, 0xffff0000, v101
	v_pk_add_f32 v[88:89], v[88:89], 1.0 op_sel_hi:[1,0]
	v_fma_f32 v106, -v104, v105, 1.0
	v_fmac_f32_e32 v105, v106, v105
	v_div_scale_f32 v106, vcc, 1.0, v94, 1.0
	v_mul_f32_e32 v107, v106, v105
	v_fma_f32 v108, -v104, v107, v106
	v_fmac_f32_e32 v107, v108, v105
	v_fma_f32 v104, -v104, v107, v106
	v_div_fmas_f32 v104, v104, v105, v107
	v_div_fixup_f32 v94, v104, v94, 1.0
	v_pk_mul_f32 v[94:95], v[94:95], v[100:101]
	v_lshlrev_b32_e32 v100, 16, v102
	v_and_b32_e32 v101, 0xffff0000, v102
	v_div_scale_f32 v102, s[14:15], v89, v89, 1.0
	v_rcp_f32_e32 v104, v102
	s_nop 0
	v_fma_f32 v105, -v102, v104, 1.0
	v_fmac_f32_e32 v104, v105, v104
	v_div_scale_f32 v105, vcc, 1.0, v89, 1.0
	v_mul_f32_e32 v106, v105, v104
	v_fma_f32 v107, -v102, v106, v105
	v_fmac_f32_e32 v106, v107, v104
	v_fma_f32 v102, -v102, v106, v105
	v_div_fmas_f32 v102, v102, v104, v106
	v_div_fixup_f32 v89, v102, v89, 1.0
	v_div_scale_f32 v102, s[14:15], v88, v88, 1.0
	v_rcp_f32_e32 v104, v102
	s_nop 0
	v_fma_f32 v105, -v102, v104, 1.0
	v_fmac_f32_e32 v104, v105, v104
	v_div_scale_f32 v105, vcc, 1.0, v88, 1.0
	v_mul_f32_e32 v106, v105, v104
	v_fma_f32 v107, -v102, v106, v105
	v_fmac_f32_e32 v106, v107, v104
	v_fma_f32 v102, -v102, v106, v105
	v_div_fmas_f32 v102, v102, v104, v106
	v_div_fixup_f32 v88, v102, v88, 1.0
	v_pk_mul_f32 v[100:101], v[88:89], v[100:101]
	v_mul_f32_e32 v88, 0xbfb8aa3b, v90
	v_mul_f32_e32 v89, 0xbfb8aa3b, v91
	v_exp_f32_e32 v88, v88
	v_exp_f32_e32 v89, v89
	v_lshlrev_b32_e32 v90, 16, v103
	v_and_b32_e32 v91, 0xffff0000, v103
	v_pk_add_f32 v[88:89], v[88:89], 1.0 op_sel_hi:[1,0]
	s_nop 0
	v_div_scale_f32 v102, s[14:15], v89, v89, 1.0
	v_rcp_f32_e32 v103, v102
	s_nop 0
	v_fma_f32 v104, -v102, v103, 1.0
	v_fmac_f32_e32 v103, v104, v103
	v_div_scale_f32 v104, vcc, 1.0, v89, 1.0
	v_mul_f32_e32 v105, v104, v103
	v_fma_f32 v106, -v102, v105, v104
	v_fmac_f32_e32 v105, v106, v103
	v_fma_f32 v102, -v102, v105, v104
	v_div_fmas_f32 v102, v102, v103, v105
	v_div_fixup_f32 v89, v102, v89, 1.0
	v_div_scale_f32 v102, s[14:15], v88, v88, 1.0
	v_rcp_f32_e32 v103, v102
	s_nop 0
	v_fma_f32 v104, -v102, v103, 1.0
	v_fmac_f32_e32 v103, v104, v103
	v_div_scale_f32 v104, vcc, 1.0, v88, 1.0
	v_mul_f32_e32 v105, v104, v103
	v_fma_f32 v106, -v102, v105, v104
	v_fmac_f32_e32 v105, v106, v103
	v_fma_f32 v102, -v102, v105, v104
	v_div_fmas_f32 v102, v102, v103, v105
	v_div_fixup_f32 v88, v102, v88, 1.0
	v_pk_mul_f32 v[102:103], v[88:89], v[90:91]
	v_cvt_pk_bf16_f32 v88, v92, v93
	v_lshl_add_u64 v[92:93], s[26:27], 0, v[96:97]
	v_cvt_pk_bf16_f32 v89, v94, v95
	v_cvt_pk_bf16_f32 v90, v100, v101
	v_cvt_pk_bf16_f32 v91, v102, v103
	v_lshl_add_u64 v[96:97], v[92:93], 0, v[142:143]
	global_store_dwordx4 v[96:97], v[88:91], off offset:1024
	s_nop 1
	s_nop 0
	s_waitcnt vmcnt(10)
; __device__ __forceinline__ float sigmoidf_(float x) { return 1.f / (1.f + __expf(-x)); }
; __device__ __forceinline__ unsigned cvt_pk_bf16(float lo, float hi) { const f32x2c v = {lo, hi}; const bf16x2c b = __builtin_convertvector(v, bf16x2c); return __builtin_bit_cast(unsigned, b); }
;     __device__ __forceinline__ void operator()(const f32x4 (&acc)[2][2][4][2], const Unit& u, int wr, int wc, int fr, int fq) const {
;     ...
;             for (int m = 0; m < 4; ++m) { const size_t row = (size_t)(row0 + ai * HALF + m * 16);
; #pragma unroll
;                 for (int bj = 0; bj < 2; ++bj) { const int col = col0 + bj * HALF;
;                     const u32x4 zz = *(const u32x4*)(Z + row * 512 + col);
;                     const f32x4 b0 = *(const f32x4*)(bias + col), b1 = *(const f32x4*)(bias + col + 4);
;                     const f32x4 v0 = acc[ai][bj][m][0] + b0, v1 = acc[ai][bj][m][1] + b1;
;                     float o[8]; const unsigned zw[4] = {zz.x, zz.y, zz.z, zz.w};
; #pragma unroll
;                     for (int q = 0; q < 4; ++q) { const float zl = __builtin_bit_cast(float, zw[q] << 16), zh = __builtin_bit_cast(float, zw[q] & 0xffff0000u);
;                         const float al = (q < 2) ? v0[2 * q] : v1[2 * q - 4], ah = (q < 2) ? v0[2 * q + 1] : v1[2 * q - 3];
;                         o[2 * q] = zl * sigmoidf_(al); o[2 * q + 1] = zh * sigmoidf_(ah); }
;                     u32x4 w; w.x = cvt_pk_bf16(o[0], o[1]); w.y = cvt_pk_bf16(o[2], o[3]); w.z = cvt_pk_bf16(o[4], o[5]); w.w = cvt_pk_bf16(o[6], o[7]);
;                     *(u32x4*)(YM + row * D + 512 + col) = w; } }
	v_mov_b32_e32 v88, v210
	v_mov_b32_e32 v89, v211
	v_mov_b32_e32 v90, v212
	v_mov_b32_e32 v91, v213
	v_mov_b32_e32 v92, v182
	v_mov_b32_e32 v93, v183
	v_mov_b32_e32 v94, v184
	v_mov_b32_e32 v95, v185
	v_mov_b32_e32 v98, v178
	v_mov_b32_e32 v99, v179
	v_mov_b32_e32 v100, v180
	v_mov_b32_e32 v101, v181
	global_load_dwordx4 v[210:213], v[168:169], off offset:256
	v_pk_add_f32 v[92:93], v[80:81], v[92:93]
	v_pk_add_f32 v[84:85], v[84:85], v[98:99]
	v_pk_add_f32 v[82:83], v[82:83], v[94:95]
	v_mul_f32_e32 v80, 0xbfb8aa3b, v84
	v_mul_f32_e32 v81, 0xbfb8aa3b, v85
	v_exp_f32_e32 v80, v80
	v_exp_f32_e32 v81, v81
	v_lshlrev_b32_e32 v84, 16, v88
	v_and_b32_e32 v85, 0xffff0000, v88
	v_pk_add_f32 v[86:87], v[86:87], v[100:101]
	v_pk_add_f32 v[80:81], v[80:81], 1.0 op_sel_hi:[1,0]
	v_mul_f32_e32 v82, 0xbfb8aa3b, v82
	v_div_scale_f32 v88, s[14:15], v81, v81, 1.0
	v_rcp_f32_e32 v94, v88
	v_mul_f32_e32 v83, 0xbfb8aa3b, v83
	v_exp_f32_e32 v82, v82
	v_exp_f32_e32 v83, v83
	v_fma_f32 v95, -v88, v94, 1.0
	v_fmac_f32_e32 v94, v95, v94
	v_div_scale_f32 v95, vcc, 1.0, v81, 1.0
	v_mul_f32_e32 v98, v95, v94
	v_fma_f32 v99, -v88, v98, v95
	v_fmac_f32_e32 v98, v99, v94
	v_fma_f32 v88, -v88, v98, v95
	v_div_fmas_f32 v88, v88, v94, v98
	v_div_fixup_f32 v81, v88, v81, 1.0
	v_div_scale_f32 v88, s[14:15], v80, v80, 1.0
	v_rcp_f32_e32 v94, v88
	v_pk_add_f32 v[82:83], v[82:83], 1.0 op_sel_hi:[1,0]
	v_fma_f32 v95, -v88, v94, 1.0
	v_fmac_f32_e32 v94, v95, v94
	v_div_scale_f32 v95, vcc, 1.0, v80, 1.0
	v_mul_f32_e32 v98, v95, v94
	v_fma_f32 v99, -v88, v98, v95
	v_fmac_f32_e32 v98, v99, v94
	v_fma_f32 v88, -v88, v98, v95
	v_div_fmas_f32 v88, v88, v94, v98
	v_div_fixup_f32 v80, v88, v80, 1.0
	v_pk_mul_f32 v[80:81], v[80:81], v[84:85]
	v_mul_f32_e32 v84, 0xbfb8aa3b, v86
	v_mul_f32_e32 v85, 0xbfb8aa3b, v87
	v_exp_f32_e32 v84, v84
	v_exp_f32_e32 v85, v85
	v_lshlrev_b32_e32 v86, 16, v89
	v_and_b32_e32 v87, 0xffff0000, v89
	v_cvt_pk_bf16_f32 v80, v80, v81
	v_pk_add_f32 v[84:85], v[84:85], 1.0 op_sel_hi:[1,0]
	s_nop 0
	v_div_scale_f32 v88, s[14:15], v85, v85, 1.0
	v_rcp_f32_e32 v89, v88
	s_nop 0
	v_fma_f32 v94, -v88, v89, 1.0
	v_fmac_f32_e32 v89, v94, v89
	v_div_scale_f32 v94, vcc, 1.0, v85, 1.0
	v_mul_f32_e32 v95, v94, v89
	v_fma_f32 v98, -v88, v95, v94
	v_fmac_f32_e32 v95, v98, v89
	v_fma_f32 v88, -v88, v95, v94
	v_div_fmas_f32 v88, v88, v89, v95
	v_div_fixup_f32 v85, v88, v85, 1.0
	v_div_scale_f32 v88, s[14:15], v84, v84, 1.0
	v_rcp_f32_e32 v89, v88
	s_nop 0
	v_fma_f32 v94, -v88, v89, 1.0
	v_fmac_f32_e32 v89, v94, v89
	v_div_scale_f32 v94, vcc, 1.0, v84, 1.0
	v_mul_f32_e32 v95, v94, v89
	v_fma_f32 v98, -v88, v95, v94
	v_fmac_f32_e32 v95, v98, v89
	v_fma_f32 v88, -v88, v95, v94
	v_div_fmas_f32 v88, v88, v89, v95
	v_div_fixup_f32 v84, v88, v84, 1.0
	v_pk_mul_f32 v[84:85], v[84:85], v[86:87]
	v_mul_f32_e32 v86, 0xbfb8aa3b, v92
	v_mul_f32_e32 v87, 0xbfb8aa3b, v93
	v_exp_f32_e32 v86, v86
	v_exp_f32_e32 v87, v87
	v_lshlrev_b32_e32 v88, 16, v90
	v_and_b32_e32 v89, 0xffff0000, v90
	v_cvt_pk_bf16_f32 v81, v84, v85
	v_pk_add_f32 v[86:87], v[86:87], 1.0 op_sel_hi:[1,0]
	s_nop 0
	v_div_scale_f32 v90, s[14:15], v87, v87, 1.0
	v_rcp_f32_e32 v92, v90
	s_nop 0
	v_fma_f32 v93, -v90, v92, 1.0
	v_fmac_f32_e32 v92, v93, v92
	v_div_scale_f32 v93, vcc, 1.0, v87, 1.0
	v_mul_f32_e32 v94, v93, v92
	v_fma_f32 v95, -v90, v94, v93
	v_fmac_f32_e32 v94, v95, v92
	v_fma_f32 v90, -v90, v94, v93
	v_div_fmas_f32 v90, v90, v92, v94
	v_div_fixup_f32 v87, v90, v87, 1.0
	v_div_scale_f32 v90, s[14:15], v86, v86, 1.0
	v_rcp_f32_e32 v92, v90
	s_nop 0
	v_fma_f32 v93, -v90, v92, 1.0
	v_fmac_f32_e32 v92, v93, v92
	v_div_scale_f32 v93, vcc, 1.0, v86, 1.0
	v_mul_f32_e32 v94, v93, v92
	v_fma_f32 v95, -v90, v94, v93
	v_fmac_f32_e32 v94, v95, v92
	v_fma_f32 v90, -v90, v94, v93
	v_div_fmas_f32 v90, v90, v92, v94
	v_div_fixup_f32 v86, v90, v86, 1.0
	v_div_scale_f32 v90, s[14:15], v83, v83, 1.0
	v_pk_mul_f32 v[86:87], v[86:87], v[88:89]
	v_lshlrev_b32_e32 v88, 16, v91
	v_and_b32_e32 v89, 0xffff0000, v91
	v_rcp_f32_e32 v91, v90
	s_nop 0
	v_fma_f32 v92, -v90, v91, 1.0
	v_fmac_f32_e32 v91, v92, v91
	v_div_scale_f32 v92, vcc, 1.0, v83, 1.0
	v_mul_f32_e32 v93, v92, v91
	v_fma_f32 v94, -v90, v93, v92
	v_fmac_f32_e32 v93, v94, v91
	v_fma_f32 v90, -v90, v93, v92
	v_div_fmas_f32 v90, v90, v91, v93
	v_div_fixup_f32 v83, v90, v83, 1.0
	v_div_scale_f32 v90, s[14:15], v82, v82, 1.0
	v_rcp_f32_e32 v91, v90
	s_nop 0
	v_fma_f32 v92, -v90, v91, 1.0
	v_fmac_f32_e32 v91, v92, v91
	v_div_scale_f32 v92, vcc, 1.0, v82, 1.0
	v_mul_f32_e32 v93, v92, v91
	v_fma_f32 v94, -v90, v93, v92
	v_fmac_f32_e32 v93, v94, v91
	v_fma_f32 v90, -v90, v93, v92
	v_div_fmas_f32 v90, v90, v91, v93
	v_div_fixup_f32 v82, v90, v82, 1.0
	v_pk_mul_f32 v[88:89], v[82:83], v[88:89]
	v_cvt_pk_bf16_f32 v82, v86, v87
	v_cvt_pk_bf16_f32 v83, v88, v89
	global_store_dwordx4 v[96:97], v[80:83], off offset:1280
	s_nop 1
	v_or_b32_e32 v80, 48, v144
	v_ashrrev_i32_e32 v81, 31, v80
	v_lshlrev_b64 v[82:83], 10, v[80:81]
	v_lshl_add_u64 v[82:83], s[36:37], 0, v[82:83]
	v_lshl_add_u64 v[82:83], v[82:83], 0, v[142:143]
	s_nop 1
	v_lshlrev_b64 v[80:81], 11, v[80:81]
	s_waitcnt vmcnt(11)
; __device__ __forceinline__ float sigmoidf_(float x) { return 1.f / (1.f + __expf(-x)); }
; __device__ __forceinline__ unsigned cvt_pk_bf16(float lo, float hi) { const f32x2c v = {lo, hi}; const bf16x2c b = __builtin_convertvector(v, bf16x2c); return __builtin_bit_cast(unsigned, b); }
;     __device__ __forceinline__ void operator()(const f32x4 (&acc)[2][2][4][2], const Unit& u, int wr, int wc, int fr, int fq) const {
;     ...
;             for (int m = 0; m < 4; ++m) { const size_t row = (size_t)(row0 + ai * HALF + m * 16);
; #pragma unroll
;                 for (int bj = 0; bj < 2; ++bj) { const int col = col0 + bj * HALF;
;                     const u32x4 zz = *(const u32x4*)(Z + row * 512 + col);
;                     const f32x4 b0 = *(const f32x4*)(bias + col), b1 = *(const f32x4*)(bias + col + 4);
;                     const f32x4 v0 = acc[ai][bj][m][0] + b0, v1 = acc[ai][bj][m][1] + b1;
;                     float o[8]; const unsigned zw[4] = {zz.x, zz.y, zz.z, zz.w};
; #pragma unroll
;                     for (int q = 0; q < 4; ++q) { const float zl = __builtin_bit_cast(float, zw[q] << 16), zh = __builtin_bit_cast(float, zw[q] & 0xffff0000u);
;                         const float al = (q < 2) ? v0[2 * q] : v1[2 * q - 4], ah = (q < 2) ? v0[2 * q + 1] : v1[2 * q - 3];
;                         o[2 * q] = zl * sigmoidf_(al); o[2 * q + 1] = zh * sigmoidf_(ah); }
;                     u32x4 w; w.x = cvt_pk_bf16(o[0], o[1]); w.y = cvt_pk_bf16(o[2], o[3]); w.z = cvt_pk_bf16(o[4], o[5]); w.w = cvt_pk_bf16(o[6], o[7]);
;                     *(u32x4*)(YM + row * D + 512 + col) = w; } }
	v_mov_b32_e32 v84, v186
	v_mov_b32_e32 v85, v187
	v_mov_b32_e32 v86, v188
	v_mov_b32_e32 v87, v189
	v_mov_b32_e32 v88, v174
	v_mov_b32_e32 v89, v175
	v_mov_b32_e32 v90, v176
	v_mov_b32_e32 v91, v177
	v_mov_b32_e32 v92, v170
	v_mov_b32_e32 v93, v171
	v_mov_b32_e32 v94, v172
	v_mov_b32_e32 v95, v173
	s_mov_b64 s[98:99], 0x28000
	v_lshl_add_u64 v[168:169], v[166:167], 0, s[98:99]
	global_load_dwordx4 v[186:189], v[168:169], off
	v_pk_add_f32 v[72:73], v[72:73], v[88:89]
	v_pk_add_f32 v[76:77], v[76:77], v[92:93]
	v_lshlrev_b32_e32 v88, 16, v84
	v_mul_f32_e32 v76, 0xbfb8aa3b, v76
	v_mul_f32_e32 v77, 0xbfb8aa3b, v77
	v_exp_f32_e32 v76, v76
	v_exp_f32_e32 v77, v77
	v_and_b32_e32 v89, 0xffff0000, v84
	v_pk_add_f32 v[74:75], v[74:75], v[90:91]
	v_pk_add_f32 v[78:79], v[78:79], v[94:95]
	v_pk_add_f32 v[76:77], v[76:77], 1.0 op_sel_hi:[1,0]
	v_mul_f32_e32 v78, 0xbfb8aa3b, v78
	v_div_scale_f32 v84, s[14:15], v77, v77, 1.0
	v_rcp_f32_e32 v90, v84
	v_mul_f32_e32 v79, 0xbfb8aa3b, v79
	v_exp_f32_e32 v78, v78
	v_exp_f32_e32 v79, v79
	v_fma_f32 v91, -v84, v90, 1.0
	v_fmac_f32_e32 v90, v91, v90
	v_div_scale_f32 v91, vcc, 1.0, v77, 1.0
	v_mul_f32_e32 v92, v91, v90
	v_fma_f32 v93, -v84, v92, v91
	v_fmac_f32_e32 v92, v93, v90
	v_fma_f32 v84, -v84, v92, v91
	v_div_fmas_f32 v84, v84, v90, v92
	v_div_fixup_f32 v77, v84, v77, 1.0
	v_div_scale_f32 v84, s[14:15], v76, v76, 1.0
	v_rcp_f32_e32 v90, v84
	v_pk_add_f32 v[78:79], v[78:79], 1.0 op_sel_hi:[1,0]
	v_mul_f32_e32 v72, 0xbfb8aa3b, v72
	v_mul_f32_e32 v73, 0xbfb8aa3b, v73
	v_fma_f32 v91, -v84, v90, 1.0
	v_fmac_f32_e32 v90, v91, v90
	v_div_scale_f32 v91, vcc, 1.0, v76, 1.0
	v_mul_f32_e32 v92, v91, v90
	v_fma_f32 v93, -v84, v92, v91
	v_fmac_f32_e32 v92, v93, v90
	v_fma_f32 v84, -v84, v92, v91
	v_div_fmas_f32 v84, v84, v90, v92
	v_div_fixup_f32 v76, v84, v76, 1.0
	v_pk_mul_f32 v[76:77], v[76:77], v[88:89]
	v_div_scale_f32 v88, s[14:15], v79, v79, 1.0
	v_rcp_f32_e32 v89, v88
	v_exp_f32_e32 v72, v72
	v_exp_f32_e32 v73, v73
	v_lshlrev_b32_e32 v84, 16, v85
	v_fma_f32 v90, -v88, v89, 1.0
	v_fmac_f32_e32 v89, v90, v89
	v_div_scale_f32 v90, vcc, 1.0, v79, 1.0
	v_mul_f32_e32 v91, v90, v89
	v_fma_f32 v92, -v88, v91, v90
	v_fmac_f32_e32 v91, v92, v89
	v_fma_f32 v88, -v88, v91, v90
	v_div_fmas_f32 v88, v88, v89, v91
	v_div_fixup_f32 v79, v88, v79, 1.0
	v_div_scale_f32 v88, s[14:15], v78, v78, 1.0
	v_rcp_f32_e32 v89, v88
	v_and_b32_e32 v85, 0xffff0000, v85
	v_pk_add_f32 v[72:73], v[72:73], 1.0 op_sel_hi:[1,0]
	v_fma_f32 v90, -v88, v89, 1.0
	v_fmac_f32_e32 v89, v90, v89
	v_div_scale_f32 v90, vcc, 1.0, v78, 1.0
	v_mul_f32_e32 v91, v90, v89
	v_fma_f32 v92, -v88, v91, v90
	v_fmac_f32_e32 v91, v92, v89
	v_fma_f32 v88, -v88, v91, v90
	v_div_fmas_f32 v88, v88, v89, v91
	v_div_fixup_f32 v78, v88, v78, 1.0
	v_pk_mul_f32 v[78:79], v[78:79], v[84:85]
	v_lshlrev_b32_e32 v84, 16, v86
	v_and_b32_e32 v85, 0xffff0000, v86
	v_div_scale_f32 v86, s[14:15], v73, v73, 1.0
	v_rcp_f32_e32 v88, v86
	s_nop 0
	v_fma_f32 v89, -v86, v88, 1.0
	v_fmac_f32_e32 v88, v89, v88
	v_div_scale_f32 v89, vcc, 1.0, v73, 1.0
	v_mul_f32_e32 v90, v89, v88
	v_fma_f32 v91, -v86, v90, v89
	v_fmac_f32_e32 v90, v91, v88
	v_fma_f32 v86, -v86, v90, v89
	v_div_fmas_f32 v86, v86, v88, v90
	v_div_fixup_f32 v73, v86, v73, 1.0
	v_div_scale_f32 v86, s[14:15], v72, v72, 1.0
	v_rcp_f32_e32 v88, v86
	s_nop 0
	v_fma_f32 v89, -v86, v88, 1.0
	v_fmac_f32_e32 v88, v89, v88
	v_div_scale_f32 v89, vcc, 1.0, v72, 1.0
	v_mul_f32_e32 v90, v89, v88
	v_fma_f32 v91, -v86, v90, v89
	v_fmac_f32_e32 v90, v91, v88
	v_fma_f32 v86, -v86, v90, v89
	v_div_fmas_f32 v86, v86, v88, v90
	v_div_fixup_f32 v72, v86, v72, 1.0
	v_pk_mul_f32 v[84:85], v[72:73], v[84:85]
	v_mul_f32_e32 v72, 0xbfb8aa3b, v74
	v_mul_f32_e32 v73, 0xbfb8aa3b, v75
	v_exp_f32_e32 v72, v72
	v_exp_f32_e32 v73, v73
	v_lshlrev_b32_e32 v74, 16, v87
	v_and_b32_e32 v75, 0xffff0000, v87
	v_pk_add_f32 v[72:73], v[72:73], 1.0 op_sel_hi:[1,0]
	s_nop 0
	v_div_scale_f32 v86, s[14:15], v73, v73, 1.0
	v_rcp_f32_e32 v87, v86
	s_nop 0
	v_fma_f32 v88, -v86, v87, 1.0
	v_fmac_f32_e32 v87, v88, v87
	v_div_scale_f32 v88, vcc, 1.0, v73, 1.0
	v_mul_f32_e32 v89, v88, v87
	v_fma_f32 v90, -v86, v89, v88
	v_fmac_f32_e32 v89, v90, v87
	v_fma_f32 v86, -v86, v89, v88
	v_div_fmas_f32 v86, v86, v87, v89
	v_div_fixup_f32 v73, v86, v73, 1.0
	v_div_scale_f32 v86, s[14:15], v72, v72, 1.0
	v_rcp_f32_e32 v87, v86
	s_nop 0
	v_fma_f32 v88, -v86, v87, 1.0
	v_fmac_f32_e32 v87, v88, v87
	v_div_scale_f32 v88, vcc, 1.0, v72, 1.0
	v_mul_f32_e32 v89, v88, v87
	v_fma_f32 v90, -v86, v89, v88
	v_fmac_f32_e32 v89, v90, v87
	v_fma_f32 v86, -v86, v89, v88
	v_div_fmas_f32 v86, v86, v87, v89
	v_div_fixup_f32 v72, v86, v72, 1.0
	v_pk_mul_f32 v[86:87], v[72:73], v[74:75]
	v_cvt_pk_bf16_f32 v72, v76, v77
	v_lshl_add_u64 v[76:77], s[26:27], 0, v[80:81]
	v_cvt_pk_bf16_f32 v73, v78, v79
	v_cvt_pk_bf16_f32 v74, v84, v85
	v_cvt_pk_bf16_f32 v75, v86, v87
	v_lshl_add_u64 v[80:81], v[76:77], 0, v[142:143]
	global_store_dwordx4 v[80:81], v[72:75], off offset:1024
	s_nop 1
	s_nop 0
	s_waitcnt vmcnt(11)
; __device__ __forceinline__ float sigmoidf_(float x) { return 1.f / (1.f + __expf(-x)); }
; __device__ __forceinline__ unsigned cvt_pk_bf16(float lo, float hi) { const f32x2c v = {lo, hi}; const bf16x2c b = __builtin_convertvector(v, bf16x2c); return __builtin_bit_cast(unsigned, b); }
;     __device__ __forceinline__ void operator()(const f32x4 (&acc)[2][2][4][2], const Unit& u, int wr, int wc, int fr, int fq) const {
;     ...
;             for (int m = 0; m < 4; ++m) { const size_t row = (size_t)(row0 + ai * HALF + m * 16);
; #pragma unroll
;                 for (int bj = 0; bj < 2; ++bj) { const int col = col0 + bj * HALF;
;                     const u32x4 zz = *(const u32x4*)(Z + row * 512 + col);
;                     const f32x4 b0 = *(const f32x4*)(bias + col), b1 = *(const f32x4*)(bias + col + 4);
;                     const f32x4 v0 = acc[ai][bj][m][0] + b0, v1 = acc[ai][bj][m][1] + b1;
;                     float o[8]; const unsigned zw[4] = {zz.x, zz.y, zz.z, zz.w};
; #pragma unroll
;                     for (int q = 0; q < 4; ++q) { const float zl = __builtin_bit_cast(float, zw[q] << 16), zh = __builtin_bit_cast(float, zw[q] & 0xffff0000u);
;                         const float al = (q < 2) ? v0[2 * q] : v1[2 * q - 4], ah = (q < 2) ? v0[2 * q + 1] : v1[2 * q - 3];
;                         o[2 * q] = zl * sigmoidf_(al); o[2 * q + 1] = zh * sigmoidf_(ah); }
;                     u32x4 w; w.x = cvt_pk_bf16(o[0], o[1]); w.y = cvt_pk_bf16(o[2], o[3]); w.z = cvt_pk_bf16(o[4], o[5]); w.w = cvt_pk_bf16(o[6], o[7]);
;                     *(u32x4*)(YM + row * D + 512 + col) = w; } }
	v_mov_b32_e32 v72, v190
	v_mov_b32_e32 v73, v191
	v_mov_b32_e32 v74, v192
	v_mov_b32_e32 v75, v193
	v_mov_b32_e32 v76, v182
	v_mov_b32_e32 v77, v183
	v_mov_b32_e32 v78, v184
	v_mov_b32_e32 v79, v185
	v_mov_b32_e32 v82, v178
	v_mov_b32_e32 v83, v179
	v_mov_b32_e32 v84, v180
	v_mov_b32_e32 v85, v181
	global_load_dwordx4 v[190:193], v[168:169], off offset:256
	v_pk_add_f32 v[76:77], v[64:65], v[76:77]
	v_pk_add_f32 v[68:69], v[68:69], v[82:83]
	v_pk_add_f32 v[66:67], v[66:67], v[78:79]
	v_mul_f32_e32 v64, 0xbfb8aa3b, v68
	v_mul_f32_e32 v65, 0xbfb8aa3b, v69
	v_exp_f32_e32 v64, v64
	v_exp_f32_e32 v65, v65
	v_lshlrev_b32_e32 v68, 16, v72
	v_and_b32_e32 v69, 0xffff0000, v72
	v_pk_add_f32 v[70:71], v[70:71], v[84:85]
	v_pk_add_f32 v[64:65], v[64:65], 1.0 op_sel_hi:[1,0]
	v_mul_f32_e32 v66, 0xbfb8aa3b, v66
	v_div_scale_f32 v72, s[14:15], v65, v65, 1.0
	v_rcp_f32_e32 v78, v72
	v_mul_f32_e32 v67, 0xbfb8aa3b, v67
	v_exp_f32_e32 v66, v66
	v_exp_f32_e32 v67, v67
	v_fma_f32 v79, -v72, v78, 1.0
	v_fmac_f32_e32 v78, v79, v78
	v_div_scale_f32 v79, vcc, 1.0, v65, 1.0
	v_mul_f32_e32 v82, v79, v78
	v_fma_f32 v83, -v72, v82, v79
	v_fmac_f32_e32 v82, v83, v78
	v_fma_f32 v72, -v72, v82, v79
	v_div_fmas_f32 v72, v72, v78, v82
	v_div_fixup_f32 v65, v72, v65, 1.0
	v_div_scale_f32 v72, s[14:15], v64, v64, 1.0
	v_rcp_f32_e32 v78, v72
	v_pk_add_f32 v[66:67], v[66:67], 1.0 op_sel_hi:[1,0]
	v_fma_f32 v79, -v72, v78, 1.0
	v_fmac_f32_e32 v78, v79, v78
	v_div_scale_f32 v79, vcc, 1.0, v64, 1.0
	v_mul_f32_e32 v82, v79, v78
	v_fma_f32 v83, -v72, v82, v79
	v_fmac_f32_e32 v82, v83, v78
	v_fma_f32 v72, -v72, v82, v79
	v_div_fmas_f32 v72, v72, v78, v82
	v_div_fixup_f32 v64, v72, v64, 1.0
	v_pk_mul_f32 v[64:65], v[64:65], v[68:69]
	v_mul_f32_e32 v68, 0xbfb8aa3b, v70
	v_mul_f32_e32 v69, 0xbfb8aa3b, v71
	v_exp_f32_e32 v68, v68
	v_exp_f32_e32 v69, v69
	v_lshlrev_b32_e32 v70, 16, v73
	v_and_b32_e32 v71, 0xffff0000, v73
	v_cvt_pk_bf16_f32 v64, v64, v65
	v_pk_add_f32 v[68:69], v[68:69], 1.0 op_sel_hi:[1,0]
	s_nop 0
	v_div_scale_f32 v72, s[14:15], v69, v69, 1.0
	v_rcp_f32_e32 v73, v72
	s_nop 0
	v_fma_f32 v78, -v72, v73, 1.0
	v_fmac_f32_e32 v73, v78, v73
	v_div_scale_f32 v78, vcc, 1.0, v69, 1.0
	v_mul_f32_e32 v79, v78, v73
	v_fma_f32 v82, -v72, v79, v78
	v_fmac_f32_e32 v79, v82, v73
	v_fma_f32 v72, -v72, v79, v78
	v_div_fmas_f32 v72, v72, v73, v79
	v_div_fixup_f32 v69, v72, v69, 1.0
	v_div_scale_f32 v72, s[14:15], v68, v68, 1.0
	v_rcp_f32_e32 v73, v72
	s_nop 0
	v_fma_f32 v78, -v72, v73, 1.0
	v_fmac_f32_e32 v73, v78, v73
	v_div_scale_f32 v78, vcc, 1.0, v68, 1.0
	v_mul_f32_e32 v79, v78, v73
	v_fma_f32 v82, -v72, v79, v78
	v_fmac_f32_e32 v79, v82, v73
	v_fma_f32 v72, -v72, v79, v78
	v_div_fmas_f32 v72, v72, v73, v79
	v_div_fixup_f32 v68, v72, v68, 1.0
	v_pk_mul_f32 v[68:69], v[68:69], v[70:71]
	v_mul_f32_e32 v70, 0xbfb8aa3b, v76
	v_mul_f32_e32 v71, 0xbfb8aa3b, v77
	v_exp_f32_e32 v70, v70
	v_exp_f32_e32 v71, v71
	v_lshlrev_b32_e32 v72, 16, v74
	v_and_b32_e32 v73, 0xffff0000, v74
	v_cvt_pk_bf16_f32 v65, v68, v69
	v_pk_add_f32 v[70:71], v[70:71], 1.0 op_sel_hi:[1,0]
	s_nop 0
	v_div_scale_f32 v74, s[14:15], v71, v71, 1.0
	v_rcp_f32_e32 v76, v74
	s_nop 0
	v_fma_f32 v77, -v74, v76, 1.0
	v_fmac_f32_e32 v76, v77, v76
	v_div_scale_f32 v77, vcc, 1.0, v71, 1.0
	v_mul_f32_e32 v78, v77, v76
	v_fma_f32 v79, -v74, v78, v77
	v_fmac_f32_e32 v78, v79, v76
	v_fma_f32 v74, -v74, v78, v77
	v_div_fmas_f32 v74, v74, v76, v78
	v_div_fixup_f32 v71, v74, v71, 1.0
	v_div_scale_f32 v74, s[14:15], v70, v70, 1.0
	v_rcp_f32_e32 v76, v74
	s_nop 0
	v_fma_f32 v77, -v74, v76, 1.0
	v_fmac_f32_e32 v76, v77, v76
	v_div_scale_f32 v77, vcc, 1.0, v70, 1.0
	v_mul_f32_e32 v78, v77, v76
	v_fma_f32 v79, -v74, v78, v77
	v_fmac_f32_e32 v78, v79, v76
	v_fma_f32 v74, -v74, v78, v77
	v_div_fmas_f32 v74, v74, v76, v78
	v_div_fixup_f32 v70, v74, v70, 1.0
	v_div_scale_f32 v74, s[14:15], v67, v67, 1.0
	v_pk_mul_f32 v[70:71], v[70:71], v[72:73]
	v_lshlrev_b32_e32 v72, 16, v75
	v_and_b32_e32 v73, 0xffff0000, v75
	v_rcp_f32_e32 v75, v74
	s_nop 0
	v_fma_f32 v76, -v74, v75, 1.0
	v_fmac_f32_e32 v75, v76, v75
	v_div_scale_f32 v76, vcc, 1.0, v67, 1.0
	v_mul_f32_e32 v77, v76, v75
	v_fma_f32 v78, -v74, v77, v76
	v_fmac_f32_e32 v77, v78, v75
	v_fma_f32 v74, -v74, v77, v76
	v_div_fmas_f32 v74, v74, v75, v77
	v_div_fixup_f32 v67, v74, v67, 1.0
	v_div_scale_f32 v74, s[14:15], v66, v66, 1.0
	v_rcp_f32_e32 v75, v74
	s_nop 0
	v_fma_f32 v76, -v74, v75, 1.0
	v_fmac_f32_e32 v75, v76, v75
	v_div_scale_f32 v76, vcc, 1.0, v66, 1.0
	v_mul_f32_e32 v77, v76, v75
	v_fma_f32 v78, -v74, v77, v76
	v_fmac_f32_e32 v77, v78, v75
	v_fma_f32 v74, -v74, v77, v76
	v_div_fmas_f32 v74, v74, v75, v77
	v_div_fixup_f32 v66, v74, v66, 1.0
	v_pk_mul_f32 v[72:73], v[66:67], v[72:73]
	v_cvt_pk_bf16_f32 v66, v70, v71
	v_cvt_pk_bf16_f32 v67, v72, v73
	global_store_dwordx4 v[80:81], v[64:67], off offset:1280
	s_nop 1
	v_add_u32_e32 v64, 0x80, v144
	v_ashrrev_i32_e32 v65, 31, v64
	v_lshlrev_b64 v[66:67], 10, v[64:65]
	v_lshl_add_u64 v[66:67], s[36:37], 0, v[66:67]
	v_lshl_add_u64 v[66:67], v[66:67], 0, v[142:143]
	s_nop 1
	v_lshlrev_b64 v[64:65], 11, v[64:65]
	s_waitcnt vmcnt(11)
; __device__ __forceinline__ float sigmoidf_(float x) { return 1.f / (1.f + __expf(-x)); }
; __device__ __forceinline__ unsigned cvt_pk_bf16(float lo, float hi) { const f32x2c v = {lo, hi}; const bf16x2c b = __builtin_convertvector(v, bf16x2c); return __builtin_bit_cast(unsigned, b); }
;     __device__ __forceinline__ void operator()(const f32x4 (&acc)[2][2][4][2], const Unit& u, int wr, int wc, int fr, int fq) const {
;     ...
;             for (int m = 0; m < 4; ++m) { const size_t row = (size_t)(row0 + ai * HALF + m * 16);
; #pragma unroll
;                 for (int bj = 0; bj < 2; ++bj) { const int col = col0 + bj * HALF;
;                     const u32x4 zz = *(const u32x4*)(Z + row * 512 + col);
;                     const f32x4 b0 = *(const f32x4*)(bias + col), b1 = *(const f32x4*)(bias + col + 4);
;                     const f32x4 v0 = acc[ai][bj][m][0] + b0, v1 = acc[ai][bj][m][1] + b1;
;                     float o[8]; const unsigned zw[4] = {zz.x, zz.y, zz.z, zz.w};
; #pragma unroll
;                     for (int q = 0; q < 4; ++q) { const float zl = __builtin_bit_cast(float, zw[q] << 16), zh = __builtin_bit_cast(float, zw[q] & 0xffff0000u);
;                         const float al = (q < 2) ? v0[2 * q] : v1[2 * q - 4], ah = (q < 2) ? v0[2 * q + 1] : v1[2 * q - 3];
;                         o[2 * q] = zl * sigmoidf_(al); o[2 * q + 1] = zh * sigmoidf_(ah); }
;                     u32x4 w; w.x = cvt_pk_bf16(o[0], o[1]); w.y = cvt_pk_bf16(o[2], o[3]); w.z = cvt_pk_bf16(o[4], o[5]); w.w = cvt_pk_bf16(o[6], o[7]);
;                     *(u32x4*)(YM + row * D + 512 + col) = w; } }
	v_mov_b32_e32 v68, v198
	v_mov_b32_e32 v69, v199
	v_mov_b32_e32 v70, v200
	v_mov_b32_e32 v71, v201
	v_mov_b32_e32 v72, v174
	v_mov_b32_e32 v73, v175
	v_mov_b32_e32 v74, v176
	v_mov_b32_e32 v75, v177
	v_mov_b32_e32 v76, v170
	v_mov_b32_e32 v77, v171
	v_mov_b32_e32 v78, v172
	v_mov_b32_e32 v79, v173
	s_mov_b64 s[98:99], 0x2c000
	v_lshl_add_u64 v[168:169], v[166:167], 0, s[98:99]
	global_load_dwordx4 v[198:201], v[168:169], off
	v_pk_add_f32 v[56:57], v[56:57], v[72:73]
	v_pk_add_f32 v[60:61], v[60:61], v[76:77]
	v_lshlrev_b32_e32 v72, 16, v68
	v_mul_f32_e32 v60, 0xbfb8aa3b, v60
	v_mul_f32_e32 v61, 0xbfb8aa3b, v61
	v_exp_f32_e32 v60, v60
	v_exp_f32_e32 v61, v61
	v_and_b32_e32 v73, 0xffff0000, v68
	v_pk_add_f32 v[58:59], v[58:59], v[74:75]
	v_pk_add_f32 v[62:63], v[62:63], v[78:79]
	v_pk_add_f32 v[60:61], v[60:61], 1.0 op_sel_hi:[1,0]
	v_mul_f32_e32 v62, 0xbfb8aa3b, v62
	v_div_scale_f32 v68, s[14:15], v61, v61, 1.0
	v_rcp_f32_e32 v74, v68
	v_mul_f32_e32 v63, 0xbfb8aa3b, v63
	v_exp_f32_e32 v62, v62
	v_exp_f32_e32 v63, v63
	v_fma_f32 v75, -v68, v74, 1.0
	v_fmac_f32_e32 v74, v75, v74
	v_div_scale_f32 v75, vcc, 1.0, v61, 1.0
	v_mul_f32_e32 v76, v75, v74
	v_fma_f32 v77, -v68, v76, v75
	v_fmac_f32_e32 v76, v77, v74
	v_fma_f32 v68, -v68, v76, v75
	v_div_fmas_f32 v68, v68, v74, v76
	v_div_fixup_f32 v61, v68, v61, 1.0
	v_div_scale_f32 v68, s[14:15], v60, v60, 1.0
	v_rcp_f32_e32 v74, v68
	v_pk_add_f32 v[62:63], v[62:63], 1.0 op_sel_hi:[1,0]
	v_mul_f32_e32 v56, 0xbfb8aa3b, v56
	v_mul_f32_e32 v57, 0xbfb8aa3b, v57
	v_fma_f32 v75, -v68, v74, 1.0
	v_fmac_f32_e32 v74, v75, v74
	v_div_scale_f32 v75, vcc, 1.0, v60, 1.0
	v_mul_f32_e32 v76, v75, v74
	v_fma_f32 v77, -v68, v76, v75
	v_fmac_f32_e32 v76, v77, v74
	v_fma_f32 v68, -v68, v76, v75
	v_div_fmas_f32 v68, v68, v74, v76
	v_div_fixup_f32 v60, v68, v60, 1.0
	v_pk_mul_f32 v[60:61], v[60:61], v[72:73]
	v_div_scale_f32 v72, s[14:15], v63, v63, 1.0
	v_rcp_f32_e32 v73, v72
	v_exp_f32_e32 v56, v56
	v_exp_f32_e32 v57, v57
	v_lshlrev_b32_e32 v68, 16, v69
	v_fma_f32 v74, -v72, v73, 1.0
	v_fmac_f32_e32 v73, v74, v73
	v_div_scale_f32 v74, vcc, 1.0, v63, 1.0
	v_mul_f32_e32 v75, v74, v73
	v_fma_f32 v76, -v72, v75, v74
	v_fmac_f32_e32 v75, v76, v73
	v_fma_f32 v72, -v72, v75, v74
	v_div_fmas_f32 v72, v72, v73, v75
	v_div_fixup_f32 v63, v72, v63, 1.0
	v_div_scale_f32 v72, s[14:15], v62, v62, 1.0
	v_rcp_f32_e32 v73, v72
	v_and_b32_e32 v69, 0xffff0000, v69
	v_pk_add_f32 v[56:57], v[56:57], 1.0 op_sel_hi:[1,0]
	v_fma_f32 v74, -v72, v73, 1.0
	v_fmac_f32_e32 v73, v74, v73
	v_div_scale_f32 v74, vcc, 1.0, v62, 1.0
	v_mul_f32_e32 v75, v74, v73
	v_fma_f32 v76, -v72, v75, v74
	v_fmac_f32_e32 v75, v76, v73
	v_fma_f32 v72, -v72, v75, v74
	v_div_fmas_f32 v72, v72, v73, v75
	v_div_fixup_f32 v62, v72, v62, 1.0
	v_pk_mul_f32 v[62:63], v[62:63], v[68:69]
	v_lshlrev_b32_e32 v68, 16, v70
	v_and_b32_e32 v69, 0xffff0000, v70
	v_div_scale_f32 v70, s[14:15], v57, v57, 1.0
	v_rcp_f32_e32 v72, v70
	s_nop 0
	v_fma_f32 v73, -v70, v72, 1.0
	v_fmac_f32_e32 v72, v73, v72
	v_div_scale_f32 v73, vcc, 1.0, v57, 1.0
	v_mul_f32_e32 v74, v73, v72
	v_fma_f32 v75, -v70, v74, v73
	v_fmac_f32_e32 v74, v75, v72
	v_fma_f32 v70, -v70, v74, v73
	v_div_fmas_f32 v70, v70, v72, v74
	v_div_fixup_f32 v57, v70, v57, 1.0
	v_div_scale_f32 v70, s[14:15], v56, v56, 1.0
	v_rcp_f32_e32 v72, v70
	s_nop 0
	v_fma_f32 v73, -v70, v72, 1.0
	v_fmac_f32_e32 v72, v73, v72
	v_div_scale_f32 v73, vcc, 1.0, v56, 1.0
	v_mul_f32_e32 v74, v73, v72
	v_fma_f32 v75, -v70, v74, v73
	v_fmac_f32_e32 v74, v75, v72
	v_fma_f32 v70, -v70, v74, v73
	v_div_fmas_f32 v70, v70, v72, v74
	v_div_fixup_f32 v56, v70, v56, 1.0
	v_pk_mul_f32 v[68:69], v[56:57], v[68:69]
	v_mul_f32_e32 v56, 0xbfb8aa3b, v58
	v_mul_f32_e32 v57, 0xbfb8aa3b, v59
	v_exp_f32_e32 v56, v56
	v_exp_f32_e32 v57, v57
	v_lshlrev_b32_e32 v58, 16, v71
	v_and_b32_e32 v59, 0xffff0000, v71
	v_pk_add_f32 v[56:57], v[56:57], 1.0 op_sel_hi:[1,0]
	s_nop 0
	v_div_scale_f32 v70, s[14:15], v57, v57, 1.0
	v_rcp_f32_e32 v71, v70
	s_nop 0
	v_fma_f32 v72, -v70, v71, 1.0
	v_fmac_f32_e32 v71, v72, v71
	v_div_scale_f32 v72, vcc, 1.0, v57, 1.0
	v_mul_f32_e32 v73, v72, v71
	v_fma_f32 v74, -v70, v73, v72
	v_fmac_f32_e32 v73, v74, v71
	v_fma_f32 v70, -v70, v73, v72
	v_div_fmas_f32 v70, v70, v71, v73
	v_div_fixup_f32 v57, v70, v57, 1.0
	v_div_scale_f32 v70, s[14:15], v56, v56, 1.0
	v_rcp_f32_e32 v71, v70
	s_nop 0
	v_fma_f32 v72, -v70, v71, 1.0
	v_fmac_f32_e32 v71, v72, v71
	v_div_scale_f32 v72, vcc, 1.0, v56, 1.0
	v_mul_f32_e32 v73, v72, v71
	v_fma_f32 v74, -v70, v73, v72
	v_fmac_f32_e32 v73, v74, v71
	v_fma_f32 v70, -v70, v73, v72
	v_div_fmas_f32 v70, v70, v71, v73
	v_div_fixup_f32 v56, v70, v56, 1.0
	v_pk_mul_f32 v[70:71], v[56:57], v[58:59]
	v_cvt_pk_bf16_f32 v56, v60, v61
	v_lshl_add_u64 v[60:61], s[26:27], 0, v[64:65]
	v_cvt_pk_bf16_f32 v57, v62, v63
	v_cvt_pk_bf16_f32 v58, v68, v69
	v_cvt_pk_bf16_f32 v59, v70, v71
	v_lshl_add_u64 v[64:65], v[60:61], 0, v[142:143]
	global_store_dwordx4 v[64:65], v[56:59], off offset:1024
	s_nop 1
	s_nop 0
	s_waitcnt vmcnt(11)
; __device__ __forceinline__ float sigmoidf_(float x) { return 1.f / (1.f + __expf(-x)); }
; __device__ __forceinline__ unsigned cvt_pk_bf16(float lo, float hi) { const f32x2c v = {lo, hi}; const bf16x2c b = __builtin_convertvector(v, bf16x2c); return __builtin_bit_cast(unsigned, b); }
;     __device__ __forceinline__ void operator()(const f32x4 (&acc)[2][2][4][2], const Unit& u, int wr, int wc, int fr, int fq) const {
;     ...
;             for (int m = 0; m < 4; ++m) { const size_t row = (size_t)(row0 + ai * HALF + m * 16);
; #pragma unroll
;                 for (int bj = 0; bj < 2; ++bj) { const int col = col0 + bj * HALF;
;                     const u32x4 zz = *(const u32x4*)(Z + row * 512 + col);
;                     const f32x4 b0 = *(const f32x4*)(bias + col), b1 = *(const f32x4*)(bias + col + 4);
;                     const f32x4 v0 = acc[ai][bj][m][0] + b0, v1 = acc[ai][bj][m][1] + b1;
;                     float o[8]; const unsigned zw[4] = {zz.x, zz.y, zz.z, zz.w};
; #pragma unroll
;                     for (int q = 0; q < 4; ++q) { const float zl = __builtin_bit_cast(float, zw[q] << 16), zh = __builtin_bit_cast(float, zw[q] & 0xffff0000u);
;                         const float al = (q < 2) ? v0[2 * q] : v1[2 * q - 4], ah = (q < 2) ? v0[2 * q + 1] : v1[2 * q - 3];
;                         o[2 * q] = zl * sigmoidf_(al); o[2 * q + 1] = zh * sigmoidf_(ah); }
;                     u32x4 w; w.x = cvt_pk_bf16(o[0], o[1]); w.y = cvt_pk_bf16(o[2], o[3]); w.z = cvt_pk_bf16(o[4], o[5]); w.w = cvt_pk_bf16(o[6], o[7]);
;                     *(u32x4*)(YM + row * D + 512 + col) = w; } }
	v_mov_b32_e32 v56, v202
	v_mov_b32_e32 v57, v203
	v_mov_b32_e32 v58, v204
	v_mov_b32_e32 v59, v205
	v_mov_b32_e32 v60, v182
	v_mov_b32_e32 v61, v183
	v_mov_b32_e32 v62, v184
	v_mov_b32_e32 v63, v185
	v_mov_b32_e32 v66, v178
	v_mov_b32_e32 v67, v179
	v_mov_b32_e32 v68, v180
	v_mov_b32_e32 v69, v181
	global_load_dwordx4 v[202:205], v[168:169], off offset:256
	v_pk_add_f32 v[60:61], v[48:49], v[60:61]
	v_pk_add_f32 v[52:53], v[52:53], v[66:67]
	v_pk_add_f32 v[50:51], v[50:51], v[62:63]
	v_mul_f32_e32 v48, 0xbfb8aa3b, v52
	v_mul_f32_e32 v49, 0xbfb8aa3b, v53
	v_exp_f32_e32 v48, v48
	v_exp_f32_e32 v49, v49
	v_lshlrev_b32_e32 v52, 16, v56
	v_and_b32_e32 v53, 0xffff0000, v56
	v_pk_add_f32 v[54:55], v[54:55], v[68:69]
	v_pk_add_f32 v[48:49], v[48:49], 1.0 op_sel_hi:[1,0]
	v_mul_f32_e32 v50, 0xbfb8aa3b, v50
	v_div_scale_f32 v56, s[14:15], v49, v49, 1.0
	v_rcp_f32_e32 v62, v56
	v_mul_f32_e32 v51, 0xbfb8aa3b, v51
	v_exp_f32_e32 v50, v50
	v_exp_f32_e32 v51, v51
	v_fma_f32 v63, -v56, v62, 1.0
	v_fmac_f32_e32 v62, v63, v62
	v_div_scale_f32 v63, vcc, 1.0, v49, 1.0
	v_mul_f32_e32 v66, v63, v62
	v_fma_f32 v67, -v56, v66, v63
	v_fmac_f32_e32 v66, v67, v62
	v_fma_f32 v56, -v56, v66, v63
	v_div_fmas_f32 v56, v56, v62, v66
	v_div_fixup_f32 v49, v56, v49, 1.0
	v_div_scale_f32 v56, s[14:15], v48, v48, 1.0
	v_rcp_f32_e32 v62, v56
	v_pk_add_f32 v[50:51], v[50:51], 1.0 op_sel_hi:[1,0]
	v_fma_f32 v63, -v56, v62, 1.0
	v_fmac_f32_e32 v62, v63, v62
	v_div_scale_f32 v63, vcc, 1.0, v48, 1.0
	v_mul_f32_e32 v66, v63, v62
	v_fma_f32 v67, -v56, v66, v63
	v_fmac_f32_e32 v66, v67, v62
	v_fma_f32 v56, -v56, v66, v63
	v_div_fmas_f32 v56, v56, v62, v66
	v_div_fixup_f32 v48, v56, v48, 1.0
	v_pk_mul_f32 v[48:49], v[48:49], v[52:53]
	v_mul_f32_e32 v52, 0xbfb8aa3b, v54
	v_mul_f32_e32 v53, 0xbfb8aa3b, v55
	v_exp_f32_e32 v52, v52
	v_exp_f32_e32 v53, v53
	v_lshlrev_b32_e32 v54, 16, v57
	v_and_b32_e32 v55, 0xffff0000, v57
	v_cvt_pk_bf16_f32 v48, v48, v49
	v_pk_add_f32 v[52:53], v[52:53], 1.0 op_sel_hi:[1,0]
	s_nop 0
	v_div_scale_f32 v56, s[14:15], v53, v53, 1.0
	v_rcp_f32_e32 v57, v56
	s_nop 0
	v_fma_f32 v62, -v56, v57, 1.0
	v_fmac_f32_e32 v57, v62, v57
	v_div_scale_f32 v62, vcc, 1.0, v53, 1.0
	v_mul_f32_e32 v63, v62, v57
	v_fma_f32 v66, -v56, v63, v62
	v_fmac_f32_e32 v63, v66, v57
	v_fma_f32 v56, -v56, v63, v62
	v_div_fmas_f32 v56, v56, v57, v63
	v_div_fixup_f32 v53, v56, v53, 1.0
	v_div_scale_f32 v56, s[14:15], v52, v52, 1.0
	v_rcp_f32_e32 v57, v56
	s_nop 0
	v_fma_f32 v62, -v56, v57, 1.0
	v_fmac_f32_e32 v57, v62, v57
	v_div_scale_f32 v62, vcc, 1.0, v52, 1.0
	v_mul_f32_e32 v63, v62, v57
	v_fma_f32 v66, -v56, v63, v62
	v_fmac_f32_e32 v63, v66, v57
	v_fma_f32 v56, -v56, v63, v62
	v_div_fmas_f32 v56, v56, v57, v63
	v_div_fixup_f32 v52, v56, v52, 1.0
	v_pk_mul_f32 v[52:53], v[52:53], v[54:55]
	v_mul_f32_e32 v54, 0xbfb8aa3b, v60
	v_mul_f32_e32 v55, 0xbfb8aa3b, v61
	v_exp_f32_e32 v54, v54
	v_exp_f32_e32 v55, v55
	v_lshlrev_b32_e32 v56, 16, v58
	v_and_b32_e32 v57, 0xffff0000, v58
	v_cvt_pk_bf16_f32 v49, v52, v53
	v_pk_add_f32 v[54:55], v[54:55], 1.0 op_sel_hi:[1,0]
	s_nop 0
	v_div_scale_f32 v58, s[14:15], v55, v55, 1.0
	v_rcp_f32_e32 v60, v58
	s_nop 0
	v_fma_f32 v61, -v58, v60, 1.0
	v_fmac_f32_e32 v60, v61, v60
	v_div_scale_f32 v61, vcc, 1.0, v55, 1.0
	v_mul_f32_e32 v62, v61, v60
	v_fma_f32 v63, -v58, v62, v61
	v_fmac_f32_e32 v62, v63, v60
	v_fma_f32 v58, -v58, v62, v61
	v_div_fmas_f32 v58, v58, v60, v62
	v_div_fixup_f32 v55, v58, v55, 1.0
	v_div_scale_f32 v58, s[14:15], v54, v54, 1.0
	v_rcp_f32_e32 v60, v58
	s_nop 0
	v_fma_f32 v61, -v58, v60, 1.0
	v_fmac_f32_e32 v60, v61, v60
	v_div_scale_f32 v61, vcc, 1.0, v54, 1.0
	v_mul_f32_e32 v62, v61, v60
	v_fma_f32 v63, -v58, v62, v61
	v_fmac_f32_e32 v62, v63, v60
	v_fma_f32 v58, -v58, v62, v61
	v_div_fmas_f32 v58, v58, v60, v62
	v_div_fixup_f32 v54, v58, v54, 1.0
	v_div_scale_f32 v58, s[14:15], v51, v51, 1.0
	v_pk_mul_f32 v[54:55], v[54:55], v[56:57]
	v_lshlrev_b32_e32 v56, 16, v59
	v_and_b32_e32 v57, 0xffff0000, v59
	v_rcp_f32_e32 v59, v58
	s_nop 0
	v_fma_f32 v60, -v58, v59, 1.0
	v_fmac_f32_e32 v59, v60, v59
	v_div_scale_f32 v60, vcc, 1.0, v51, 1.0
	v_mul_f32_e32 v61, v60, v59
	v_fma_f32 v62, -v58, v61, v60
	v_fmac_f32_e32 v61, v62, v59
	v_fma_f32 v58, -v58, v61, v60
	v_div_fmas_f32 v58, v58, v59, v61
	v_div_fixup_f32 v51, v58, v51, 1.0
	v_div_scale_f32 v58, s[14:15], v50, v50, 1.0
	v_rcp_f32_e32 v59, v58
	s_nop 0
	v_fma_f32 v60, -v58, v59, 1.0
	v_fmac_f32_e32 v59, v60, v59
	v_div_scale_f32 v60, vcc, 1.0, v50, 1.0
	v_mul_f32_e32 v61, v60, v59
	v_fma_f32 v62, -v58, v61, v60
	v_fmac_f32_e32 v61, v62, v59
	v_fma_f32 v58, -v58, v61, v60
	v_div_fmas_f32 v58, v58, v59, v61
	v_div_fixup_f32 v50, v58, v50, 1.0
	v_pk_mul_f32 v[56:57], v[50:51], v[56:57]
	v_cvt_pk_bf16_f32 v50, v54, v55
	v_cvt_pk_bf16_f32 v51, v56, v57
	global_store_dwordx4 v[64:65], v[48:51], off offset:1280
	s_nop 1
	v_add_u32_e32 v48, 0x90, v144
	v_ashrrev_i32_e32 v49, 31, v48
	v_lshlrev_b64 v[50:51], 10, v[48:49]
	v_lshl_add_u64 v[50:51], s[36:37], 0, v[50:51]
	v_lshl_add_u64 v[50:51], v[50:51], 0, v[142:143]
	s_nop 1
	v_lshlrev_b64 v[48:49], 11, v[48:49]
	s_waitcnt vmcnt(11)
; __device__ __forceinline__ float sigmoidf_(float x) { return 1.f / (1.f + __expf(-x)); }
; __device__ __forceinline__ unsigned cvt_pk_bf16(float lo, float hi) { const f32x2c v = {lo, hi}; const bf16x2c b = __builtin_convertvector(v, bf16x2c); return __builtin_bit_cast(unsigned, b); }
;     __device__ __forceinline__ void operator()(const f32x4 (&acc)[2][2][4][2], const Unit& u, int wr, int wc, int fr, int fq) const {
;     ...
;             for (int m = 0; m < 4; ++m) { const size_t row = (size_t)(row0 + ai * HALF + m * 16);
; #pragma unroll
;                 for (int bj = 0; bj < 2; ++bj) { const int col = col0 + bj * HALF;
;                     const u32x4 zz = *(const u32x4*)(Z + row * 512 + col);
;                     const f32x4 b0 = *(const f32x4*)(bias + col), b1 = *(const f32x4*)(bias + col + 4);
;                     const f32x4 v0 = acc[ai][bj][m][0] + b0, v1 = acc[ai][bj][m][1] + b1;
;                     float o[8]; const unsigned zw[4] = {zz.x, zz.y, zz.z, zz.w};
; #pragma unroll
;                     for (int q = 0; q < 4; ++q) { const float zl = __builtin_bit_cast(float, zw[q] << 16), zh = __builtin_bit_cast(float, zw[q] & 0xffff0000u);
;                         const float al = (q < 2) ? v0[2 * q] : v1[2 * q - 4], ah = (q < 2) ? v0[2 * q + 1] : v1[2 * q - 3];
;                         o[2 * q] = zl * sigmoidf_(al); o[2 * q + 1] = zh * sigmoidf_(ah); }
;                     u32x4 w; w.x = cvt_pk_bf16(o[0], o[1]); w.y = cvt_pk_bf16(o[2], o[3]); w.z = cvt_pk_bf16(o[4], o[5]); w.w = cvt_pk_bf16(o[6], o[7]);
;                     *(u32x4*)(YM + row * D + 512 + col) = w; } }
	v_mov_b32_e32 v52, v206
	v_mov_b32_e32 v53, v207
	v_mov_b32_e32 v54, v208
	v_mov_b32_e32 v55, v209
	v_mov_b32_e32 v56, v174
	v_mov_b32_e32 v57, v175
	v_mov_b32_e32 v58, v176
	v_mov_b32_e32 v59, v177
	v_mov_b32_e32 v60, v170
	v_mov_b32_e32 v61, v171
	v_mov_b32_e32 v62, v172
	v_mov_b32_e32 v63, v173
	v_pk_add_f32 v[40:41], v[40:41], v[56:57]
	v_pk_add_f32 v[44:45], v[44:45], v[60:61]
	v_lshlrev_b32_e32 v56, 16, v52
	v_mul_f32_e32 v44, 0xbfb8aa3b, v44
	v_mul_f32_e32 v45, 0xbfb8aa3b, v45
	v_exp_f32_e32 v44, v44
	v_exp_f32_e32 v45, v45
	v_and_b32_e32 v57, 0xffff0000, v52
	v_pk_add_f32 v[42:43], v[42:43], v[58:59]
	v_pk_add_f32 v[46:47], v[46:47], v[62:63]
	v_pk_add_f32 v[44:45], v[44:45], 1.0 op_sel_hi:[1,0]
	v_mul_f32_e32 v46, 0xbfb8aa3b, v46
	v_div_scale_f32 v52, s[14:15], v45, v45, 1.0
	v_rcp_f32_e32 v58, v52
	v_mul_f32_e32 v47, 0xbfb8aa3b, v47
	v_exp_f32_e32 v46, v46
	v_exp_f32_e32 v47, v47
	v_fma_f32 v59, -v52, v58, 1.0
	v_fmac_f32_e32 v58, v59, v58
	v_div_scale_f32 v59, vcc, 1.0, v45, 1.0
	v_mul_f32_e32 v60, v59, v58
	v_fma_f32 v61, -v52, v60, v59
	v_fmac_f32_e32 v60, v61, v58
	v_fma_f32 v52, -v52, v60, v59
	v_div_fmas_f32 v52, v52, v58, v60
	v_div_fixup_f32 v45, v52, v45, 1.0
	v_div_scale_f32 v52, s[14:15], v44, v44, 1.0
	v_rcp_f32_e32 v58, v52
	v_pk_add_f32 v[46:47], v[46:47], 1.0 op_sel_hi:[1,0]
	v_mul_f32_e32 v40, 0xbfb8aa3b, v40
	v_mul_f32_e32 v41, 0xbfb8aa3b, v41
	v_fma_f32 v59, -v52, v58, 1.0
	v_fmac_f32_e32 v58, v59, v58
	v_div_scale_f32 v59, vcc, 1.0, v44, 1.0
	v_mul_f32_e32 v60, v59, v58
	v_fma_f32 v61, -v52, v60, v59
	v_fmac_f32_e32 v60, v61, v58
	v_fma_f32 v52, -v52, v60, v59
	v_div_fmas_f32 v52, v52, v58, v60
	v_div_fixup_f32 v44, v52, v44, 1.0
	v_pk_mul_f32 v[44:45], v[44:45], v[56:57]
	v_div_scale_f32 v56, s[14:15], v47, v47, 1.0
	v_rcp_f32_e32 v57, v56
	v_exp_f32_e32 v40, v40
	v_exp_f32_e32 v41, v41
	v_lshlrev_b32_e32 v52, 16, v53
	v_fma_f32 v58, -v56, v57, 1.0
	v_fmac_f32_e32 v57, v58, v57
	v_div_scale_f32 v58, vcc, 1.0, v47, 1.0
	v_mul_f32_e32 v59, v58, v57
	v_fma_f32 v60, -v56, v59, v58
	v_fmac_f32_e32 v59, v60, v57
	v_fma_f32 v56, -v56, v59, v58
	v_div_fmas_f32 v56, v56, v57, v59
	v_div_fixup_f32 v47, v56, v47, 1.0
	v_div_scale_f32 v56, s[14:15], v46, v46, 1.0
	v_rcp_f32_e32 v57, v56
	v_and_b32_e32 v53, 0xffff0000, v53
	v_pk_add_f32 v[40:41], v[40:41], 1.0 op_sel_hi:[1,0]
	v_fma_f32 v58, -v56, v57, 1.0
	v_fmac_f32_e32 v57, v58, v57
	v_div_scale_f32 v58, vcc, 1.0, v46, 1.0
	v_mul_f32_e32 v59, v58, v57
	v_fma_f32 v60, -v56, v59, v58
	v_fmac_f32_e32 v59, v60, v57
	v_fma_f32 v56, -v56, v59, v58
	v_div_fmas_f32 v56, v56, v57, v59
	v_div_fixup_f32 v46, v56, v46, 1.0
	v_pk_mul_f32 v[46:47], v[46:47], v[52:53]
	v_lshlrev_b32_e32 v52, 16, v54
	v_and_b32_e32 v53, 0xffff0000, v54
	v_div_scale_f32 v54, s[14:15], v41, v41, 1.0
	v_rcp_f32_e32 v56, v54
	s_nop 0
	v_fma_f32 v57, -v54, v56, 1.0
	v_fmac_f32_e32 v56, v57, v56
	v_div_scale_f32 v57, vcc, 1.0, v41, 1.0
	v_mul_f32_e32 v58, v57, v56
	v_fma_f32 v59, -v54, v58, v57
	v_fmac_f32_e32 v58, v59, v56
	v_fma_f32 v54, -v54, v58, v57
	v_div_fmas_f32 v54, v54, v56, v58
	v_div_fixup_f32 v41, v54, v41, 1.0
	v_div_scale_f32 v54, s[14:15], v40, v40, 1.0
	v_rcp_f32_e32 v56, v54
	s_nop 0
	v_fma_f32 v57, -v54, v56, 1.0
	v_fmac_f32_e32 v56, v57, v56
	v_div_scale_f32 v57, vcc, 1.0, v40, 1.0
	v_mul_f32_e32 v58, v57, v56
	v_fma_f32 v59, -v54, v58, v57
	v_fmac_f32_e32 v58, v59, v56
	v_fma_f32 v54, -v54, v58, v57
	v_div_fmas_f32 v54, v54, v56, v58
	v_div_fixup_f32 v40, v54, v40, 1.0
	v_pk_mul_f32 v[52:53], v[40:41], v[52:53]
	v_mul_f32_e32 v40, 0xbfb8aa3b, v42
	v_mul_f32_e32 v41, 0xbfb8aa3b, v43
	v_exp_f32_e32 v40, v40
	v_exp_f32_e32 v41, v41
	v_lshlrev_b32_e32 v42, 16, v55
	v_and_b32_e32 v43, 0xffff0000, v55
	v_pk_add_f32 v[40:41], v[40:41], 1.0 op_sel_hi:[1,0]
	s_nop 0
	v_div_scale_f32 v54, s[14:15], v41, v41, 1.0
	v_rcp_f32_e32 v55, v54
	s_nop 0
	v_fma_f32 v56, -v54, v55, 1.0
	v_fmac_f32_e32 v55, v56, v55
	v_div_scale_f32 v56, vcc, 1.0, v41, 1.0
	v_mul_f32_e32 v57, v56, v55
	v_fma_f32 v58, -v54, v57, v56
	v_fmac_f32_e32 v57, v58, v55
	v_fma_f32 v54, -v54, v57, v56
	v_div_fmas_f32 v54, v54, v55, v57
	v_div_fixup_f32 v41, v54, v41, 1.0
	v_div_scale_f32 v54, s[14:15], v40, v40, 1.0
	v_rcp_f32_e32 v55, v54
	s_nop 0
	v_fma_f32 v56, -v54, v55, 1.0
	v_fmac_f32_e32 v55, v56, v55
	v_div_scale_f32 v56, vcc, 1.0, v40, 1.0
	v_mul_f32_e32 v57, v56, v55
	v_fma_f32 v58, -v54, v57, v56
	v_fmac_f32_e32 v57, v58, v55
	v_fma_f32 v54, -v54, v57, v56
	v_div_fmas_f32 v54, v54, v55, v57
	v_div_fixup_f32 v40, v54, v40, 1.0
	v_pk_mul_f32 v[54:55], v[40:41], v[42:43]
	v_cvt_pk_bf16_f32 v40, v44, v45
	v_lshl_add_u64 v[44:45], s[26:27], 0, v[48:49]
	v_cvt_pk_bf16_f32 v41, v46, v47
	v_cvt_pk_bf16_f32 v42, v52, v53
	v_cvt_pk_bf16_f32 v43, v54, v55
	v_lshl_add_u64 v[48:49], v[44:45], 0, v[142:143]
	global_store_dwordx4 v[48:49], v[40:43], off offset:1024
	s_nop 1
	s_nop 0
	s_waitcnt vmcnt(10)
; __device__ __forceinline__ float sigmoidf_(float x) { return 1.f / (1.f + __expf(-x)); }
; __device__ __forceinline__ unsigned cvt_pk_bf16(float lo, float hi) { const f32x2c v = {lo, hi}; const bf16x2c b = __builtin_convertvector(v, bf16x2c); return __builtin_bit_cast(unsigned, b); }
;     __device__ __forceinline__ void operator()(const f32x4 (&acc)[2][2][4][2], const Unit& u, int wr, int wc, int fr, int fq) const {
;     ...
;             for (int m = 0; m < 4; ++m) { const size_t row = (size_t)(row0 + ai * HALF + m * 16);
; #pragma unroll
;                 for (int bj = 0; bj < 2; ++bj) { const int col = col0 + bj * HALF;
;                     const u32x4 zz = *(const u32x4*)(Z + row * 512 + col);
;                     const f32x4 b0 = *(const f32x4*)(bias + col), b1 = *(const f32x4*)(bias + col + 4);
;                     const f32x4 v0 = acc[ai][bj][m][0] + b0, v1 = acc[ai][bj][m][1] + b1;
;                     float o[8]; const unsigned zw[4] = {zz.x, zz.y, zz.z, zz.w};
; #pragma unroll
;                     for (int q = 0; q < 4; ++q) { const float zl = __builtin_bit_cast(float, zw[q] << 16), zh = __builtin_bit_cast(float, zw[q] & 0xffff0000u);
;                         const float al = (q < 2) ? v0[2 * q] : v1[2 * q - 4], ah = (q < 2) ? v0[2 * q + 1] : v1[2 * q - 3];
;                         o[2 * q] = zl * sigmoidf_(al); o[2 * q + 1] = zh * sigmoidf_(ah); }
;                     u32x4 w; w.x = cvt_pk_bf16(o[0], o[1]); w.y = cvt_pk_bf16(o[2], o[3]); w.z = cvt_pk_bf16(o[4], o[5]); w.w = cvt_pk_bf16(o[6], o[7]);
;                     *(u32x4*)(YM + row * D + 512 + col) = w; } }
	v_mov_b32_e32 v40, v210
	v_mov_b32_e32 v41, v211
	v_mov_b32_e32 v42, v212
	v_mov_b32_e32 v43, v213
	v_mov_b32_e32 v44, v182
	v_mov_b32_e32 v45, v183
	v_mov_b32_e32 v46, v184
	v_mov_b32_e32 v47, v185
	v_mov_b32_e32 v50, v178
	v_mov_b32_e32 v51, v179
	v_mov_b32_e32 v52, v180
	v_mov_b32_e32 v53, v181
	v_pk_add_f32 v[44:45], v[32:33], v[44:45]
	v_pk_add_f32 v[36:37], v[36:37], v[50:51]
	v_pk_add_f32 v[34:35], v[34:35], v[46:47]
	v_mul_f32_e32 v32, 0xbfb8aa3b, v36
	v_mul_f32_e32 v33, 0xbfb8aa3b, v37
	v_exp_f32_e32 v32, v32
	v_exp_f32_e32 v33, v33
	v_lshlrev_b32_e32 v36, 16, v40
	v_and_b32_e32 v37, 0xffff0000, v40
	v_pk_add_f32 v[38:39], v[38:39], v[52:53]
	v_pk_add_f32 v[32:33], v[32:33], 1.0 op_sel_hi:[1,0]
	v_mul_f32_e32 v34, 0xbfb8aa3b, v34
	v_div_scale_f32 v40, s[14:15], v33, v33, 1.0
	v_rcp_f32_e32 v46, v40
	v_mul_f32_e32 v35, 0xbfb8aa3b, v35
	v_exp_f32_e32 v34, v34
	v_exp_f32_e32 v35, v35
	v_fma_f32 v47, -v40, v46, 1.0
	v_fmac_f32_e32 v46, v47, v46
	v_div_scale_f32 v47, vcc, 1.0, v33, 1.0
	v_mul_f32_e32 v50, v47, v46
	v_fma_f32 v51, -v40, v50, v47
	v_fmac_f32_e32 v50, v51, v46
	v_fma_f32 v40, -v40, v50, v47
	v_div_fmas_f32 v40, v40, v46, v50
	v_div_fixup_f32 v33, v40, v33, 1.0
	v_div_scale_f32 v40, s[14:15], v32, v32, 1.0
	v_rcp_f32_e32 v46, v40
	v_pk_add_f32 v[34:35], v[34:35], 1.0 op_sel_hi:[1,0]
	v_fma_f32 v47, -v40, v46, 1.0
	v_fmac_f32_e32 v46, v47, v46
	v_div_scale_f32 v47, vcc, 1.0, v32, 1.0
	v_mul_f32_e32 v50, v47, v46
	v_fma_f32 v51, -v40, v50, v47
	v_fmac_f32_e32 v50, v51, v46
	v_fma_f32 v40, -v40, v50, v47
	v_div_fmas_f32 v40, v40, v46, v50
	v_div_fixup_f32 v32, v40, v32, 1.0
	v_pk_mul_f32 v[32:33], v[32:33], v[36:37]
	v_mul_f32_e32 v36, 0xbfb8aa3b, v38
	v_mul_f32_e32 v37, 0xbfb8aa3b, v39
	v_exp_f32_e32 v36, v36
	v_exp_f32_e32 v37, v37
	v_lshlrev_b32_e32 v38, 16, v41
	v_and_b32_e32 v39, 0xffff0000, v41
	v_cvt_pk_bf16_f32 v32, v32, v33
	v_pk_add_f32 v[36:37], v[36:37], 1.0 op_sel_hi:[1,0]
	s_nop 0
	v_div_scale_f32 v40, s[14:15], v37, v37, 1.0
	v_rcp_f32_e32 v41, v40
	s_nop 0
	v_fma_f32 v46, -v40, v41, 1.0
	v_fmac_f32_e32 v41, v46, v41
	v_div_scale_f32 v46, vcc, 1.0, v37, 1.0
	v_mul_f32_e32 v47, v46, v41
	v_fma_f32 v50, -v40, v47, v46
	v_fmac_f32_e32 v47, v50, v41
	v_fma_f32 v40, -v40, v47, v46
	v_div_fmas_f32 v40, v40, v41, v47
	v_div_fixup_f32 v37, v40, v37, 1.0
	v_div_scale_f32 v40, s[14:15], v36, v36, 1.0
	v_rcp_f32_e32 v41, v40
	s_nop 0
	v_fma_f32 v46, -v40, v41, 1.0
	v_fmac_f32_e32 v41, v46, v41
	v_div_scale_f32 v46, vcc, 1.0, v36, 1.0
	v_mul_f32_e32 v47, v46, v41
	v_fma_f32 v50, -v40, v47, v46
	v_fmac_f32_e32 v47, v50, v41
	v_fma_f32 v40, -v40, v47, v46
	v_div_fmas_f32 v40, v40, v41, v47
	v_div_fixup_f32 v36, v40, v36, 1.0
	v_pk_mul_f32 v[36:37], v[36:37], v[38:39]
	v_mul_f32_e32 v38, 0xbfb8aa3b, v44
	v_mul_f32_e32 v39, 0xbfb8aa3b, v45
	v_exp_f32_e32 v38, v38
	v_exp_f32_e32 v39, v39
	v_lshlrev_b32_e32 v40, 16, v42
	v_and_b32_e32 v41, 0xffff0000, v42
	v_cvt_pk_bf16_f32 v33, v36, v37
	v_pk_add_f32 v[38:39], v[38:39], 1.0 op_sel_hi:[1,0]
	s_nop 0
	v_div_scale_f32 v42, s[14:15], v39, v39, 1.0
	v_rcp_f32_e32 v44, v42
	s_nop 0
	v_fma_f32 v45, -v42, v44, 1.0
	v_fmac_f32_e32 v44, v45, v44
	v_div_scale_f32 v45, vcc, 1.0, v39, 1.0
	v_mul_f32_e32 v46, v45, v44
	v_fma_f32 v47, -v42, v46, v45
	v_fmac_f32_e32 v46, v47, v44
	v_fma_f32 v42, -v42, v46, v45
	v_div_fmas_f32 v42, v42, v44, v46
	v_div_fixup_f32 v39, v42, v39, 1.0
	v_div_scale_f32 v42, s[14:15], v38, v38, 1.0
	v_rcp_f32_e32 v44, v42
	s_nop 0
	v_fma_f32 v45, -v42, v44, 1.0
	v_fmac_f32_e32 v44, v45, v44
	v_div_scale_f32 v45, vcc, 1.0, v38, 1.0
	v_mul_f32_e32 v46, v45, v44
	v_fma_f32 v47, -v42, v46, v45
	v_fmac_f32_e32 v46, v47, v44
	v_fma_f32 v42, -v42, v46, v45
	v_div_fmas_f32 v42, v42, v44, v46
	v_div_fixup_f32 v38, v42, v38, 1.0
	v_div_scale_f32 v42, s[14:15], v35, v35, 1.0
	v_pk_mul_f32 v[38:39], v[38:39], v[40:41]
	v_lshlrev_b32_e32 v40, 16, v43
	v_and_b32_e32 v41, 0xffff0000, v43
	v_rcp_f32_e32 v43, v42
	s_nop 0
	v_fma_f32 v44, -v42, v43, 1.0
	v_fmac_f32_e32 v43, v44, v43
	v_div_scale_f32 v44, vcc, 1.0, v35, 1.0
	v_mul_f32_e32 v45, v44, v43
	v_fma_f32 v46, -v42, v45, v44
	v_fmac_f32_e32 v45, v46, v43
	v_fma_f32 v42, -v42, v45, v44
	v_div_fmas_f32 v42, v42, v43, v45
	v_div_fixup_f32 v35, v42, v35, 1.0
	v_div_scale_f32 v42, s[14:15], v34, v34, 1.0
	v_rcp_f32_e32 v43, v42
	s_nop 0
	v_fma_f32 v44, -v42, v43, 1.0
	v_fmac_f32_e32 v43, v44, v43
	v_div_scale_f32 v44, vcc, 1.0, v34, 1.0
	v_mul_f32_e32 v45, v44, v43
	v_fma_f32 v46, -v42, v45, v44
	v_fmac_f32_e32 v45, v46, v43
	v_fma_f32 v42, -v42, v45, v44
	v_div_fmas_f32 v42, v42, v43, v45
	v_div_fixup_f32 v34, v42, v34, 1.0
	v_pk_mul_f32 v[40:41], v[34:35], v[40:41]
	v_cvt_pk_bf16_f32 v34, v38, v39
	v_cvt_pk_bf16_f32 v35, v40, v41
	global_store_dwordx4 v[48:49], v[32:35], off offset:1280
	s_nop 1
	v_add_u32_e32 v32, 0xa0, v144
	v_ashrrev_i32_e32 v33, 31, v32
	v_lshlrev_b64 v[34:35], 10, v[32:33]
	v_lshl_add_u64 v[34:35], s[36:37], 0, v[34:35]
	v_lshl_add_u64 v[34:35], v[34:35], 0, v[142:143]
	s_nop 1
	v_lshlrev_b64 v[32:33], 11, v[32:33]
	s_waitcnt vmcnt(9)
; __device__ __forceinline__ float sigmoidf_(float x) { return 1.f / (1.f + __expf(-x)); }
; __device__ __forceinline__ unsigned cvt_pk_bf16(float lo, float hi) { const f32x2c v = {lo, hi}; const bf16x2c b = __builtin_convertvector(v, bf16x2c); return __builtin_bit_cast(unsigned, b); }
;     __device__ __forceinline__ void operator()(const f32x4 (&acc)[2][2][4][2], const Unit& u, int wr, int wc, int fr, int fq) const {
;     ...
;             for (int m = 0; m < 4; ++m) { const size_t row = (size_t)(row0 + ai * HALF + m * 16);
; #pragma unroll
;                 for (int bj = 0; bj < 2; ++bj) { const int col = col0 + bj * HALF;
;                     const u32x4 zz = *(const u32x4*)(Z + row * 512 + col);
;                     const f32x4 b0 = *(const f32x4*)(bias + col), b1 = *(const f32x4*)(bias + col + 4);
;                     const f32x4 v0 = acc[ai][bj][m][0] + b0, v1 = acc[ai][bj][m][1] + b1;
;                     float o[8]; const unsigned zw[4] = {zz.x, zz.y, zz.z, zz.w};
; #pragma unroll
;                     for (int q = 0; q < 4; ++q) { const float zl = __builtin_bit_cast(float, zw[q] << 16), zh = __builtin_bit_cast(float, zw[q] & 0xffff0000u);
;                         const float al = (q < 2) ? v0[2 * q] : v1[2 * q - 4], ah = (q < 2) ? v0[2 * q + 1] : v1[2 * q - 3];
;                         o[2 * q] = zl * sigmoidf_(al); o[2 * q + 1] = zh * sigmoidf_(ah); }
;                     u32x4 w; w.x = cvt_pk_bf16(o[0], o[1]); w.y = cvt_pk_bf16(o[2], o[3]); w.z = cvt_pk_bf16(o[4], o[5]); w.w = cvt_pk_bf16(o[6], o[7]);
;                     *(u32x4*)(YM + row * D + 512 + col) = w; } }
	v_mov_b32_e32 v36, v186
	v_mov_b32_e32 v37, v187
	v_mov_b32_e32 v38, v188
	v_mov_b32_e32 v39, v189
	v_mov_b32_e32 v40, v174
	v_mov_b32_e32 v41, v175
	v_mov_b32_e32 v42, v176
	v_mov_b32_e32 v43, v177
	v_mov_b32_e32 v44, v170
	v_mov_b32_e32 v45, v171
	v_mov_b32_e32 v46, v172
	v_mov_b32_e32 v47, v173
	v_pk_add_f32 v[24:25], v[24:25], v[40:41]
	v_pk_add_f32 v[28:29], v[28:29], v[44:45]
	v_lshlrev_b32_e32 v40, 16, v36
	v_mul_f32_e32 v28, 0xbfb8aa3b, v28
	v_mul_f32_e32 v29, 0xbfb8aa3b, v29
	v_exp_f32_e32 v28, v28
	v_exp_f32_e32 v29, v29
	v_and_b32_e32 v41, 0xffff0000, v36
	v_pk_add_f32 v[26:27], v[26:27], v[42:43]
	v_pk_add_f32 v[30:31], v[30:31], v[46:47]
	v_pk_add_f32 v[28:29], v[28:29], 1.0 op_sel_hi:[1,0]
	v_mul_f32_e32 v30, 0xbfb8aa3b, v30
	v_div_scale_f32 v36, s[14:15], v29, v29, 1.0
	v_rcp_f32_e32 v42, v36
	v_mul_f32_e32 v31, 0xbfb8aa3b, v31
	v_exp_f32_e32 v30, v30
	v_exp_f32_e32 v31, v31
	v_fma_f32 v43, -v36, v42, 1.0
	v_fmac_f32_e32 v42, v43, v42
	v_div_scale_f32 v43, vcc, 1.0, v29, 1.0
	v_mul_f32_e32 v44, v43, v42
	v_fma_f32 v45, -v36, v44, v43
	v_fmac_f32_e32 v44, v45, v42
	v_fma_f32 v36, -v36, v44, v43
	v_div_fmas_f32 v36, v36, v42, v44
	v_div_fixup_f32 v29, v36, v29, 1.0
	v_div_scale_f32 v36, s[14:15], v28, v28, 1.0
	v_rcp_f32_e32 v42, v36
	v_pk_add_f32 v[30:31], v[30:31], 1.0 op_sel_hi:[1,0]
	v_mul_f32_e32 v24, 0xbfb8aa3b, v24
	v_mul_f32_e32 v25, 0xbfb8aa3b, v25
	v_fma_f32 v43, -v36, v42, 1.0
	v_fmac_f32_e32 v42, v43, v42
	v_div_scale_f32 v43, vcc, 1.0, v28, 1.0
	v_mul_f32_e32 v44, v43, v42
	v_fma_f32 v45, -v36, v44, v43
	v_fmac_f32_e32 v44, v45, v42
	v_fma_f32 v36, -v36, v44, v43
	v_div_fmas_f32 v36, v36, v42, v44
	v_div_fixup_f32 v28, v36, v28, 1.0
	v_pk_mul_f32 v[28:29], v[28:29], v[40:41]
	v_div_scale_f32 v40, s[14:15], v31, v31, 1.0
	v_rcp_f32_e32 v41, v40
	v_exp_f32_e32 v24, v24
	v_exp_f32_e32 v25, v25
	v_lshlrev_b32_e32 v36, 16, v37
	v_fma_f32 v42, -v40, v41, 1.0
	v_fmac_f32_e32 v41, v42, v41
	v_div_scale_f32 v42, vcc, 1.0, v31, 1.0
	v_mul_f32_e32 v43, v42, v41
	v_fma_f32 v44, -v40, v43, v42
	v_fmac_f32_e32 v43, v44, v41
	v_fma_f32 v40, -v40, v43, v42
	v_div_fmas_f32 v40, v40, v41, v43
	v_div_fixup_f32 v31, v40, v31, 1.0
	v_div_scale_f32 v40, s[14:15], v30, v30, 1.0
	v_rcp_f32_e32 v41, v40
	v_and_b32_e32 v37, 0xffff0000, v37
	v_pk_add_f32 v[24:25], v[24:25], 1.0 op_sel_hi:[1,0]
	v_fma_f32 v42, -v40, v41, 1.0
	v_fmac_f32_e32 v41, v42, v41
	v_div_scale_f32 v42, vcc, 1.0, v30, 1.0
	v_mul_f32_e32 v43, v42, v41
	v_fma_f32 v44, -v40, v43, v42
	v_fmac_f32_e32 v43, v44, v41
	v_fma_f32 v40, -v40, v43, v42
	v_div_fmas_f32 v40, v40, v41, v43
	v_div_fixup_f32 v30, v40, v30, 1.0
	v_pk_mul_f32 v[30:31], v[30:31], v[36:37]
	v_lshlrev_b32_e32 v36, 16, v38
	v_and_b32_e32 v37, 0xffff0000, v38
	v_div_scale_f32 v38, s[14:15], v25, v25, 1.0
	v_rcp_f32_e32 v40, v38
	s_nop 0
	v_fma_f32 v41, -v38, v40, 1.0
	v_fmac_f32_e32 v40, v41, v40
	v_div_scale_f32 v41, vcc, 1.0, v25, 1.0
	v_mul_f32_e32 v42, v41, v40
	v_fma_f32 v43, -v38, v42, v41
	v_fmac_f32_e32 v42, v43, v40
	v_fma_f32 v38, -v38, v42, v41
	v_div_fmas_f32 v38, v38, v40, v42
	v_div_fixup_f32 v25, v38, v25, 1.0
	v_div_scale_f32 v38, s[14:15], v24, v24, 1.0
	v_rcp_f32_e32 v40, v38
	s_nop 0
	v_fma_f32 v41, -v38, v40, 1.0
	v_fmac_f32_e32 v40, v41, v40
	v_div_scale_f32 v41, vcc, 1.0, v24, 1.0
	v_mul_f32_e32 v42, v41, v40
	v_fma_f32 v43, -v38, v42, v41
	v_fmac_f32_e32 v42, v43, v40
	v_fma_f32 v38, -v38, v42, v41
	v_div_fmas_f32 v38, v38, v40, v42
	v_div_fixup_f32 v24, v38, v24, 1.0
	v_pk_mul_f32 v[36:37], v[24:25], v[36:37]
	v_mul_f32_e32 v24, 0xbfb8aa3b, v26
	v_mul_f32_e32 v25, 0xbfb8aa3b, v27
	v_exp_f32_e32 v24, v24
	v_exp_f32_e32 v25, v25
	v_lshlrev_b32_e32 v26, 16, v39
	v_and_b32_e32 v27, 0xffff0000, v39
	v_pk_add_f32 v[24:25], v[24:25], 1.0 op_sel_hi:[1,0]
	s_nop 0
	v_div_scale_f32 v38, s[14:15], v25, v25, 1.0
	v_rcp_f32_e32 v39, v38
	s_nop 0
	v_fma_f32 v40, -v38, v39, 1.0
	v_fmac_f32_e32 v39, v40, v39
	v_div_scale_f32 v40, vcc, 1.0, v25, 1.0
	v_mul_f32_e32 v41, v40, v39
	v_fma_f32 v42, -v38, v41, v40
	v_fmac_f32_e32 v41, v42, v39
	v_fma_f32 v38, -v38, v41, v40
	v_div_fmas_f32 v38, v38, v39, v41
	v_div_fixup_f32 v25, v38, v25, 1.0
	v_div_scale_f32 v38, s[14:15], v24, v24, 1.0
	v_rcp_f32_e32 v39, v38
	s_nop 0
	v_fma_f32 v40, -v38, v39, 1.0
	v_fmac_f32_e32 v39, v40, v39
	v_div_scale_f32 v40, vcc, 1.0, v24, 1.0
	v_mul_f32_e32 v41, v40, v39
	v_fma_f32 v42, -v38, v41, v40
	v_fmac_f32_e32 v41, v42, v39
	v_fma_f32 v38, -v38, v41, v40
	v_div_fmas_f32 v38, v38, v39, v41
	v_div_fixup_f32 v24, v38, v24, 1.0
	v_pk_mul_f32 v[38:39], v[24:25], v[26:27]
	v_cvt_pk_bf16_f32 v24, v28, v29
	v_lshl_add_u64 v[28:29], s[26:27], 0, v[32:33]
	v_cvt_pk_bf16_f32 v25, v30, v31
	v_cvt_pk_bf16_f32 v26, v36, v37
	v_cvt_pk_bf16_f32 v27, v38, v39
	v_lshl_add_u64 v[32:33], v[28:29], 0, v[142:143]
	global_store_dwordx4 v[32:33], v[24:27], off offset:1024
	s_nop 1
	s_nop 0
	s_waitcnt vmcnt(8)
; __device__ __forceinline__ float sigmoidf_(float x) { return 1.f / (1.f + __expf(-x)); }
; __device__ __forceinline__ unsigned cvt_pk_bf16(float lo, float hi) { const f32x2c v = {lo, hi}; const bf16x2c b = __builtin_convertvector(v, bf16x2c); return __builtin_bit_cast(unsigned, b); }
;     __device__ __forceinline__ void operator()(const f32x4 (&acc)[2][2][4][2], const Unit& u, int wr, int wc, int fr, int fq) const {
;     ...
;             for (int m = 0; m < 4; ++m) { const size_t row = (size_t)(row0 + ai * HALF + m * 16);
; #pragma unroll
;                 for (int bj = 0; bj < 2; ++bj) { const int col = col0 + bj * HALF;
;                     const u32x4 zz = *(const u32x4*)(Z + row * 512 + col);
;                     const f32x4 b0 = *(const f32x4*)(bias + col), b1 = *(const f32x4*)(bias + col + 4);
;                     const f32x4 v0 = acc[ai][bj][m][0] + b0, v1 = acc[ai][bj][m][1] + b1;
;                     float o[8]; const unsigned zw[4] = {zz.x, zz.y, zz.z, zz.w};
; #pragma unroll
;                     for (int q = 0; q < 4; ++q) { const float zl = __builtin_bit_cast(float, zw[q] << 16), zh = __builtin_bit_cast(float, zw[q] & 0xffff0000u);
;                         const float al = (q < 2) ? v0[2 * q] : v1[2 * q - 4], ah = (q < 2) ? v0[2 * q + 1] : v1[2 * q - 3];
;                         o[2 * q] = zl * sigmoidf_(al); o[2 * q + 1] = zh * sigmoidf_(ah); }
;                     u32x4 w; w.x = cvt_pk_bf16(o[0], o[1]); w.y = cvt_pk_bf16(o[2], o[3]); w.z = cvt_pk_bf16(o[4], o[5]); w.w = cvt_pk_bf16(o[6], o[7]);
;                     *(u32x4*)(YM + row * D + 512 + col) = w; } }
	v_mov_b32_e32 v24, v190
	v_mov_b32_e32 v25, v191
	v_mov_b32_e32 v26, v192
	v_mov_b32_e32 v27, v193
	v_mov_b32_e32 v28, v182
	v_mov_b32_e32 v29, v183
	v_mov_b32_e32 v30, v184
	v_mov_b32_e32 v31, v185
	v_mov_b32_e32 v34, v178
	v_mov_b32_e32 v35, v179
	v_mov_b32_e32 v36, v180
	v_mov_b32_e32 v37, v181
	v_pk_add_f32 v[28:29], v[16:17], v[28:29]
	v_pk_add_f32 v[20:21], v[20:21], v[34:35]
	v_pk_add_f32 v[18:19], v[18:19], v[30:31]
	v_mul_f32_e32 v16, 0xbfb8aa3b, v20
	v_mul_f32_e32 v17, 0xbfb8aa3b, v21
	v_exp_f32_e32 v16, v16
	v_exp_f32_e32 v17, v17
	v_lshlrev_b32_e32 v20, 16, v24
	v_and_b32_e32 v21, 0xffff0000, v24
	v_pk_add_f32 v[22:23], v[22:23], v[36:37]
	v_pk_add_f32 v[16:17], v[16:17], 1.0 op_sel_hi:[1,0]
	v_mul_f32_e32 v18, 0xbfb8aa3b, v18
	v_div_scale_f32 v24, s[14:15], v17, v17, 1.0
	v_rcp_f32_e32 v30, v24
	v_mul_f32_e32 v19, 0xbfb8aa3b, v19
	v_exp_f32_e32 v18, v18
	v_exp_f32_e32 v19, v19
	v_fma_f32 v31, -v24, v30, 1.0
	v_fmac_f32_e32 v30, v31, v30
	v_div_scale_f32 v31, vcc, 1.0, v17, 1.0
	v_mul_f32_e32 v34, v31, v30
	v_fma_f32 v35, -v24, v34, v31
	v_fmac_f32_e32 v34, v35, v30
	v_fma_f32 v24, -v24, v34, v31
	v_div_fmas_f32 v24, v24, v30, v34
	v_div_fixup_f32 v17, v24, v17, 1.0
	v_div_scale_f32 v24, s[14:15], v16, v16, 1.0
	v_rcp_f32_e32 v30, v24
	v_pk_add_f32 v[18:19], v[18:19], 1.0 op_sel_hi:[1,0]
	v_fma_f32 v31, -v24, v30, 1.0
	v_fmac_f32_e32 v30, v31, v30
	v_div_scale_f32 v31, vcc, 1.0, v16, 1.0
	v_mul_f32_e32 v34, v31, v30
	v_fma_f32 v35, -v24, v34, v31
	v_fmac_f32_e32 v34, v35, v30
	v_fma_f32 v24, -v24, v34, v31
	v_div_fmas_f32 v24, v24, v30, v34
	v_div_fixup_f32 v16, v24, v16, 1.0
	v_pk_mul_f32 v[16:17], v[16:17], v[20:21]
	v_mul_f32_e32 v20, 0xbfb8aa3b, v22
	v_mul_f32_e32 v21, 0xbfb8aa3b, v23
	v_exp_f32_e32 v20, v20
	v_exp_f32_e32 v21, v21
	v_lshlrev_b32_e32 v22, 16, v25
	v_and_b32_e32 v23, 0xffff0000, v25
	v_cvt_pk_bf16_f32 v16, v16, v17
	v_pk_add_f32 v[20:21], v[20:21], 1.0 op_sel_hi:[1,0]
	s_nop 0
	v_div_scale_f32 v24, s[14:15], v21, v21, 1.0
	v_rcp_f32_e32 v25, v24
	s_nop 0
	v_fma_f32 v30, -v24, v25, 1.0
	v_fmac_f32_e32 v25, v30, v25
	v_div_scale_f32 v30, vcc, 1.0, v21, 1.0
	v_mul_f32_e32 v31, v30, v25
	v_fma_f32 v34, -v24, v31, v30
	v_fmac_f32_e32 v31, v34, v25
	v_fma_f32 v24, -v24, v31, v30
	v_div_fmas_f32 v24, v24, v25, v31
	v_div_fixup_f32 v21, v24, v21, 1.0
	v_div_scale_f32 v24, s[14:15], v20, v20, 1.0
	v_rcp_f32_e32 v25, v24
	s_nop 0
	v_fma_f32 v30, -v24, v25, 1.0
	v_fmac_f32_e32 v25, v30, v25
	v_div_scale_f32 v30, vcc, 1.0, v20, 1.0
	v_mul_f32_e32 v31, v30, v25
	v_fma_f32 v34, -v24, v31, v30
	v_fmac_f32_e32 v31, v34, v25
	v_fma_f32 v24, -v24, v31, v30
	v_div_fmas_f32 v24, v24, v25, v31
	v_div_fixup_f32 v20, v24, v20, 1.0
	v_pk_mul_f32 v[20:21], v[20:21], v[22:23]
	v_mul_f32_e32 v22, 0xbfb8aa3b, v28
	v_mul_f32_e32 v23, 0xbfb8aa3b, v29
	v_exp_f32_e32 v22, v22
	v_exp_f32_e32 v23, v23
	v_lshlrev_b32_e32 v24, 16, v26
	v_and_b32_e32 v25, 0xffff0000, v26
	v_cvt_pk_bf16_f32 v17, v20, v21
	v_pk_add_f32 v[22:23], v[22:23], 1.0 op_sel_hi:[1,0]
	s_nop 0
	v_div_scale_f32 v26, s[14:15], v23, v23, 1.0
	v_rcp_f32_e32 v28, v26
	s_nop 0
	v_fma_f32 v29, -v26, v28, 1.0
	v_fmac_f32_e32 v28, v29, v28
	v_div_scale_f32 v29, vcc, 1.0, v23, 1.0
	v_mul_f32_e32 v30, v29, v28
	v_fma_f32 v31, -v26, v30, v29
	v_fmac_f32_e32 v30, v31, v28
	v_fma_f32 v26, -v26, v30, v29
	v_div_fmas_f32 v26, v26, v28, v30
	v_div_fixup_f32 v23, v26, v23, 1.0
	v_div_scale_f32 v26, s[14:15], v22, v22, 1.0
	v_rcp_f32_e32 v28, v26
	s_nop 0
	v_fma_f32 v29, -v26, v28, 1.0
	v_fmac_f32_e32 v28, v29, v28
	v_div_scale_f32 v29, vcc, 1.0, v22, 1.0
	v_mul_f32_e32 v30, v29, v28
	v_fma_f32 v31, -v26, v30, v29
	v_fmac_f32_e32 v30, v31, v28
	v_fma_f32 v26, -v26, v30, v29
	v_div_fmas_f32 v26, v26, v28, v30
	v_div_fixup_f32 v22, v26, v22, 1.0
	v_div_scale_f32 v26, s[14:15], v19, v19, 1.0
	v_pk_mul_f32 v[22:23], v[22:23], v[24:25]
	v_lshlrev_b32_e32 v24, 16, v27
	v_and_b32_e32 v25, 0xffff0000, v27
	v_rcp_f32_e32 v27, v26
	s_nop 0
	v_fma_f32 v28, -v26, v27, 1.0
	v_fmac_f32_e32 v27, v28, v27
	v_div_scale_f32 v28, vcc, 1.0, v19, 1.0
	v_mul_f32_e32 v29, v28, v27
	v_fma_f32 v30, -v26, v29, v28
	v_fmac_f32_e32 v29, v30, v27
	v_fma_f32 v26, -v26, v29, v28
	v_div_fmas_f32 v26, v26, v27, v29
	v_div_fixup_f32 v19, v26, v19, 1.0
	v_div_scale_f32 v26, s[14:15], v18, v18, 1.0
	v_rcp_f32_e32 v27, v26
	s_nop 0
	v_fma_f32 v28, -v26, v27, 1.0
	v_fmac_f32_e32 v27, v28, v27
	v_div_scale_f32 v28, vcc, 1.0, v18, 1.0
	v_mul_f32_e32 v29, v28, v27
	v_fma_f32 v30, -v26, v29, v28
	v_fmac_f32_e32 v29, v30, v27
	v_fma_f32 v26, -v26, v29, v28
	v_div_fmas_f32 v26, v26, v27, v29
	v_div_fixup_f32 v18, v26, v18, 1.0
	v_pk_mul_f32 v[24:25], v[18:19], v[24:25]
	v_cvt_pk_bf16_f32 v18, v22, v23
	v_cvt_pk_bf16_f32 v19, v24, v25
	global_store_dwordx4 v[32:33], v[16:19], off offset:1280
	s_nop 1
	v_add_u32_e32 v16, 0xb0, v144
	v_ashrrev_i32_e32 v17, 31, v16
	v_lshlrev_b64 v[18:19], 10, v[16:17]
	v_lshlrev_b64 v[30:31], 11, v[16:17]
	v_lshl_add_u64 v[16:17], s[36:37], 0, v[18:19]
	v_lshl_add_u64 v[16:17], v[16:17], 0, v[142:143]
	s_nop 1
	s_waitcnt vmcnt(7)
; __device__ __forceinline__ float sigmoidf_(float x) { return 1.f / (1.f + __expf(-x)); }
; __device__ __forceinline__ unsigned cvt_pk_bf16(float lo, float hi) { const f32x2c v = {lo, hi}; const bf16x2c b = __builtin_convertvector(v, bf16x2c); return __builtin_bit_cast(unsigned, b); }
;     __device__ __forceinline__ void operator()(const f32x4 (&acc)[2][2][4][2], const Unit& u, int wr, int wc, int fr, int fq) const {
;     ...
;             for (int m = 0; m < 4; ++m) { const size_t row = (size_t)(row0 + ai * HALF + m * 16);
; #pragma unroll
;                 for (int bj = 0; bj < 2; ++bj) { const int col = col0 + bj * HALF;
;                     const u32x4 zz = *(const u32x4*)(Z + row * 512 + col);
;                     const f32x4 b0 = *(const f32x4*)(bias + col), b1 = *(const f32x4*)(bias + col + 4);
;                     const f32x4 v0 = acc[ai][bj][m][0] + b0, v1 = acc[ai][bj][m][1] + b1;
;                     float o[8]; const unsigned zw[4] = {zz.x, zz.y, zz.z, zz.w};
; #pragma unroll
;                     for (int q = 0; q < 4; ++q) { const float zl = __builtin_bit_cast(float, zw[q] << 16), zh = __builtin_bit_cast(float, zw[q] & 0xffff0000u);
;                         const float al = (q < 2) ? v0[2 * q] : v1[2 * q - 4], ah = (q < 2) ? v0[2 * q + 1] : v1[2 * q - 3];
;                         o[2 * q] = zl * sigmoidf_(al); o[2 * q + 1] = zh * sigmoidf_(ah); }
;                     u32x4 w; w.x = cvt_pk_bf16(o[0], o[1]); w.y = cvt_pk_bf16(o[2], o[3]); w.z = cvt_pk_bf16(o[4], o[5]); w.w = cvt_pk_bf16(o[6], o[7]);
;                     *(u32x4*)(YM + row * D + 512 + col) = w; } }
	v_mov_b32_e32 v18, v198
	v_mov_b32_e32 v19, v199
	v_mov_b32_e32 v20, v200
	v_mov_b32_e32 v21, v201
	v_mov_b32_e32 v22, v174
	v_mov_b32_e32 v23, v175
	v_mov_b32_e32 v24, v176
	v_mov_b32_e32 v25, v177
	v_mov_b32_e32 v26, v170
	v_mov_b32_e32 v27, v171
	v_mov_b32_e32 v28, v172
	v_mov_b32_e32 v29, v173
	v_pk_add_f32 v[8:9], v[8:9], v[22:23]
	v_pk_add_f32 v[12:13], v[12:13], v[26:27]
	v_lshlrev_b32_e32 v22, 16, v18
	v_mul_f32_e32 v12, 0xbfb8aa3b, v12
	v_mul_f32_e32 v13, 0xbfb8aa3b, v13
	v_exp_f32_e32 v12, v12
	v_exp_f32_e32 v13, v13
	v_and_b32_e32 v23, 0xffff0000, v18
	v_pk_add_f32 v[10:11], v[10:11], v[24:25]
	v_pk_add_f32 v[14:15], v[14:15], v[28:29]
	v_pk_add_f32 v[12:13], v[12:13], 1.0 op_sel_hi:[1,0]
	v_mul_f32_e32 v14, 0xbfb8aa3b, v14
	v_div_scale_f32 v18, s[14:15], v13, v13, 1.0
	v_rcp_f32_e32 v24, v18
	v_mul_f32_e32 v15, 0xbfb8aa3b, v15
	v_exp_f32_e32 v14, v14
	v_exp_f32_e32 v15, v15
	v_fma_f32 v25, -v18, v24, 1.0
	v_fmac_f32_e32 v24, v25, v24
	v_div_scale_f32 v25, vcc, 1.0, v13, 1.0
	v_mul_f32_e32 v26, v25, v24
	v_fma_f32 v27, -v18, v26, v25
	v_fmac_f32_e32 v26, v27, v24
	v_fma_f32 v18, -v18, v26, v25
	v_div_fmas_f32 v18, v18, v24, v26
	v_div_fixup_f32 v13, v18, v13, 1.0
	v_div_scale_f32 v18, s[14:15], v12, v12, 1.0
	v_rcp_f32_e32 v24, v18
	v_pk_add_f32 v[14:15], v[14:15], 1.0 op_sel_hi:[1,0]
	v_mul_f32_e32 v8, 0xbfb8aa3b, v8
	v_mul_f32_e32 v9, 0xbfb8aa3b, v9
	v_fma_f32 v25, -v18, v24, 1.0
	v_fmac_f32_e32 v24, v25, v24
	v_div_scale_f32 v25, vcc, 1.0, v12, 1.0
	v_mul_f32_e32 v26, v25, v24
	v_fma_f32 v27, -v18, v26, v25
	v_fmac_f32_e32 v26, v27, v24
	v_fma_f32 v18, -v18, v26, v25
	v_div_fmas_f32 v18, v18, v24, v26
	v_div_fixup_f32 v12, v18, v12, 1.0
	v_pk_mul_f32 v[12:13], v[12:13], v[22:23]
	v_div_scale_f32 v22, s[14:15], v15, v15, 1.0
	v_rcp_f32_e32 v23, v22
	v_exp_f32_e32 v8, v8
	v_exp_f32_e32 v9, v9
	v_lshlrev_b32_e32 v18, 16, v19
	v_fma_f32 v24, -v22, v23, 1.0
	v_fmac_f32_e32 v23, v24, v23
	v_div_scale_f32 v24, vcc, 1.0, v15, 1.0
	v_mul_f32_e32 v25, v24, v23
	v_fma_f32 v26, -v22, v25, v24
	v_fmac_f32_e32 v25, v26, v23
	v_fma_f32 v22, -v22, v25, v24
	v_div_fmas_f32 v22, v22, v23, v25
	v_div_fixup_f32 v15, v22, v15, 1.0
	v_div_scale_f32 v22, s[14:15], v14, v14, 1.0
	v_rcp_f32_e32 v23, v22
	v_and_b32_e32 v19, 0xffff0000, v19
	v_pk_add_f32 v[8:9], v[8:9], 1.0 op_sel_hi:[1,0]
	v_fma_f32 v24, -v22, v23, 1.0
	v_fmac_f32_e32 v23, v24, v23
	v_div_scale_f32 v24, vcc, 1.0, v14, 1.0
	v_mul_f32_e32 v25, v24, v23
	v_fma_f32 v26, -v22, v25, v24
	v_fmac_f32_e32 v25, v26, v23
	v_fma_f32 v22, -v22, v25, v24
	v_div_fmas_f32 v22, v22, v23, v25
	v_div_fixup_f32 v14, v22, v14, 1.0
	v_pk_mul_f32 v[14:15], v[14:15], v[18:19]
	v_lshlrev_b32_e32 v18, 16, v20
	v_and_b32_e32 v19, 0xffff0000, v20
	v_div_scale_f32 v20, s[14:15], v9, v9, 1.0
	v_rcp_f32_e32 v22, v20
	s_nop 0
	v_fma_f32 v23, -v20, v22, 1.0
	v_fmac_f32_e32 v22, v23, v22
	v_div_scale_f32 v23, vcc, 1.0, v9, 1.0
	v_mul_f32_e32 v24, v23, v22
	v_fma_f32 v25, -v20, v24, v23
	v_fmac_f32_e32 v24, v25, v22
	v_fma_f32 v20, -v20, v24, v23
	v_div_fmas_f32 v20, v20, v22, v24
	v_div_fixup_f32 v9, v20, v9, 1.0
	v_div_scale_f32 v20, s[14:15], v8, v8, 1.0
	v_rcp_f32_e32 v22, v20
	s_nop 0
	v_fma_f32 v23, -v20, v22, 1.0
	v_fmac_f32_e32 v22, v23, v22
	v_div_scale_f32 v23, vcc, 1.0, v8, 1.0
	v_mul_f32_e32 v24, v23, v22
	v_fma_f32 v25, -v20, v24, v23
	v_fmac_f32_e32 v24, v25, v22
	v_fma_f32 v20, -v20, v24, v23
	v_div_fmas_f32 v20, v20, v22, v24
	v_div_fixup_f32 v8, v20, v8, 1.0
	v_pk_mul_f32 v[18:19], v[8:9], v[18:19]
	v_mul_f32_e32 v8, 0xbfb8aa3b, v10
	v_mul_f32_e32 v9, 0xbfb8aa3b, v11
	v_exp_f32_e32 v8, v8
	v_exp_f32_e32 v9, v9
	v_lshlrev_b32_e32 v10, 16, v21
	v_and_b32_e32 v11, 0xffff0000, v21
	v_pk_add_f32 v[8:9], v[8:9], 1.0 op_sel_hi:[1,0]
	s_nop 0
	v_div_scale_f32 v20, s[14:15], v9, v9, 1.0
	v_rcp_f32_e32 v21, v20
	s_nop 0
	v_fma_f32 v22, -v20, v21, 1.0
	v_fmac_f32_e32 v21, v22, v21
	v_div_scale_f32 v22, vcc, 1.0, v9, 1.0
	v_mul_f32_e32 v23, v22, v21
	v_fma_f32 v24, -v20, v23, v22
	v_fmac_f32_e32 v23, v24, v21
	v_fma_f32 v20, -v20, v23, v22
	v_div_fmas_f32 v20, v20, v21, v23
	v_div_fixup_f32 v9, v20, v9, 1.0
	v_div_scale_f32 v20, s[14:15], v8, v8, 1.0
	v_rcp_f32_e32 v21, v20
	s_nop 0
	v_fma_f32 v22, -v20, v21, 1.0
	v_fmac_f32_e32 v21, v22, v21
	v_div_scale_f32 v22, vcc, 1.0, v8, 1.0
	v_mul_f32_e32 v23, v22, v21
	v_fma_f32 v24, -v20, v23, v22
	v_fmac_f32_e32 v23, v24, v21
	v_fma_f32 v20, -v20, v23, v22
	v_div_fmas_f32 v20, v20, v21, v23
	v_div_fixup_f32 v8, v20, v8, 1.0
	v_pk_mul_f32 v[20:21], v[8:9], v[10:11]
	v_cvt_pk_bf16_f32 v8, v12, v13
	v_lshl_add_u64 v[12:13], s[26:27], 0, v[30:31]
	v_cvt_pk_bf16_f32 v9, v14, v15
	v_cvt_pk_bf16_f32 v10, v18, v19
	v_cvt_pk_bf16_f32 v11, v20, v21
	v_lshl_add_u64 v[12:13], v[12:13], 0, v[142:143]
	global_store_dwordx4 v[12:13], v[8:11], off offset:1024
	s_nop 1
	s_nop 0
	s_waitcnt vmcnt(6)
; __device__ __forceinline__ float sigmoidf_(float x) { return 1.f / (1.f + __expf(-x)); }
; __device__ __forceinline__ unsigned cvt_pk_bf16(float lo, float hi) { const f32x2c v = {lo, hi}; const bf16x2c b = __builtin_convertvector(v, bf16x2c); return __builtin_bit_cast(unsigned, b); }
;     __device__ __forceinline__ void operator()(const f32x4 (&acc)[2][2][4][2], const Unit& u, int wr, int wc, int fr, int fq) const {
;     ...
;             for (int m = 0; m < 4; ++m) { const size_t row = (size_t)(row0 + ai * HALF + m * 16);
; #pragma unroll
;                 for (int bj = 0; bj < 2; ++bj) { const int col = col0 + bj * HALF;
;                     const u32x4 zz = *(const u32x4*)(Z + row * 512 + col);
;                     const f32x4 b0 = *(const f32x4*)(bias + col), b1 = *(const f32x4*)(bias + col + 4);
;                     const f32x4 v0 = acc[ai][bj][m][0] + b0, v1 = acc[ai][bj][m][1] + b1;
;                     float o[8]; const unsigned zw[4] = {zz.x, zz.y, zz.z, zz.w};
; #pragma unroll
;                     for (int q = 0; q < 4; ++q) { const float zl = __builtin_bit_cast(float, zw[q] << 16), zh = __builtin_bit_cast(float, zw[q] & 0xffff0000u);
;                         const float al = (q < 2) ? v0[2 * q] : v1[2 * q - 4], ah = (q < 2) ? v0[2 * q + 1] : v1[2 * q - 3];
;                         o[2 * q] = zl * sigmoidf_(al); o[2 * q + 1] = zh * sigmoidf_(ah); }
;                     u32x4 w; w.x = cvt_pk_bf16(o[0], o[1]); w.y = cvt_pk_bf16(o[2], o[3]); w.z = cvt_pk_bf16(o[4], o[5]); w.w = cvt_pk_bf16(o[6], o[7]);
;                     *(u32x4*)(YM + row * D + 512 + col) = w; } }
	v_mov_b32_e32 v8, v202
	v_mov_b32_e32 v9, v203
	v_mov_b32_e32 v10, v204
	v_mov_b32_e32 v11, v205
	v_mov_b32_e32 v18, v182
	v_mov_b32_e32 v19, v183
	v_mov_b32_e32 v20, v184
	v_mov_b32_e32 v21, v185
	v_mov_b32_e32 v14, v178
	v_mov_b32_e32 v15, v179
	v_mov_b32_e32 v16, v180
	v_mov_b32_e32 v17, v181
	v_pk_add_f32 v[0:1], v[0:1], v[14:15]
	s_nop 0
	v_mul_f32_e32 v0, 0xbfb8aa3b, v0
	v_mul_f32_e32 v1, 0xbfb8aa3b, v1
	v_exp_f32_e32 v0, v0
	v_exp_f32_e32 v1, v1
	v_pk_add_f32 v[2:3], v[2:3], v[16:17]
	v_pk_add_f32 v[4:5], v[4:5], v[18:19]
	v_mul_f32_e32 v2, 0xbfb8aa3b, v2
	v_pk_add_f32 v[0:1], v[0:1], 1.0 op_sel_hi:[1,0]
	v_mul_f32_e32 v3, 0xbfb8aa3b, v3
	v_div_scale_f32 v14, s[14:15], v1, v1, 1.0
	v_rcp_f32_e32 v15, v14
	v_exp_f32_e32 v2, v2
	v_exp_f32_e32 v3, v3
	v_mul_f32_e32 v4, 0xbfb8aa3b, v4
	v_fma_f32 v16, -v14, v15, 1.0
	v_fmac_f32_e32 v15, v16, v15
	v_div_scale_f32 v16, vcc, 1.0, v1, 1.0
	v_mul_f32_e32 v17, v16, v15
	v_fma_f32 v18, -v14, v17, v16
	v_fmac_f32_e32 v17, v18, v15
	v_fma_f32 v14, -v14, v17, v16
	v_div_fmas_f32 v14, v14, v15, v17
	v_div_fixup_f32 v1, v14, v1, 1.0
	v_div_scale_f32 v14, s[14:15], v0, v0, 1.0
	v_rcp_f32_e32 v15, v14
	v_pk_add_f32 v[2:3], v[2:3], 1.0 op_sel_hi:[1,0]
	v_mul_f32_e32 v5, 0xbfb8aa3b, v5
	v_exp_f32_e32 v4, v4
	v_fma_f32 v16, -v14, v15, 1.0
	v_fmac_f32_e32 v15, v16, v15
	v_div_scale_f32 v16, vcc, 1.0, v0, 1.0
	v_mul_f32_e32 v17, v16, v15
	v_fma_f32 v18, -v14, v17, v16
	v_fmac_f32_e32 v17, v18, v15
	v_fma_f32 v14, -v14, v17, v16
	v_div_fmas_f32 v14, v14, v15, v17
	v_div_fixup_f32 v0, v14, v0, 1.0
	v_lshlrev_b32_e32 v14, 16, v8
	v_and_b32_e32 v15, 0xffff0000, v8
	v_div_scale_f32 v8, s[14:15], v3, v3, 1.0
	v_pk_mul_f32 v[0:1], v[0:1], v[14:15]
	v_rcp_f32_e32 v14, v8
	v_exp_f32_e32 v5, v5
	v_pk_add_f32 v[6:7], v[6:7], v[20:21]
	v_cvt_pk_bf16_f32 v0, v0, v1
	v_fma_f32 v15, -v8, v14, 1.0
	v_fmac_f32_e32 v14, v15, v14
	v_div_scale_f32 v15, vcc, 1.0, v3, 1.0
	v_mul_f32_e32 v16, v15, v14
	v_fma_f32 v17, -v8, v16, v15
	v_fmac_f32_e32 v16, v17, v14
	v_fma_f32 v8, -v8, v16, v15
	v_div_fmas_f32 v8, v8, v14, v16
	v_div_fixup_f32 v3, v8, v3, 1.0
	v_div_scale_f32 v8, s[14:15], v2, v2, 1.0
	v_rcp_f32_e32 v14, v8
	v_pk_add_f32 v[4:5], v[4:5], 1.0 op_sel_hi:[1,0]
	v_mul_f32_e32 v6, 0xbfb8aa3b, v6
	v_mul_f32_e32 v7, 0xbfb8aa3b, v7
	v_fma_f32 v15, -v8, v14, 1.0
	v_fmac_f32_e32 v14, v15, v14
	v_div_scale_f32 v15, vcc, 1.0, v2, 1.0
	v_mul_f32_e32 v16, v15, v14
	v_fma_f32 v17, -v8, v16, v15
	v_fmac_f32_e32 v16, v17, v14
	v_fma_f32 v8, -v8, v16, v15
	v_div_fmas_f32 v8, v8, v14, v16
	v_div_fixup_f32 v2, v8, v2, 1.0
	v_lshlrev_b32_e32 v8, 16, v9
	v_and_b32_e32 v9, 0xffff0000, v9
	v_pk_mul_f32 v[2:3], v[2:3], v[8:9]
	v_div_scale_f32 v8, s[14:15], v5, v5, 1.0
	v_rcp_f32_e32 v9, v8
	v_exp_f32_e32 v6, v6
	v_exp_f32_e32 v7, v7
	v_cvt_pk_bf16_f32 v1, v2, v3
	v_fma_f32 v14, -v8, v9, 1.0
	v_fmac_f32_e32 v9, v14, v9
	v_div_scale_f32 v14, vcc, 1.0, v5, 1.0
	v_mul_f32_e32 v15, v14, v9
	v_fma_f32 v16, -v8, v15, v14
	v_fmac_f32_e32 v15, v16, v9
	v_fma_f32 v8, -v8, v15, v14
	v_div_fmas_f32 v8, v8, v9, v15
	v_div_fixup_f32 v5, v8, v5, 1.0
	v_div_scale_f32 v8, s[14:15], v4, v4, 1.0
	v_rcp_f32_e32 v9, v8
	v_pk_add_f32 v[6:7], v[6:7], 1.0 op_sel_hi:[1,0]
	v_fma_f32 v14, -v8, v9, 1.0
	v_fmac_f32_e32 v9, v14, v9
	v_div_scale_f32 v14, vcc, 1.0, v4, 1.0
	v_mul_f32_e32 v15, v14, v9
	v_fma_f32 v16, -v8, v15, v14
	v_fmac_f32_e32 v15, v16, v9
	v_fma_f32 v8, -v8, v15, v14
	v_div_fmas_f32 v8, v8, v9, v15
	v_div_fixup_f32 v4, v8, v4, 1.0
	v_lshlrev_b32_e32 v8, 16, v10
	v_and_b32_e32 v9, 0xffff0000, v10
	v_div_scale_f32 v10, s[14:15], v7, v7, 1.0
	v_pk_mul_f32 v[4:5], v[4:5], v[8:9]
	v_lshlrev_b32_e32 v8, 16, v11
	v_and_b32_e32 v9, 0xffff0000, v11
	v_rcp_f32_e32 v11, v10
	v_cvt_pk_bf16_f32 v2, v4, v5
	v_fma_f32 v14, -v10, v11, 1.0
	v_fmac_f32_e32 v11, v14, v11
	v_div_scale_f32 v14, vcc, 1.0, v7, 1.0
	v_mul_f32_e32 v15, v14, v11
	v_fma_f32 v16, -v10, v15, v14
	v_fmac_f32_e32 v15, v16, v11
	v_fma_f32 v10, -v10, v15, v14
	v_div_fmas_f32 v10, v10, v11, v15
	v_div_fixup_f32 v7, v10, v7, 1.0
	v_div_scale_f32 v10, s[14:15], v6, v6, 1.0
	v_rcp_f32_e32 v11, v10
	s_mov_b64 s[14:15], -1
	v_fma_f32 v14, -v10, v11, 1.0
	v_fmac_f32_e32 v11, v14, v11
	v_div_scale_f32 v14, vcc, 1.0, v6, 1.0
	v_mul_f32_e32 v15, v14, v11
	v_fma_f32 v16, -v10, v15, v14
	v_fmac_f32_e32 v15, v16, v11
	v_fma_f32 v10, -v10, v15, v14
	v_div_fmas_f32 v10, v10, v11, v15
	v_div_fixup_f32 v6, v10, v6, 1.0
	v_pk_mul_f32 v[6:7], v[6:7], v[8:9]
	s_and_b64 vcc, exec, s[38:39]
	v_cvt_pk_bf16_f32 v3, v6, v7
	global_store_dwordx4 v[12:13], v[0:3], off offset:1280
	s_cbranch_vccnz .LBB0_2014
	s_andn2_b64 vcc, exec, s[96:97]
	s_cbranch_vccnz .LBB0_2013
	s_barrier
	s_branch .LBB0_2013

; __device__ __forceinline__ int lane_id() { int l; asm volatile("v_mbcnt_lo_u32_b32 %0, -1, 0\n\tv_mbcnt_hi_u32_b32 %0, -1, %0" : "=v"(l)); return l; }
; __device__ __forceinline__ void final_ph(const int WID_, const bf16* __restrict__ x3, float* __restrict__ out, const bf16* __restrict__ yslot, const int* __restrict__ tok_slot, const float* __restrict__ w) {
;     const int lane = lane_id(), wv = WID_;
;     float4 g[4];
; #pragma unroll
;     for (int j = 0; j < 4; ++j) g[j] = *(const float4*)(w + (lane + 64 * j) * 4);
;     for (int row0 = (GB * 8 + wv) * 2; row0 < M; row0 += GN * 16) {
;         float4 v[2][4]; uint2 xa[2][4], ya[2][4], yb[2][4];
; #pragma unroll
;         for (int r = 0; r < 2; ++r) { const int row = row0 + r;
;             const uint2* xr = (const uint2*)(x3 + (size_t)row * D);
;             const uint2* pa = (const uint2*)(yslot + (size_t)tok_slot[2 * row] * D);
;             const uint2* pb = (const uint2*)(yslot + (size_t)tok_slot[2 * row + 1] * D);
; #pragma unroll
;             for (int j = 0; j < 4; ++j) { xa[r][j] = xr[lane + 64 * j]; ya[r][j] = pa[lane + 64 * j]; yb[r][j] = pb[lane + 64 * j]; } }
; #pragma unroll
.LBB0_2421:
	s_or_b64 exec, exec, s[0:1]
	v_readlane_b32 s5, v243, 44
	s_lshl_b32 s0, s68, 4
	s_lshl_b32 s1, s5, 1
	s_add_i32 s4, s1, s0
	s_cmp_gt_i32 s4, 0xffff
	s_waitcnt lgkmcnt(0)
	s_barrier
	v_mbcnt_lo_u32_b32 v18, -1, 0
	v_mbcnt_hi_u32_b32 v18, -1, v18
	s_cbranch_scc1 .LBB0_2424
	v_lshlrev_b32_e32 v2, 2, v18
	v_mov_b32_e32 v0, s88
	v_mov_b32_e32 v1, s89
	v_ashrrev_i32_e32 v3, 31, v2
	v_lshl_add_u64 v[16:17], v[2:3], 2, v[0:1]
	global_load_dwordx4 v[0:3], v[16:17], off
	global_load_dwordx4 v[4:7], v[16:17], off offset:1024
	global_load_dwordx4 v[8:11], v[16:17], off offset:2048
	global_load_dwordx4 v[12:15], v[16:17], off offset:3072
	v_ashrrev_i32_e32 v19, 31, v18
	v_lshlrev_b64 v[20:21], 3, v[18:19]
	s_lshl_b32 s0, s68, 5
	s_lshl_b32 s1, s5, 2
	s_ashr_i32 s5, s4, 31
	s_lshl_b32 s6, s94, 4
	v_lshl_add_u64 v[16:17], s[2:3], 0, v[20:21]
	s_add_i32 s2, s0, s1
	s_lshl_b32 s14, s94, 5
	s_lshl_b64 s[0:1], s[4:5], 12
	s_add_u32 s0, s90, s0
	s_addc_u32 s1, s91, s1
	v_lshl_add_u64 v[18:19], v[18:19], 4, s[0:1]
	s_mov_b64 s[0:1], 0x1000
	s_ashr_i32 s7, s6, 31
	v_lshl_add_u64 v[18:19], v[18:19], 0, s[0:1]
	s_lshl_b64 s[8:9], s[6:7], 12
	s_lshl_b64 s[0:1], s[4:5], 11
	s_add_u32 s0, s92, s0
	s_addc_u32 s1, s93, s1
	v_lshl_add_u64 v[20:21], s[0:1], 0, v[20:21]
	s_mov_b64 s[0:1], 0xe00
	v_lshl_add_u64 v[20:21], v[20:21], 0, s[0:1]
	s_lshl_b64 s[10:11], s[6:7], 11
	v_mov_b32_e32 v38, 0
	v_mov_b32_e32 v39, 0x358637bd
	v_mov_b32_e32 v40, 0x3a800000
	s_mov_b32 s5, 0x800000
	s_ashr_i32 s3, s2, 31
	s_lshl_b64 s[98:99], s[2:3], 2
	s_add_u32 s98, s12, s98
	s_addc_u32 s99, s13, s99
	global_load_dwordx4 v[126:129], v38, s[98:99]
.LBB0_2423:
	s_ashr_i32 s3, s2, 31
	s_lshl_b64 s[0:1], s[2:3], 2
	s_add_u32 s0, s12, s0
	s_addc_u32 s1, s13, s1
	global_load_dwordx2 v[24:25], v[20:21], off offset:-3584
	global_load_dwordx2 v[28:29], v[20:21], off offset:-3072
	global_load_dwordx2 v[26:27], v[20:21], off offset:-2560
	global_load_dwordx2 v[22:23], v[20:21], off offset:-2048
	global_load_dwordx2 v[30:31], v[20:21], off offset:-1536
	global_load_dwordx2 v[36:37], v[20:21], off offset:-1024
	global_load_dwordx2 v[34:35], v[20:21], off offset:-512
	global_load_dwordx2 v[32:33], v[20:21], off
	v_mov_b32_e32 v41, 0
	v_mov_b32_e32 v123, 0
	v_mov_b32_e32 v122, 0
	v_mov_b32_e32 v124, 0
	s_add_i32 s4, s4, s6
	s_add_i32 s2, s2, s14
	v_lshl_add_u64 v[20:21], v[20:21], 0, s[10:11]
	s_waitcnt vmcnt(7)
	v_lshlrev_b32_e32 v46, 16, v24
	v_and_b32_e32 v47, 0xffff0000, v24
	s_waitcnt vmcnt(6)
	v_lshlrev_b32_e32 v48, 16, v28
	v_and_b32_e32 v49, 0xffff0000, v28
	s_waitcnt vmcnt(5)
	v_lshlrev_b32_e32 v50, 16, v26
	v_and_b32_e32 v51, 0xffff0000, v26
	s_waitcnt vmcnt(0)
	v_mov_b32_e32 v42, v126
	v_mov_b32_e32 v43, v127
	v_mov_b32_e32 v44, v128
	v_mov_b32_e32 v45, v129
	v_ashrrev_i32_e32 v63, 31, v42
	v_mov_b32_e32 v62, v42
	v_ashrrev_i32_e32 v65, 31, v43
	v_mov_b32_e32 v64, v43
	v_ashrrev_i32_e32 v43, 31, v44
	v_mov_b32_e32 v42, v44
	v_ashrrev_i32_e32 v67, 31, v45
	v_mov_b32_e32 v66, v45
	v_lshlrev_b64 v[62:63], 11, v[62:63]
	v_lshlrev_b64 v[42:43], 11, v[42:43]
	v_lshlrev_b64 v[44:45], 11, v[64:65]
	v_lshlrev_b64 v[64:65], 11, v[66:67]
	v_lshl_add_u64 v[62:63], v[16:17], 0, v[62:63]
	v_lshl_add_u64 v[42:43], v[16:17], 0, v[42:43]
	v_lshl_add_u64 v[44:45], v[16:17], 0, v[44:45]
	v_lshl_add_u64 v[64:65], v[16:17], 0, v[64:65]
	global_load_dwordx2 v[66:67], v[62:63], off
	global_load_dwordx2 v[68:69], v[44:45], off
	global_load_dwordx2 v[70:71], v[62:63], off offset:512
	global_load_dwordx2 v[72:73], v[44:45], off offset:512
	global_load_dwordx2 v[74:75], v[62:63], off offset:1024
	global_load_dwordx2 v[76:77], v[44:45], off offset:1024
	global_load_dwordx2 v[78:79], v[62:63], off offset:1536
	global_load_dwordx2 v[80:81], v[44:45], off offset:1536
	global_load_dwordx2 v[82:83], v[42:43], off
	global_load_dwordx2 v[84:85], v[64:65], off
	global_load_dwordx2 v[86:87], v[42:43], off offset:512
	global_load_dwordx2 v[88:89], v[64:65], off offset:512
	global_load_dwordx2 v[90:91], v[42:43], off offset:1024
	global_load_dwordx2 v[92:93], v[64:65], off offset:1024
	global_load_dwordx2 v[94:95], v[42:43], off offset:1536
	s_nop 0
	global_load_dwordx2 v[42:43], v[64:65], off offset:1536
	s_ashr_i32 s3, s2, 31
	s_lshl_b64 s[98:99], s[2:3], 2
	s_add_u32 s98, s12, s98
	s_addc_u32 s99, s13, s99
	global_load_dwordx4 v[126:129], v38, s[98:99]
	s_cmp_lt_i32 s4, 0x10000
	v_lshlrev_b32_e32 v52, 16, v22
	v_and_b32_e32 v53, 0xffff0000, v22
	v_lshlrev_b32_e32 v54, 16, v30
	v_and_b32_e32 v55, 0xffff0000, v30
	v_lshlrev_b32_e32 v56, 16, v36
	v_and_b32_e32 v57, 0xffff0000, v36
	v_lshlrev_b32_e32 v58, 16, v34
	v_and_b32_e32 v59, 0xffff0000, v34
	v_lshlrev_b32_e32 v60, 16, v32
	v_and_b32_e32 v61, 0xffff0000, v32
	v_lshlrev_b32_e32 v32, 16, v33
	v_and_b32_e32 v33, 0xffff0000, v33
	v_lshlrev_b32_e32 v24, 16, v25
	v_and_b32_e32 v25, 0xffff0000, v25
	v_lshlrev_b32_e32 v28, 16, v29
	v_and_b32_e32 v29, 0xffff0000, v29
	v_lshlrev_b32_e32 v26, 16, v27
	v_and_b32_e32 v27, 0xffff0000, v27
	v_lshlrev_b32_e32 v22, 16, v23
	v_and_b32_e32 v23, 0xffff0000, v23
	v_lshlrev_b32_e32 v30, 16, v31
	v_and_b32_e32 v31, 0xffff0000, v31
	v_lshlrev_b32_e32 v36, 16, v37
	v_and_b32_e32 v37, 0xffff0000, v37
	v_lshlrev_b32_e32 v34, 16, v35
	v_and_b32_e32 v35, 0xffff0000, v35
	s_waitcnt vmcnt(16)
	v_lshlrev_b32_e32 v44, 16, v66
	s_waitcnt vmcnt(15)
	v_lshlrev_b32_e32 v62, 16, v68
	v_and_b32_e32 v45, 0xffff0000, v66
	v_and_b32_e32 v63, 0xffff0000, v68
	v_lshlrev_b32_e32 v64, 16, v67
	v_lshlrev_b32_e32 v66, 16, v69
	v_and_b32_e32 v65, 0xffff0000, v67
	v_and_b32_e32 v67, 0xffff0000, v69
	s_waitcnt vmcnt(14)
	v_lshlrev_b32_e32 v68, 16, v70
	s_waitcnt vmcnt(13)
; __device__ __forceinline__ void final_ph(const int WID_, const bf16* __restrict__ x3, float* __restrict__ out, const bf16* __restrict__ yslot, const int* __restrict__ tok_slot, const float* __restrict__ w) {
;     ...
;         for (int r = 0; r < 2; ++r) { float s = 0.f;
; #pragma unroll
;             for (int j = 0; j < 4; ++j) { const uint2 a = ya[r][j], b = yb[r][j], x = xa[r][j];
;                 v[r][j] = make_float4(__builtin_bit_cast(float, x.x << 16), __builtin_bit_cast(float, x.x & 0xffff0000u), __builtin_bit_cast(float, x.y << 16), __builtin_bit_cast(float, x.y & 0xffff0000u));
;                 v[r][j].x += __builtin_bit_cast(float, a.x << 16) + __builtin_bit_cast(float, b.x << 16);
;                 v[r][j].y += __builtin_bit_cast(float, a.x & 0xffff0000u) + __builtin_bit_cast(float, b.x & 0xffff0000u);
;                 v[r][j].z += __builtin_bit_cast(float, a.y << 16) + __builtin_bit_cast(float, b.y << 16);
;                 v[r][j].w += __builtin_bit_cast(float, a.y & 0xffff0000u) + __builtin_bit_cast(float, b.y & 0xffff0000u);
;                 s += v[r][j].x * v[r][j].x + v[r][j].y * v[r][j].y + v[r][j].z * v[r][j].z + v[r][j].w * v[r][j].w; }
	v_lshlrev_b32_e32 v96, 16, v72
	v_and_b32_e32 v69, 0xffff0000, v70
	v_and_b32_e32 v97, 0xffff0000, v72
	s_waitcnt vmcnt(12)
	v_lshlrev_b32_e32 v98, 16, v74
	s_waitcnt vmcnt(11)
	v_lshlrev_b32_e32 v100, 16, v76
	v_and_b32_e32 v99, 0xffff0000, v74
	v_and_b32_e32 v101, 0xffff0000, v76
	s_waitcnt vmcnt(10)
	v_lshlrev_b32_e32 v102, 16, v78
	s_waitcnt vmcnt(9)
	v_lshlrev_b32_e32 v104, 16, v80
	v_and_b32_e32 v103, 0xffff0000, v78
	v_and_b32_e32 v105, 0xffff0000, v80
	v_lshlrev_b32_e32 v78, 16, v79
	v_lshlrev_b32_e32 v80, 16, v81
	v_and_b32_e32 v79, 0xffff0000, v79
	v_and_b32_e32 v81, 0xffff0000, v81
	v_lshlrev_b32_e32 v74, 16, v75
	v_lshlrev_b32_e32 v76, 16, v77
	v_and_b32_e32 v75, 0xffff0000, v75
	v_and_b32_e32 v77, 0xffff0000, v77
	s_waitcnt vmcnt(8)
	v_lshlrev_b32_e32 v106, 16, v82
	s_waitcnt vmcnt(7)
	v_lshlrev_b32_e32 v108, 16, v84
	v_and_b32_e32 v107, 0xffff0000, v82
	v_and_b32_e32 v109, 0xffff0000, v84
	s_waitcnt vmcnt(6)
	v_lshlrev_b32_e32 v110, 16, v86
	s_waitcnt vmcnt(5)
	v_lshlrev_b32_e32 v112, 16, v88
	v_and_b32_e32 v111, 0xffff0000, v86
	v_and_b32_e32 v113, 0xffff0000, v88
	v_lshlrev_b32_e32 v86, 16, v87
	v_lshlrev_b32_e32 v88, 16, v89
	v_and_b32_e32 v87, 0xffff0000, v87
	v_and_b32_e32 v89, 0xffff0000, v89
	s_waitcnt vmcnt(4)
	v_lshlrev_b32_e32 v114, 16, v90
	s_waitcnt vmcnt(3)
	v_lshlrev_b32_e32 v116, 16, v92
	v_and_b32_e32 v115, 0xffff0000, v90
	v_and_b32_e32 v117, 0xffff0000, v92
	s_waitcnt vmcnt(2)
	v_lshlrev_b32_e32 v118, 16, v94
	s_waitcnt vmcnt(1)
	v_lshlrev_b32_e32 v120, 16, v42
	v_and_b32_e32 v119, 0xffff0000, v94
	v_and_b32_e32 v121, 0xffff0000, v42
	v_lshlrev_b32_e32 v94, 16, v95
	v_lshlrev_b32_e32 v42, 16, v43
	v_and_b32_e32 v95, 0xffff0000, v95
	v_and_b32_e32 v43, 0xffff0000, v43
	v_pk_add_f32 v[102:103], v[102:103], v[104:105]
	v_pk_add_f32 v[78:79], v[78:79], v[80:81]
	v_pk_add_f32 v[80:81], v[98:99], v[100:101]
	v_pk_add_f32 v[68:69], v[68:69], v[96:97]
	v_pk_add_f32 v[44:45], v[44:45], v[62:63]
	v_lshlrev_b32_e32 v70, 16, v71
	v_lshlrev_b32_e32 v72, 16, v73
	v_and_b32_e32 v71, 0xffff0000, v71
	v_and_b32_e32 v73, 0xffff0000, v73
	v_pk_add_f32 v[74:75], v[74:75], v[76:77]
	v_pk_add_f32 v[62:63], v[64:65], v[66:67]
	v_pk_add_f32 v[64:65], v[118:119], v[120:121]
	v_pk_add_f32 v[42:43], v[94:95], v[42:43]
	v_pk_add_f32 v[66:67], v[114:115], v[116:117]
	v_pk_add_f32 v[76:77], v[110:111], v[112:113]
	v_pk_add_f32 v[86:87], v[86:87], v[88:89]
	v_pk_add_f32 v[88:89], v[106:107], v[108:109]
	v_pk_add_f32 v[52:53], v[102:103], v[52:53]
	v_pk_add_f32 v[50:51], v[80:81], v[50:51]
	v_pk_add_f32 v[48:49], v[68:69], v[48:49]
	v_pk_add_f32 v[44:45], v[44:45], v[46:47]
	v_lshlrev_b32_e32 v82, 16, v83
	v_lshlrev_b32_e32 v84, 16, v85
	v_and_b32_e32 v83, 0xffff0000, v83
	v_and_b32_e32 v85, 0xffff0000, v85
	v_lshlrev_b32_e32 v90, 16, v91
	v_lshlrev_b32_e32 v92, 16, v93
	v_and_b32_e32 v91, 0xffff0000, v91
	v_and_b32_e32 v93, 0xffff0000, v93
	v_pk_add_f32 v[70:71], v[70:71], v[72:73]
	v_pk_add_f32 v[46:47], v[64:65], v[60:61]
	v_pk_add_f32 v[32:33], v[42:43], v[32:33]
	v_pk_add_f32 v[42:43], v[66:67], v[58:59]
	v_pk_add_f32 v[56:57], v[76:77], v[56:57]
	v_pk_add_f32 v[54:55], v[88:89], v[54:55]
	v_mov_b32_e32 v60, v51
	v_mov_b32_e32 v61, v53
	v_mov_b32_e32 v68, v45
	v_mov_b32_e32 v69, v49
	v_pk_add_f32 v[72:73], v[90:91], v[92:93]
	v_pk_add_f32 v[82:83], v[82:83], v[84:85]
	v_pk_add_f32 v[28:29], v[70:71], v[28:29]
	v_pk_add_f32 v[24:25], v[62:63], v[24:25]
	v_mov_b32_e32 v58, v50
	v_mov_b32_e32 v59, v52
	v_mov_b32_e32 v66, v44
	v_mov_b32_e32 v67, v48
	v_mov_b32_e32 v76, v43
	v_mov_b32_e32 v77, v47
	v_mov_b32_e32 v84, v55
	v_mov_b32_e32 v85, v57
	v_pk_mul_f32 v[60:61], v[60:61], v[60:61]
	v_pk_mul_f32 v[68:69], v[68:69], v[68:69]
	v_pk_add_f32 v[22:23], v[78:79], v[22:23]
	v_pk_add_f32 v[26:27], v[74:75], v[26:27]
	v_pk_add_f32 v[34:35], v[72:73], v[34:35]
	v_pk_add_f32 v[36:37], v[86:87], v[36:37]
	v_pk_add_f32 v[30:31], v[82:83], v[30:31]
	v_mov_b32_e32 v70, v24
	v_mov_b32_e32 v71, v28
	v_mov_b32_e32 v74, v42
	v_mov_b32_e32 v75, v46
	v_mov_b32_e32 v82, v54
	v_mov_b32_e32 v83, v56
	v_pk_mul_f32 v[76:77], v[76:77], v[76:77]
	v_pk_mul_f32 v[84:85], v[84:85], v[84:85]
	v_pk_fma_f32 v[58:59], v[58:59], v[58:59], v[60:61]
	v_pk_fma_f32 v[60:61], v[66:67], v[66:67], v[68:69]
	v_mov_b32_e32 v62, v26
	v_mov_b32_e32 v63, v22
	v_mov_b32_e32 v72, v25
	v_mov_b32_e32 v73, v29
	v_mov_b32_e32 v78, v34
	v_mov_b32_e32 v79, v32
	v_mov_b32_e32 v86, v30
	v_mov_b32_e32 v87, v36
	v_pk_fma_f32 v[66:67], v[74:75], v[74:75], v[76:77]
	v_pk_fma_f32 v[68:69], v[82:83], v[82:83], v[84:85]
; template <int CTRL, int ROWMASK> __device__ __forceinline__ float dppf_(float x) { return __builtin_bit_cast(float, __builtin_amdgcn_update_dpp(0, __builtin_bit_cast(int, x), CTRL, ROWMASK, 0xf, false)); }
; __device__ __forceinline__ float wave_sum(float v) {
;     v += dppf_<0xB1, 0xf>(v); v += dppf_<0x4E, 0xf>(v); v += dppf_<0x141, 0xf>(v); v += dppf_<0x140, 0xf>(v);
;     v += dppf_<0x142, 0xa>(v);
;     v += dppf_<0x143, 0xc>(v);
;     return __builtin_bit_cast(float, __builtin_amdgcn_readlane(__builtin_bit_cast(int, v), 63));
; }
; __device__ __forceinline__ void final_ph(const int WID_, const bf16* __restrict__ x3, float* __restrict__ out, const bf16* __restrict__ yslot, const int* __restrict__ tok_slot, const float* __restrict__ w) {
;     ...
;                 s += v[r][j].x * v[r][j].x + v[r][j].y * v[r][j].y + v[r][j].z * v[r][j].z + v[r][j].w * v[r][j].w; }
;             s = wave_sum(s);
;             const float rs = rsqrtf(s * (1.f / D) + 1e-6f);
;             float4* xo = (float4*)(out + (size_t)(row0 + r) * D);
; #pragma unroll
;             for (int j = 0; j < 4; ++j) xo[lane + 64 * j] = make_float4(v[r][j].x * rs * g[j].x, v[r][j].y * rs * g[j].y, v[r][j].z * rs * g[j].z, v[r][j].w * rs * g[j].w); }
;     }
	v_pk_fma_f32 v[60:61], v[70:71], v[70:71], v[60:61]
	v_mov_b32_e32 v64, v27
	v_mov_b32_e32 v65, v23
	v_mov_b32_e32 v88, v31
	v_mov_b32_e32 v89, v37
	v_pk_fma_f32 v[58:59], v[62:63], v[62:63], v[58:59]
	v_pk_fma_f32 v[62:63], v[78:79], v[78:79], v[66:67]
	v_pk_fma_f32 v[66:67], v[86:87], v[86:87], v[68:69]
	v_pk_fma_f32 v[60:61], v[72:73], v[72:73], v[60:61]
	v_mov_b32_e32 v80, v35
	v_mov_b32_e32 v81, v33
	v_pk_fma_f32 v[58:59], v[64:65], v[64:65], v[58:59]
	v_pk_fma_f32 v[64:65], v[88:89], v[88:89], v[66:67]
	v_add_f32_e32 v60, v60, v61
	v_pk_fma_f32 v[62:63], v[80:81], v[80:81], v[62:63]
	v_add_f32_e32 v61, v64, v65
	v_add_f32_e32 v58, v60, v58
	v_add_f32_e32 v60, v61, v62
	v_add_f32_e32 v58, v58, v59
	v_add_f32_e32 v59, v60, v63
	s_nop 0
	v_add_f32_dpp v58, v58, v58 quad_perm:[1,0,3,2] row_mask:0xf bank_mask:0xf bound_ctrl:1
	v_add_f32_dpp v59, v59, v59 quad_perm:[1,0,3,2] row_mask:0xf bank_mask:0xf bound_ctrl:1
	s_nop 0
	v_add_f32_dpp v58, v58, v58 quad_perm:[2,3,0,1] row_mask:0xf bank_mask:0xf bound_ctrl:1
	v_add_f32_dpp v59, v59, v59 quad_perm:[2,3,0,1] row_mask:0xf bank_mask:0xf bound_ctrl:1
	s_nop 0
	v_add_f32_dpp v58, v58, v58 row_half_mirror row_mask:0xf bank_mask:0xf bound_ctrl:1
	v_add_f32_dpp v59, v59, v59 row_half_mirror row_mask:0xf bank_mask:0xf bound_ctrl:1
	s_nop 0
	v_add_f32_dpp v58, v58, v58 row_mirror row_mask:0xf bank_mask:0xf bound_ctrl:1
	v_add_f32_dpp v59, v59, v59 row_mirror row_mask:0xf bank_mask:0xf bound_ctrl:1
	s_nop 0
	v_mov_b32_dpp v41, v58 row_bcast:15 row_mask:0xa bank_mask:0xf
	v_mov_b32_dpp v123, v59 row_bcast:15 row_mask:0xa bank_mask:0xf
	v_add_f32_e32 v41, v58, v41
	v_add_f32_e32 v58, v59, v123
	s_nop 0
	v_mov_b32_dpp v122, v41 row_bcast:31 row_mask:0xc bank_mask:0xf
	v_mov_b32_dpp v124, v58 row_bcast:31 row_mask:0xc bank_mask:0xf
	v_add_f32_e32 v41, v41, v122
	v_add_f32_e32 v58, v58, v124
	v_readlane_b32 s0, v41, 63
	v_readlane_b32 s1, v58, 63
	s_nop 0
	v_fma_f32 v41, s0, v40, v39
	v_fma_f32 v58, s1, v40, v39
	v_mul_f32_e32 v59, 0x4b800000, v41
	v_cmp_gt_f32_e64 s[0:1], s5, v41
	v_mul_f32_e32 v60, 0x4b800000, v58
	v_cmp_gt_f32_e32 vcc, s5, v58
	v_cndmask_b32_e64 v41, v41, v59, s[0:1]
	v_rsq_f32_e32 v41, v41
	v_cndmask_b32_e32 v58, v58, v60, vcc
	v_rsq_f32_e32 v59, v58
	v_mul_f32_e32 v58, 0x45800000, v41
	v_cndmask_b32_e64 v58, v41, v58, s[0:1]
	v_mul_f32_e32 v60, 0x45800000, v59
	v_cndmask_b32_e32 v60, v59, v60, vcc
	v_pk_mul_f32 v[44:45], v[44:45], v[58:59] op_sel_hi:[1,0]
	v_pk_mul_f32 v[24:25], v[24:25], v[58:59] op_sel_hi:[1,0]
	v_pk_mul_f32 v[48:49], v[48:49], v[58:59] op_sel_hi:[1,0]
	v_pk_mul_f32 v[28:29], v[28:29], v[58:59] op_sel_hi:[1,0]
	v_pk_mul_f32 v[50:51], v[50:51], v[58:59] op_sel_hi:[1,0]
	v_pk_mul_f32 v[62:63], v[26:27], v[58:59] op_sel_hi:[1,0]
	v_pk_mul_f32 v[52:53], v[52:53], v[58:59] op_sel_hi:[1,0]
	v_pk_mul_f32 v[58:59], v[22:23], v[58:59] op_sel_hi:[1,0]
	v_pk_mul_f32 v[54:55], v[54:55], v[60:61] op_sel_hi:[1,0]
	v_pk_mul_f32 v[64:65], v[30:31], v[60:61] op_sel_hi:[1,0]
	v_pk_mul_f32 v[56:57], v[56:57], v[60:61] op_sel_hi:[1,0]
	v_pk_mul_f32 v[66:67], v[36:37], v[60:61] op_sel_hi:[1,0]
	v_pk_mul_f32 v[68:69], v[42:43], v[60:61] op_sel_hi:[1,0]
	v_pk_mul_f32 v[70:71], v[34:35], v[60:61] op_sel_hi:[1,0]
	v_pk_mul_f32 v[72:73], v[46:47], v[60:61] op_sel_hi:[1,0]
	v_pk_mul_f32 v[60:61], v[32:33], v[60:61] op_sel_hi:[1,0]
	v_pk_mul_f32 v[22:23], v[0:1], v[44:45]
	v_pk_mul_f32 v[24:25], v[2:3], v[24:25]
	v_pk_mul_f32 v[26:27], v[4:5], v[48:49]
	v_pk_mul_f32 v[28:29], v[6:7], v[28:29]
	v_pk_mul_f32 v[30:31], v[8:9], v[50:51]
	v_pk_mul_f32 v[32:33], v[10:11], v[62:63]
	v_pk_mul_f32 v[34:35], v[12:13], v[52:53]
	v_pk_mul_f32 v[36:37], v[14:15], v[58:59]
	v_pk_mul_f32 v[42:43], v[0:1], v[54:55]
	v_pk_mul_f32 v[44:45], v[2:3], v[64:65]
	v_pk_mul_f32 v[46:47], v[4:5], v[56:57]
	v_pk_mul_f32 v[48:49], v[6:7], v[66:67]
	v_pk_mul_f32 v[50:51], v[8:9], v[68:69]
	v_pk_mul_f32 v[52:53], v[10:11], v[70:71]
	v_pk_mul_f32 v[54:55], v[12:13], v[72:73]
	v_pk_mul_f32 v[56:57], v[14:15], v[60:61]
	global_store_dwordx4 v[18:19], v[22:25], off offset:-4096
	global_store_dwordx4 v[18:19], v[26:29], off offset:-3072
	global_store_dwordx4 v[18:19], v[30:33], off offset:-2048
	global_store_dwordx4 v[18:19], v[34:37], off offset:-1024
	global_store_dwordx4 v[18:19], v[42:45], off
	global_store_dwordx4 v[18:19], v[46:49], off offset:1024
	global_store_dwordx4 v[18:19], v[50:53], off offset:2048
	global_store_dwordx4 v[18:19], v[54:57], off offset:3072
	v_lshl_add_u64 v[18:19], v[18:19], 0, s[8:9]
	s_cbranch_scc1 .LBB0_2423
